# sec 6.3(2) A/B: hipcc's 128 per-phase s_setprio flips in the 8-phase GEMM loops deleted
# speedup vs baseline: 1.0085x; 1.0085x over previous
.LBB0_545:
	s_add_u32 s34, s30, 0xfffc0080
	s_addc_u32 s35, s31, -1
	s_add_i32 s48, 0, 0x10000
	v_add_u32_e32 v142, s48, v143
	ds_read_b128 v[148:151], v142
	ds_read_b128 v[152:155], v142 offset:1024
	ds_read_b128 v[156:159], v142 offset:2048
	ds_read_b128 v[160:163], v142 offset:3072
	s_cmp_eq_u32 s47, 12
	s_cselect_b32 s37, s25, s35
	s_cselect_b32 s36, s43, s34
	s_cselect_b32 s35, s23, s46
	s_cselect_b32 s34, s44, s45
	v_lshl_add_u64 v[144:145], s[30:31], 0, v[138:139]
	s_add_i32 m0, s9, 0xc000
	ds_read_b128 v[166:169], v165
	ds_read_b128 v[170:173], v165 offset:1024
	ds_read_b128 v[180:183], v165 offset:2048
	ds_read_b128 v[184:187], v165 offset:3072
	ds_read_b128 v[188:191], v165 offset:4096
	ds_read_b128 v[192:195], v165 offset:5120
	ds_read_b128 v[196:199], v165 offset:6144
	ds_read_b128 v[200:203], v165 offset:7168
	global_load_lds_dwordx4 v[144:145], off
	v_lshl_add_u64 v[144:145], s[30:31], 0, v[140:141]
	s_add_i32 m0, s9, 0xe000
	s_nop 0
	global_load_lds_dwordx4 v[144:145], off
	s_waitcnt lgkmcnt(8)
	s_barrier
	s_waitcnt lgkmcnt(0)
	s_waitcnt lgkmcnt(0)
	v_mfma_i32_16x16x64_i8 v[128:131], v[148:151], v[166:169], v[128:131]
	v_mfma_i32_16x16x64_i8 v[124:127], v[156:159], v[166:169], v[124:127]
	v_mfma_i32_16x16x64_i8 v[120:123], v[148:151], v[180:183], v[120:123]
	v_mfma_i32_16x16x64_i8 v[116:119], v[156:159], v[180:183], v[116:119]
	v_mfma_i32_16x16x64_i8 v[112:115], v[148:151], v[188:191], v[112:115]
	v_mfma_i32_16x16x64_i8 v[108:111], v[156:159], v[188:191], v[108:111]
	v_mfma_i32_16x16x64_i8 v[104:107], v[148:151], v[196:199], v[104:107]
	v_mfma_i32_16x16x64_i8 v[100:103], v[156:159], v[196:199], v[100:103]
	v_mfma_i32_16x16x64_i8 v[128:131], v[152:155], v[170:173], v[128:131]
	v_mfma_i32_16x16x64_i8 v[124:127], v[160:163], v[170:173], v[124:127]
	v_mfma_i32_16x16x64_i8 v[120:123], v[152:155], v[184:187], v[120:123]
	v_mfma_i32_16x16x64_i8 v[116:119], v[160:163], v[184:187], v[116:119]
	v_mfma_i32_16x16x64_i8 v[112:115], v[152:155], v[192:195], v[112:115]
	v_mfma_i32_16x16x64_i8 v[108:111], v[160:163], v[192:195], v[108:111]
	v_mfma_i32_16x16x64_i8 v[104:107], v[152:155], v[200:203], v[104:107]
	v_mfma_i32_16x16x64_i8 v[100:103], v[160:163], v[200:203], v[100:103]
	s_barrier
	s_add_i32 s50, 0, 0x14000
	s_add_i32 s48, s48, s8
	v_add_u32_e32 v142, s50, v143
	v_lshl_add_u64 v[144:145], s[34:35], 0, v[98:99]
	s_mov_b32 m0, s48
	ds_read_b128 v[204:207], v142
	ds_read_b128 v[208:211], v142 offset:1024
	ds_read_b128 v[230:233], v142 offset:2048
	ds_read_b128 v[236:239], v142 offset:3072
	global_load_lds_dwordx4 v[144:145], off
	v_lshl_add_u64 v[174:175], s[34:35], 0, v[132:133]
	s_add_i32 m0, s48, 0x2000
	s_nop 0
	global_load_lds_dwordx4 v[174:175], off
	s_barrier
	s_waitcnt lgkmcnt(0)
	s_waitcnt lgkmcnt(0)
	v_mfma_i32_16x16x64_i8 v[94:97], v[204:207], v[166:169], v[94:97]
	v_mfma_i32_16x16x64_i8 v[90:93], v[230:233], v[166:169], v[90:93]
	v_mfma_i32_16x16x64_i8 v[86:89], v[204:207], v[180:183], v[86:89]
	v_mfma_i32_16x16x64_i8 v[82:85], v[230:233], v[180:183], v[82:85]
	v_mfma_i32_16x16x64_i8 v[78:81], v[204:207], v[188:191], v[78:81]
	v_mfma_i32_16x16x64_i8 v[74:77], v[230:233], v[188:191], v[74:77]
	v_mfma_i32_16x16x64_i8 v[70:73], v[204:207], v[196:199], v[70:73]
	v_mfma_i32_16x16x64_i8 v[66:69], v[230:233], v[196:199], v[66:69]
	v_mfma_i32_16x16x64_i8 v[94:97], v[208:211], v[170:173], v[94:97]
	v_mfma_i32_16x16x64_i8 v[90:93], v[236:239], v[170:173], v[90:93]
	v_mfma_i32_16x16x64_i8 v[86:89], v[208:211], v[184:187], v[86:89]
	v_mfma_i32_16x16x64_i8 v[82:85], v[236:239], v[184:187], v[82:85]
	v_mfma_i32_16x16x64_i8 v[78:81], v[208:211], v[192:195], v[78:81]
	v_mfma_i32_16x16x64_i8 v[74:77], v[236:239], v[192:195], v[74:77]
	v_mfma_i32_16x16x64_i8 v[70:73], v[208:211], v[200:203], v[70:73]
	v_mfma_i32_16x16x64_i8 v[66:69], v[236:239], v[200:203], v[66:69]
	s_mov_b32 m0, s9
	v_lshl_add_u64 v[176:177], s[36:37], 0, v[136:137]
	s_barrier
	ds_read_b128 v[166:169], v165 offset:16384
	ds_read_b128 v[170:173], v165 offset:17408
	ds_read_b128 v[180:183], v165 offset:18432
	ds_read_b128 v[184:187], v165 offset:19456
	ds_read_b128 v[188:191], v165 offset:20480
	ds_read_b128 v[192:195], v165 offset:21504
	ds_read_b128 v[196:199], v165 offset:22528
	ds_read_b128 v[200:203], v165 offset:23552
	global_load_lds_dwordx4 v[176:177], off
	v_lshl_add_u64 v[178:179], s[36:37], 0, v[134:135]
	s_mov_b32 m0, s20
	s_nop 0
	global_load_lds_dwordx4 v[178:179], off
	s_barrier
	s_waitcnt lgkmcnt(0)
	s_waitcnt lgkmcnt(0)
	v_mfma_i32_16x16x64_i8 v[62:65], v[148:151], v[166:169], v[62:65]
	v_mfma_i32_16x16x64_i8 v[58:61], v[156:159], v[166:169], v[58:61]
	v_mfma_i32_16x16x64_i8 v[54:57], v[148:151], v[180:183], v[54:57]
	v_mfma_i32_16x16x64_i8 v[50:53], v[156:159], v[180:183], v[50:53]
	v_mfma_i32_16x16x64_i8 v[46:49], v[148:151], v[188:191], v[46:49]
	v_mfma_i32_16x16x64_i8 v[42:45], v[156:159], v[188:191], v[42:45]
	v_mfma_i32_16x16x64_i8 v[38:41], v[148:151], v[196:199], v[38:41]
	v_mfma_i32_16x16x64_i8 v[34:37], v[156:159], v[196:199], v[34:37]
	v_mfma_i32_16x16x64_i8 v[62:65], v[152:155], v[170:173], v[62:65]
	v_mfma_i32_16x16x64_i8 v[58:61], v[160:163], v[170:173], v[58:61]
	v_mfma_i32_16x16x64_i8 v[54:57], v[152:155], v[184:187], v[54:57]
	v_mfma_i32_16x16x64_i8 v[50:53], v[160:163], v[184:187], v[50:53]
	v_mfma_i32_16x16x64_i8 v[46:49], v[152:155], v[192:195], v[46:49]
	v_mfma_i32_16x16x64_i8 v[42:45], v[160:163], v[192:195], v[42:45]
	v_mfma_i32_16x16x64_i8 v[38:41], v[152:155], v[200:203], v[38:41]
	v_mfma_i32_16x16x64_i8 v[34:37], v[160:163], v[200:203], v[34:37]
	s_barrier
	s_add_u32 s48, s34, 0x40000
	s_addc_u32 s49, s35, 0
	s_add_i32 s50, s50, s8
	v_lshl_add_u64 v[148:149], s[48:49], 0, v[98:99]
	s_mov_b32 m0, s50
	s_nop 0
	global_load_lds_dwordx4 v[148:149], off
	v_lshl_add_u64 v[148:149], s[48:49], 0, v[132:133]
	s_add_i32 m0, s50, 0x2000
	s_nop 0
	global_load_lds_dwordx4 v[148:149], off
	s_waitcnt vmcnt(6)
	s_barrier
	v_mfma_i32_16x16x64_i8 v[30:33], v[204:207], v[166:169], v[30:33]
	v_mfma_i32_16x16x64_i8 v[26:29], v[230:233], v[166:169], v[26:29]
	v_mfma_i32_16x16x64_i8 v[22:25], v[204:207], v[180:183], v[22:25]
	v_mfma_i32_16x16x64_i8 v[18:21], v[230:233], v[180:183], v[18:21]
	v_mfma_i32_16x16x64_i8 v[14:17], v[204:207], v[188:191], v[14:17]
	v_mfma_i32_16x16x64_i8 v[10:13], v[230:233], v[188:191], v[10:13]
	v_mfma_i32_16x16x64_i8 v[6:9], v[204:207], v[196:199], v[6:9]
	v_mfma_i32_16x16x64_i8 v[2:5], v[230:233], v[196:199], v[2:5]
	v_mfma_i32_16x16x64_i8 v[30:33], v[208:211], v[170:173], v[30:33]
	v_mfma_i32_16x16x64_i8 v[26:29], v[236:239], v[170:173], v[26:29]
	v_mfma_i32_16x16x64_i8 v[22:25], v[208:211], v[184:187], v[22:25]
	v_mfma_i32_16x16x64_i8 v[18:21], v[236:239], v[184:187], v[18:21]
	v_mfma_i32_16x16x64_i8 v[14:17], v[208:211], v[192:195], v[14:17]
	v_mfma_i32_16x16x64_i8 v[10:13], v[236:239], v[192:195], v[10:13]
	v_mfma_i32_16x16x64_i8 v[6:9], v[208:211], v[200:203], v[6:9]
	v_mfma_i32_16x16x64_i8 v[2:5], v[236:239], v[200:203], v[2:5]
	s_add_i32 s48, 0, 0x18000
	v_add_u32_e32 v142, s48, v143
	s_barrier
	ds_read_b128 v[148:151], v142
	ds_read_b128 v[152:155], v142 offset:1024
	ds_read_b128 v[156:159], v142 offset:2048
	ds_read_b128 v[160:163], v142 offset:3072
	s_add_u32 s36, s36, 0x40000
	s_addc_u32 s37, s37, 0
	s_mov_b32 m0, s21
	v_lshl_add_u64 v[204:205], s[36:37], 0, v[136:137]
	ds_read_b128 v[166:169], v165 offset:32768
	ds_read_b128 v[170:173], v165 offset:33792
	ds_read_b128 v[180:183], v165 offset:34816
	ds_read_b128 v[184:187], v165 offset:35840
	ds_read_b128 v[188:191], v165 offset:36864
	ds_read_b128 v[192:195], v165 offset:37888
	ds_read_b128 v[196:199], v165 offset:38912
	ds_read_b128 v[200:203], v165 offset:39936
	global_load_lds_dwordx4 v[204:205], off
	v_lshl_add_u64 v[204:205], s[36:37], 0, v[134:135]
	s_mov_b32 m0, s33
	s_nop 0
	global_load_lds_dwordx4 v[204:205], off
	s_waitcnt lgkmcnt(8)
	s_barrier
	s_waitcnt lgkmcnt(0)
	s_waitcnt lgkmcnt(0)
	v_mfma_i32_16x16x64_i8 v[128:131], v[148:151], v[166:169], v[128:131]
	v_mfma_i32_16x16x64_i8 v[124:127], v[156:159], v[166:169], v[124:127]
	v_mfma_i32_16x16x64_i8 v[120:123], v[148:151], v[180:183], v[120:123]
	v_mfma_i32_16x16x64_i8 v[116:119], v[156:159], v[180:183], v[116:119]
	v_mfma_i32_16x16x64_i8 v[112:115], v[148:151], v[188:191], v[112:115]
	v_mfma_i32_16x16x64_i8 v[108:111], v[156:159], v[188:191], v[108:111]
	v_mfma_i32_16x16x64_i8 v[104:107], v[148:151], v[196:199], v[104:107]
	v_mfma_i32_16x16x64_i8 v[100:103], v[156:159], v[196:199], v[100:103]
	v_mfma_i32_16x16x64_i8 v[128:131], v[152:155], v[170:173], v[128:131]
	v_mfma_i32_16x16x64_i8 v[124:127], v[160:163], v[170:173], v[124:127]
	v_mfma_i32_16x16x64_i8 v[120:123], v[152:155], v[184:187], v[120:123]
	v_mfma_i32_16x16x64_i8 v[116:119], v[160:163], v[184:187], v[116:119]
	v_mfma_i32_16x16x64_i8 v[112:115], v[152:155], v[192:195], v[112:115]
	v_mfma_i32_16x16x64_i8 v[108:111], v[160:163], v[192:195], v[108:111]
	v_mfma_i32_16x16x64_i8 v[104:107], v[152:155], v[200:203], v[104:107]
	v_mfma_i32_16x16x64_i8 v[100:103], v[160:163], v[200:203], v[100:103]
	s_barrier
	s_add_i32 s36, 0, 0x1c000
	s_add_i32 s37, s48, s8
	v_add_u32_e32 v142, s36, v143
	v_lshl_add_u64 v[144:145], v[144:145], 0, s[68:69]
	s_mov_b32 m0, s37
	ds_read_b128 v[204:207], v142
	ds_read_b128 v[208:211], v142 offset:1024
	ds_read_b128 v[230:233], v142 offset:2048
	ds_read_b128 v[236:239], v142 offset:3072
	global_load_lds_dwordx4 v[144:145], off
	v_lshl_add_u64 v[144:145], v[174:175], 0, s[68:69]
	s_add_i32 m0, s37, 0x2000
	s_nop 0
	global_load_lds_dwordx4 v[144:145], off
	s_barrier
	s_waitcnt lgkmcnt(0)
	s_waitcnt lgkmcnt(0)
	v_mfma_i32_16x16x64_i8 v[94:97], v[204:207], v[166:169], v[94:97]
	v_mfma_i32_16x16x64_i8 v[90:93], v[230:233], v[166:169], v[90:93]
	v_mfma_i32_16x16x64_i8 v[86:89], v[204:207], v[180:183], v[86:89]
	v_mfma_i32_16x16x64_i8 v[82:85], v[230:233], v[180:183], v[82:85]
	v_mfma_i32_16x16x64_i8 v[78:81], v[204:207], v[188:191], v[78:81]
	v_mfma_i32_16x16x64_i8 v[74:77], v[230:233], v[188:191], v[74:77]
	v_mfma_i32_16x16x64_i8 v[70:73], v[204:207], v[196:199], v[70:73]
	v_mfma_i32_16x16x64_i8 v[66:69], v[230:233], v[196:199], v[66:69]
	v_mfma_i32_16x16x64_i8 v[94:97], v[208:211], v[170:173], v[94:97]
	v_mfma_i32_16x16x64_i8 v[90:93], v[236:239], v[170:173], v[90:93]
	v_mfma_i32_16x16x64_i8 v[86:89], v[208:211], v[184:187], v[86:89]
	v_mfma_i32_16x16x64_i8 v[82:85], v[236:239], v[184:187], v[82:85]
	v_mfma_i32_16x16x64_i8 v[78:81], v[208:211], v[192:195], v[78:81]
	v_mfma_i32_16x16x64_i8 v[74:77], v[236:239], v[192:195], v[74:77]
	v_mfma_i32_16x16x64_i8 v[70:73], v[208:211], v[200:203], v[70:73]
	v_mfma_i32_16x16x64_i8 v[66:69], v[236:239], v[200:203], v[66:69]
	s_mov_b32 m0, s38
	v_lshl_add_u64 v[144:145], v[176:177], 0, s[68:69]
	s_barrier
	ds_read_b128 v[166:169], v165 offset:49152
	ds_read_b128 v[170:173], v165 offset:50176
	ds_read_b128 v[180:183], v165 offset:51200
	ds_read_b128 v[184:187], v165 offset:52224
	ds_read_b128 v[188:191], v165 offset:53248
	ds_read_b128 v[192:195], v165 offset:54272
	ds_read_b128 v[196:199], v165 offset:55296
	ds_read_b128 v[200:203], v165 offset:56320
	global_load_lds_dwordx4 v[144:145], off
	v_lshl_add_u64 v[144:145], v[178:179], 0, s[68:69]
	s_mov_b32 m0, s39
	s_nop 0
	global_load_lds_dwordx4 v[144:145], off
	s_barrier
	s_waitcnt lgkmcnt(0)
	s_waitcnt lgkmcnt(0)
	v_mfma_i32_16x16x64_i8 v[62:65], v[148:151], v[166:169], v[62:65]
	v_mfma_i32_16x16x64_i8 v[58:61], v[156:159], v[166:169], v[58:61]
	v_mfma_i32_16x16x64_i8 v[54:57], v[148:151], v[180:183], v[54:57]
	v_mfma_i32_16x16x64_i8 v[50:53], v[156:159], v[180:183], v[50:53]
	v_mfma_i32_16x16x64_i8 v[46:49], v[148:151], v[188:191], v[46:49]
	v_mfma_i32_16x16x64_i8 v[42:45], v[156:159], v[188:191], v[42:45]
	v_mfma_i32_16x16x64_i8 v[38:41], v[148:151], v[196:199], v[38:41]
	v_mfma_i32_16x16x64_i8 v[34:37], v[156:159], v[196:199], v[34:37]
	v_mfma_i32_16x16x64_i8 v[62:65], v[152:155], v[170:173], v[62:65]
	v_mfma_i32_16x16x64_i8 v[58:61], v[160:163], v[170:173], v[58:61]
	v_mfma_i32_16x16x64_i8 v[54:57], v[152:155], v[184:187], v[54:57]
	v_mfma_i32_16x16x64_i8 v[50:53], v[160:163], v[184:187], v[50:53]
	v_mfma_i32_16x16x64_i8 v[46:49], v[152:155], v[192:195], v[46:49]
	v_mfma_i32_16x16x64_i8 v[42:45], v[160:163], v[192:195], v[42:45]
	v_mfma_i32_16x16x64_i8 v[38:41], v[152:155], v[200:203], v[38:41]
	v_mfma_i32_16x16x64_i8 v[34:37], v[160:163], v[200:203], v[34:37]
	s_barrier
	s_add_u32 s34, s34, 0x40080
	s_addc_u32 s35, s35, 0
	s_add_i32 s36, s36, s8
	v_lshl_add_u64 v[144:145], s[34:35], 0, v[98:99]
	s_mov_b32 m0, s36
	s_nop 0
	global_load_lds_dwordx4 v[144:145], off
	v_lshl_add_u64 v[144:145], s[34:35], 0, v[132:133]
	s_add_i32 m0, s36, 0x2000
	s_nop 0
	global_load_lds_dwordx4 v[144:145], off
	s_waitcnt vmcnt(6)
	s_barrier
	v_mfma_i32_16x16x64_i8 v[30:33], v[204:207], v[166:169], v[30:33]
	v_mfma_i32_16x16x64_i8 v[26:29], v[230:233], v[166:169], v[26:29]
	v_mfma_i32_16x16x64_i8 v[22:25], v[204:207], v[180:183], v[22:25]
	v_mfma_i32_16x16x64_i8 v[18:21], v[230:233], v[180:183], v[18:21]
	v_mfma_i32_16x16x64_i8 v[14:17], v[204:207], v[188:191], v[14:17]
	v_mfma_i32_16x16x64_i8 v[10:13], v[230:233], v[188:191], v[10:13]
	v_mfma_i32_16x16x64_i8 v[6:9], v[204:207], v[196:199], v[6:9]
	v_mfma_i32_16x16x64_i8 v[2:5], v[230:233], v[196:199], v[2:5]
	v_mfma_i32_16x16x64_i8 v[30:33], v[208:211], v[170:173], v[30:33]
	v_mfma_i32_16x16x64_i8 v[26:29], v[236:239], v[170:173], v[26:29]
	v_mfma_i32_16x16x64_i8 v[22:25], v[208:211], v[184:187], v[22:25]
	v_mfma_i32_16x16x64_i8 v[18:21], v[236:239], v[184:187], v[18:21]
	v_mfma_i32_16x16x64_i8 v[14:17], v[208:211], v[192:195], v[14:17]
	v_mfma_i32_16x16x64_i8 v[10:13], v[236:239], v[192:195], v[10:13]
	v_mfma_i32_16x16x64_i8 v[6:9], v[208:211], v[200:203], v[6:9]
	v_mfma_i32_16x16x64_i8 v[2:5], v[236:239], v[200:203], v[2:5]
	s_add_i32 s47, s47, 2
	s_add_u32 s30, s30, 0x100
	s_addc_u32 s31, s31, 0
	s_add_u32 s45, s45, 0x100
	s_addc_u32 s46, s46, 0
	s_cmp_gt_u32 s47, 13
	s_barrier
	s_cbranch_scc0 .LBB0_545
	v_lshl_add_u32 v144, s42, 8, v1
	v_or_b32_e32 v182, 16, v144
	v_ashrrev_i32_e32 v145, 31, v144
	v_ashrrev_i32_e32 v183, 31, v182
	v_or_b32_e32 v174, 32, v144
	v_lshl_add_u64 v[148:149], v[144:145], 2, s[54:55]
	v_lshl_add_u64 v[150:151], v[182:183], 2, s[54:55]
	v_ashrrev_i32_e32 v175, 31, v174
	v_or_b32_e32 v170, 48, v144
	v_lshl_or_b32 v186, s41, 8, v147
	global_load_dword v184, v[148:149], off
	global_load_dword v180, v[150:151], off
	v_lshl_add_u64 v[150:151], v[174:175], 2, s[54:55]
	v_ashrrev_i32_e32 v171, 31, v170
	v_ashrrev_i32_e32 v187, 31, v186
	global_load_dword v172, v[150:151], off
	v_lshl_add_u64 v[150:151], v[170:171], 2, s[54:55]
	v_lshl_add_u64 v[158:159], v[186:187], 2, s[18:19]
	global_load_dword v168, v[150:151], off
	global_load_dword v166, v[148:149], off offset:512
	global_load_dword v164, v[148:149], off offset:576
	global_load_dword v146, v[148:149], off offset:640
	global_load_dword v142, v[148:149], off offset:704
	global_load_dwordx4 v[154:157], v[158:159], off offset:16
	global_load_dwordx4 v[150:153], v[158:159], off
	global_load_dwordx4 v[188:191], v[158:159], off offset:528
	s_nop 0
	global_load_dwordx4 v[158:161], v[158:159], off offset:512
	v_cvt_f32_i32_e32 v129, v129
	v_cvt_f32_i32_e32 v128, v128
	v_cvt_f32_i32_e32 v127, v127
	v_cvt_f32_i32_e32 v126, v126
	v_cvt_f32_i32_e32 v131, v131
	v_cvt_f32_i32_e32 v130, v130
	v_readlane_b32 s30, v252, 59
	v_cvt_f32_i32_e32 v177, v125
	v_cvt_f32_i32_e32 v176, v124
	v_readlane_b32 s31, v252, 60
	v_cvt_f32_i32_e32 v97, v97
	v_cvt_f32_i32_e32 v96, v96
	v_cvt_f32_i32_e32 v179, v95
	v_cvt_f32_i32_e32 v178, v94
	v_cvt_f32_i32_e32 v95, v93
	v_cvt_f32_i32_e32 v94, v92
	v_cvt_f32_i32_e32 v93, v79
	v_cvt_f32_i32_e32 v92, v78
	v_cvt_f32_i32_e32 v79, v77
	v_cvt_f32_i32_e32 v78, v76
	v_cvt_f32_i32_e32 v77, v71
	v_cvt_f32_i32_e32 v76, v70
	v_cvt_f32_i32_e32 v71, v69
	v_cvt_f32_i32_e32 v70, v68
	v_cvt_f32_i32_e32 v69, v63
	v_cvt_f32_i32_e32 v68, v62
	v_cvt_f32_i32_e32 v63, v59
	v_cvt_f32_i32_e32 v62, v58
	v_cvt_f32_i32_e32 v59, v27
	v_cvt_f32_i32_e32 v58, v26
	v_cvt_f32_i32_e32 v27, v19
	v_cvt_f32_i32_e32 v26, v18
	v_cvt_f32_i32_e32 v19, v11
	v_cvt_f32_i32_e32 v18, v10
	v_mov_b64_e32 v[10:11], s[30:31]
	s_movk_i32 s23, 0x3200
	v_cvt_f32_i32_e32 v125, v91
	v_cvt_f32_i32_e32 v124, v90
	v_cvt_f32_i32_e32 v91, v75
	v_cvt_f32_i32_e32 v90, v74
	v_cvt_f32_i32_e32 v75, v67
	v_cvt_f32_i32_e32 v74, v66
	v_cvt_f32_i32_e32 v67, v31
	v_cvt_f32_i32_e32 v66, v30
	v_cvt_f32_i32_e32 v31, v29
	v_cvt_f32_i32_e32 v30, v28
	v_cvt_f32_i32_e32 v29, v23
	v_cvt_f32_i32_e32 v28, v22
	v_cvt_f32_i32_e32 v23, v21
	v_cvt_f32_i32_e32 v22, v20
	v_cvt_f32_i32_e32 v21, v15
	v_cvt_f32_i32_e32 v20, v14
	v_cvt_f32_i32_e32 v15, v13
	v_cvt_f32_i32_e32 v14, v12
	v_lshlrev_b64 v[12:13], 1, v[186:187]
	v_cvt_f32_i32_e32 v121, v121
	v_cvt_f32_i32_e32 v120, v120
	v_cvt_f32_i32_e32 v123, v123
	v_cvt_f32_i32_e32 v122, v122
	v_cvt_f32_i32_e32 v119, v119
	v_cvt_f32_i32_e32 v118, v118
	v_cvt_f32_i32_e32 v117, v117
	v_cvt_f32_i32_e32 v116, v116
	v_cvt_f32_i32_e32 v89, v89
	v_cvt_f32_i32_e32 v88, v88
	v_cvt_f32_i32_e32 v87, v87
	v_cvt_f32_i32_e32 v86, v86
	v_cvt_f32_i32_e32 v85, v85
	s_waitcnt vmcnt(0)
	v_pk_mul_f32 v[128:129], v[184:185], v[128:129] op_sel_hi:[0,1]
	v_pk_mul_f32 v[126:127], v[184:185], v[126:127] op_sel_hi:[0,1]
	v_pk_mul_f32 v[130:131], v[184:185], v[130:131] op_sel_hi:[0,1]
	v_pk_mul_f32 v[176:177], v[184:185], v[176:177] op_sel_hi:[0,1]
	v_pk_mul_f32 v[96:97], v[184:185], v[96:97] op_sel_hi:[0,1]
	v_pk_mul_f32 v[94:95], v[184:185], v[94:95] op_sel_hi:[0,1]
	v_cvt_f32_i32_e32 v84, v84
	v_cvt_f32_i32_e32 v83, v83
	v_cvt_f32_i32_e32 v82, v82
	v_pk_mul_f32 v[154:155], v[154:155], s[58:59] op_sel_hi:[1,0]
	v_pk_mul_f32 v[148:149], v[152:153], s[58:59] op_sel_hi:[1,0]
	v_pk_mul_f32 v[150:151], v[150:151], s[58:59] op_sel_hi:[1,0]
	v_pk_mul_f32 v[152:153], v[156:157], s[58:59] op_sel_hi:[1,0]
	v_pk_mul_f32 v[162:163], v[188:189], s[58:59] op_sel_hi:[1,0]
	v_mad_i64_i32 v[188:189], s[30:31], v144, s23, v[10:11]
	v_lshl_add_u64 v[186:187], v[188:189], 0, v[12:13]
	v_pk_mul_f32 v[188:189], v[152:153], v[126:127]
	v_pk_mul_f32 v[126:127], v[150:151], v[128:129]
	v_pk_mul_f32 v[130:131], v[148:149], v[130:131]
	v_cvt_pk_bf16_f32 v126, v126, v127
	v_pk_mul_f32 v[156:157], v[160:161], s[58:59] op_sel_hi:[1,0]
	v_cvt_pk_bf16_f32 v127, v130, v131
	v_pk_mul_f32 v[158:159], v[158:159], s[58:59] op_sel_hi:[1,0]
	v_pk_mul_f32 v[160:161], v[190:191], s[58:59] op_sel_hi:[1,0]
	v_pk_mul_f32 v[176:177], v[154:155], v[176:177]
	v_pk_mul_f32 v[124:125], v[184:185], v[124:125] op_sel_hi:[0,1]
	v_cvt_pk_bf16_f32 v128, v176, v177
	v_cvt_pk_bf16_f32 v129, v188, v189
	global_store_dwordx4 v[186:187], v[126:129], off
	v_pk_mul_f32 v[96:97], v[156:157], v[96:97]
	v_pk_mul_f32 v[124:125], v[162:163], v[124:125]
	v_pk_mul_f32 v[126:127], v[184:185], v[178:179] op_sel_hi:[0,1]
	v_pk_mul_f32 v[126:127], v[158:159], v[126:127]
	v_pk_mul_f32 v[128:129], v[160:161], v[94:95]
	v_cvt_pk_bf16_f32 v94, v126, v127
	v_cvt_pk_bf16_f32 v95, v96, v97
	v_cvt_pk_bf16_f32 v96, v124, v125
	v_cvt_f32_i32_e32 v113, v113
	v_cvt_pk_bf16_f32 v97, v128, v129
	global_store_dwordx4 v[186:187], v[94:97], off offset:256
	v_cvt_f32_i32_e32 v112, v112
	v_cvt_f32_i32_e32 v115, v115
	v_mad_i64_i32 v[94:95], s[30:31], v182, s23, v[10:11]
	v_lshl_add_u64 v[124:125], v[94:95], 0, v[12:13]
	v_pk_mul_f32 v[94:95], v[180:181], v[120:121] op_sel_hi:[0,1]
	v_pk_mul_f32 v[96:97], v[180:181], v[122:123] op_sel_hi:[0,1]
	v_pk_mul_f32 v[94:95], v[150:151], v[94:95]
	v_cvt_f32_i32_e32 v114, v114
	v_pk_mul_f32 v[116:117], v[180:181], v[116:117] op_sel_hi:[0,1]
	v_pk_mul_f32 v[118:119], v[180:181], v[118:119] op_sel_hi:[0,1]
	v_pk_mul_f32 v[96:97], v[148:149], v[96:97]
	v_cvt_pk_bf16_f32 v94, v94, v95
	v_pk_mul_f32 v[86:87], v[180:181], v[86:87] op_sel_hi:[0,1]
	v_cvt_pk_bf16_f32 v95, v96, v97
	v_pk_mul_f32 v[88:89], v[180:181], v[88:89] op_sel_hi:[0,1]
	v_pk_mul_f32 v[82:83], v[180:181], v[82:83] op_sel_hi:[0,1]
	v_pk_mul_f32 v[84:85], v[180:181], v[84:85] op_sel_hi:[0,1]
	v_cvt_f32_i32_e32 v111, v111
	v_cvt_f32_i32_e32 v110, v110
	v_cvt_f32_i32_e32 v109, v109
	v_cvt_f32_i32_e32 v108, v108
	v_pk_mul_f32 v[118:119], v[152:153], v[118:119]
	v_pk_mul_f32 v[116:117], v[154:155], v[116:117]
	v_pk_mul_f32 v[88:89], v[156:157], v[88:89]
	v_cvt_pk_bf16_f32 v96, v116, v117
	v_cvt_pk_bf16_f32 v97, v118, v119
	global_store_dwordx4 v[124:125], v[94:97], off
	v_pk_mul_f32 v[86:87], v[158:159], v[86:87]
	v_cvt_f32_i32_e32 v81, v81
	v_pk_mul_f32 v[94:95], v[160:161], v[84:85]
	v_pk_mul_f32 v[84:85], v[162:163], v[82:83]
	v_cvt_pk_bf16_f32 v82, v86, v87
	v_cvt_pk_bf16_f32 v83, v88, v89
	v_cvt_f32_i32_e32 v80, v80
	v_cvt_pk_bf16_f32 v84, v84, v85
	v_cvt_pk_bf16_f32 v85, v94, v95
	global_store_dwordx4 v[124:125], v[82:85], off offset:256
	v_cvt_f32_i32_e32 v105, v105
	v_cvt_f32_i32_e32 v104, v104
	v_mad_i64_i32 v[82:83], s[30:31], v174, s23, v[10:11]
	v_lshl_add_u64 v[86:87], v[82:83], 0, v[12:13]
	v_pk_mul_f32 v[82:83], v[172:173], v[112:113] op_sel_hi:[0,1]
	v_pk_mul_f32 v[84:85], v[172:173], v[114:115] op_sel_hi:[0,1]
	v_pk_mul_f32 v[82:83], v[150:151], v[82:83]
	v_pk_mul_f32 v[88:89], v[172:173], v[108:109] op_sel_hi:[0,1]
	v_pk_mul_f32 v[94:95], v[172:173], v[110:111] op_sel_hi:[0,1]
	v_pk_mul_f32 v[84:85], v[148:149], v[84:85]
	v_cvt_pk_bf16_f32 v82, v82, v83
	v_cvt_f32_i32_e32 v107, v107
	v_cvt_pk_bf16_f32 v83, v84, v85
	v_cvt_f32_i32_e32 v106, v106
	v_cvt_f32_i32_e32 v73, v73
	v_cvt_f32_i32_e32 v72, v72
	v_pk_mul_f32 v[94:95], v[152:153], v[94:95]
	v_pk_mul_f32 v[88:89], v[154:155], v[88:89]
	v_pk_mul_f32 v[80:81], v[172:173], v[80:81] op_sel_hi:[0,1]
	v_cvt_pk_bf16_f32 v84, v88, v89
	v_cvt_pk_bf16_f32 v85, v94, v95
	global_store_dwordx4 v[86:87], v[82:85], off
	v_pk_mul_f32 v[78:79], v[172:173], v[78:79] op_sel_hi:[0,1]
	v_cvt_f32_i32_e32 v103, v103
	v_pk_mul_f32 v[82:83], v[172:173], v[92:93] op_sel_hi:[0,1]
	v_cvt_f32_i32_e32 v102, v102
	v_cvt_f32_i32_e32 v101, v101
	v_cvt_f32_i32_e32 v100, v100
	v_pk_mul_f32 v[84:85], v[172:173], v[90:91] op_sel_hi:[0,1]
	v_pk_mul_f32 v[80:81], v[156:157], v[80:81]
	v_pk_mul_f32 v[82:83], v[158:159], v[82:83]
	v_pk_mul_f32 v[88:89], v[160:161], v[78:79]
	v_cvt_pk_bf16_f32 v78, v82, v83
	v_cvt_pk_bf16_f32 v79, v80, v81
	v_cvt_f32_i32_e32 v61, v61
	v_cvt_f32_i32_e32 v60, v60
	v_pk_mul_f32 v[84:85], v[162:163], v[84:85]
	v_cvt_f32_i32_e32 v65, v65
	v_cvt_pk_bf16_f32 v80, v84, v85
	v_cvt_pk_bf16_f32 v81, v88, v89
	global_store_dwordx4 v[86:87], v[78:81], off offset:256
	v_cvt_f32_i32_e32 v64, v64
	v_pk_mul_f32 v[72:73], v[168:169], v[72:73] op_sel_hi:[0,1]
	v_mad_i64_i32 v[78:79], s[30:31], v170, s23, v[10:11]
	v_lshl_add_u64 v[82:83], v[78:79], 0, v[12:13]
	v_pk_mul_f32 v[78:79], v[168:169], v[104:105] op_sel_hi:[0,1]
	v_pk_mul_f32 v[80:81], v[168:169], v[106:107] op_sel_hi:[0,1]
	v_pk_mul_f32 v[78:79], v[150:151], v[78:79]
	v_cvt_f32_i32_e32 v33, v33
	v_cvt_f32_i32_e32 v32, v32
	v_pk_mul_f32 v[84:85], v[168:169], v[100:101] op_sel_hi:[0,1]
	v_pk_mul_f32 v[86:87], v[168:169], v[102:103] op_sel_hi:[0,1]
	v_pk_mul_f32 v[80:81], v[148:149], v[80:81]
	v_cvt_pk_bf16_f32 v78, v78, v79
	v_pk_mul_f32 v[76:77], v[168:169], v[76:77] op_sel_hi:[0,1]
	v_cvt_pk_bf16_f32 v79, v80, v81
	v_pk_mul_f32 v[74:75], v[168:169], v[74:75] op_sel_hi:[0,1]
	v_pk_mul_f32 v[70:71], v[168:169], v[70:71] op_sel_hi:[0,1]
	v_pk_mul_f32 v[72:73], v[156:157], v[72:73]
	v_add_u32_e32 v145, 0x80, v144
	v_pk_mul_f32 v[86:87], v[152:153], v[86:87]
	v_pk_mul_f32 v[84:85], v[154:155], v[84:85]
	v_pk_mul_f32 v[76:77], v[158:159], v[76:77]
	v_cvt_pk_bf16_f32 v80, v84, v85
	v_cvt_pk_bf16_f32 v81, v86, v87
	global_store_dwordx4 v[82:83], v[78:81], off
	v_pk_mul_f32 v[74:75], v[162:163], v[74:75]
	v_pk_mul_f32 v[68:69], v[166:167], v[68:69] op_sel_hi:[0,1]
	v_pk_mul_f32 v[78:79], v[160:161], v[70:71]
	v_cvt_pk_bf16_f32 v70, v76, v77
	v_cvt_pk_bf16_f32 v71, v72, v73
	v_cvt_pk_bf16_f32 v72, v74, v75
	v_pk_mul_f32 v[60:61], v[166:167], v[60:61] op_sel_hi:[0,1]
	v_cvt_pk_bf16_f32 v73, v78, v79
	global_store_dwordx4 v[82:83], v[70:73], off offset:256
	v_pk_mul_f32 v[64:65], v[166:167], v[64:65] op_sel_hi:[0,1]
	v_pk_mul_f32 v[62:63], v[166:167], v[62:63] op_sel_hi:[0,1]
	v_mad_i64_i32 v[70:71], s[30:31], v145, s23, v[10:11]
	v_pk_mul_f32 v[72:73], v[152:153], v[60:61]
	v_pk_mul_f32 v[60:61], v[150:151], v[68:69]
	v_lshl_add_u64 v[70:71], v[70:71], 0, v[12:13]
	v_pk_mul_f32 v[62:63], v[154:155], v[62:63]
	v_pk_mul_f32 v[64:65], v[148:149], v[64:65]
	v_cvt_pk_bf16_f32 v60, v60, v61
	v_cvt_f32_i32_e32 v55, v55
	v_cvt_pk_bf16_f32 v61, v64, v65
	v_cvt_f32_i32_e32 v54, v54
	v_cvt_pk_bf16_f32 v62, v62, v63
	v_cvt_pk_bf16_f32 v63, v72, v73
	global_store_dwordx4 v[70:71], v[60:63], off
	v_pk_mul_f32 v[32:33], v[166:167], v[32:33] op_sel_hi:[0,1]
	v_pk_mul_f32 v[30:31], v[166:167], v[30:31] op_sel_hi:[0,1]
	v_pk_mul_f32 v[60:61], v[166:167], v[66:67] op_sel_hi:[0,1]
	v_cvt_f32_i32_e32 v57, v57
	v_cvt_f32_i32_e32 v56, v56
	v_pk_mul_f32 v[58:59], v[166:167], v[58:59] op_sel_hi:[0,1]
	v_pk_mul_f32 v[32:33], v[156:157], v[32:33]
	v_pk_mul_f32 v[60:61], v[158:159], v[60:61]
	v_pk_mul_f32 v[62:63], v[160:161], v[30:31]
	v_cvt_pk_bf16_f32 v30, v60, v61
	v_cvt_f32_i32_e32 v53, v53
	v_cvt_f32_i32_e32 v52, v52
	v_cvt_f32_i32_e32 v51, v51
	v_cvt_f32_i32_e32 v50, v50
	v_cvt_f32_i32_e32 v25, v25
	v_cvt_f32_i32_e32 v24, v24
	v_pk_mul_f32 v[58:59], v[162:163], v[58:59]
	v_cvt_pk_bf16_f32 v31, v32, v33
	v_cvt_f32_i32_e32 v47, v47
	v_cvt_pk_bf16_f32 v32, v58, v59
	v_cvt_pk_bf16_f32 v33, v62, v63
	global_store_dwordx4 v[70:71], v[30:33], off offset:256
	v_cvt_f32_i32_e32 v46, v46
	v_pk_mul_f32 v[50:51], v[164:165], v[50:51] op_sel_hi:[0,1]
	v_add_u32_e32 v30, 0x90, v144
	v_mad_i64_i32 v[30:31], s[30:31], v30, s23, v[10:11]
	v_lshl_add_u64 v[58:59], v[30:31], 0, v[12:13]
	v_pk_mul_f32 v[30:31], v[164:165], v[54:55] op_sel_hi:[0,1]
	v_pk_mul_f32 v[32:33], v[164:165], v[56:57] op_sel_hi:[0,1]
	v_pk_mul_f32 v[30:31], v[150:151], v[30:31]
	v_pk_mul_f32 v[52:53], v[164:165], v[52:53] op_sel_hi:[0,1]
	v_pk_mul_f32 v[32:33], v[148:149], v[32:33]
	v_cvt_pk_bf16_f32 v30, v30, v31
	v_pk_mul_f32 v[28:29], v[164:165], v[28:29] op_sel_hi:[0,1]
	v_cvt_pk_bf16_f32 v31, v32, v33
	v_pk_mul_f32 v[24:25], v[164:165], v[24:25] op_sel_hi:[0,1]
	v_pk_mul_f32 v[22:23], v[164:165], v[22:23] op_sel_hi:[0,1]
	v_cvt_f32_i32_e32 v49, v49
	v_cvt_f32_i32_e32 v48, v48
	v_pk_mul_f32 v[52:53], v[152:153], v[52:53]
	v_pk_mul_f32 v[50:51], v[154:155], v[50:51]
	v_pk_mul_f32 v[26:27], v[164:165], v[26:27] op_sel_hi:[0,1]
	v_cvt_pk_bf16_f32 v32, v50, v51
	v_cvt_pk_bf16_f32 v33, v52, v53
	global_store_dwordx4 v[58:59], v[30:33], off
	v_pk_mul_f32 v[24:25], v[156:157], v[24:25]
	v_pk_mul_f32 v[28:29], v[158:159], v[28:29]
	v_pk_mul_f32 v[30:31], v[160:161], v[22:23]
	v_cvt_pk_bf16_f32 v22, v28, v29
	v_cvt_f32_i32_e32 v45, v45
	v_cvt_f32_i32_e32 v44, v44
	v_cvt_f32_i32_e32 v43, v43
	v_cvt_f32_i32_e32 v42, v42
	v_cvt_f32_i32_e32 v17, v17
	v_cvt_f32_i32_e32 v16, v16
	v_pk_mul_f32 v[26:27], v[162:163], v[26:27]
	v_cvt_pk_bf16_f32 v23, v24, v25
	v_cvt_f32_i32_e32 v39, v39
	v_cvt_pk_bf16_f32 v24, v26, v27
	v_cvt_pk_bf16_f32 v25, v30, v31
	global_store_dwordx4 v[58:59], v[22:25], off offset:256
	v_cvt_f32_i32_e32 v38, v38
	v_pk_mul_f32 v[28:29], v[146:147], v[42:43] op_sel_hi:[0,1]
	v_add_u32_e32 v22, 0xa0, v144
	v_mad_i64_i32 v[22:23], s[30:31], v22, s23, v[10:11]
	v_lshl_add_u64 v[26:27], v[22:23], 0, v[12:13]
	v_pk_mul_f32 v[22:23], v[146:147], v[46:47] op_sel_hi:[0,1]
	v_pk_mul_f32 v[24:25], v[146:147], v[48:49] op_sel_hi:[0,1]
	v_pk_mul_f32 v[22:23], v[150:151], v[22:23]
	v_pk_mul_f32 v[30:31], v[146:147], v[44:45] op_sel_hi:[0,1]
	v_pk_mul_f32 v[24:25], v[148:149], v[24:25]
	v_cvt_pk_bf16_f32 v22, v22, v23
	v_pk_mul_f32 v[20:21], v[146:147], v[20:21] op_sel_hi:[0,1]
	v_cvt_pk_bf16_f32 v23, v24, v25
	v_pk_mul_f32 v[16:17], v[146:147], v[16:17] op_sel_hi:[0,1]
	v_pk_mul_f32 v[14:15], v[146:147], v[14:15] op_sel_hi:[0,1]
	v_cvt_f32_i32_e32 v41, v41
	v_cvt_f32_i32_e32 v40, v40
	v_pk_mul_f32 v[30:31], v[152:153], v[30:31]
	v_pk_mul_f32 v[28:29], v[154:155], v[28:29]
	v_pk_mul_f32 v[18:19], v[146:147], v[18:19] op_sel_hi:[0,1]
	v_cvt_pk_bf16_f32 v24, v28, v29
	v_cvt_pk_bf16_f32 v25, v30, v31
	global_store_dwordx4 v[26:27], v[22:25], off
	v_pk_mul_f32 v[16:17], v[156:157], v[16:17]
	v_pk_mul_f32 v[20:21], v[158:159], v[20:21]
	v_pk_mul_f32 v[22:23], v[160:161], v[14:15]
	v_cvt_pk_bf16_f32 v14, v20, v21
	v_cvt_f32_i32_e32 v37, v37
	v_cvt_f32_i32_e32 v36, v36
	v_cvt_f32_i32_e32 v35, v35
	v_cvt_f32_i32_e32 v34, v34
	v_cvt_f32_i32_e32 v5, v5
	v_cvt_f32_i32_e32 v4, v4
	v_cvt_f32_i32_e32 v3, v3
	v_cvt_f32_i32_e32 v2, v2
	v_pk_mul_f32 v[18:19], v[162:163], v[18:19]
	v_cvt_pk_bf16_f32 v15, v16, v17
	v_cvt_f32_i32_e32 v9, v9
	v_cvt_pk_bf16_f32 v16, v18, v19
	v_cvt_pk_bf16_f32 v17, v22, v23
	global_store_dwordx4 v[26:27], v[14:17], off offset:256
	v_cvt_f32_i32_e32 v8, v8
	v_cvt_f32_i32_e32 v7, v7
	v_add_u32_e32 v14, 0xb0, v144
	v_cvt_f32_i32_e32 v6, v6
	v_mad_i64_i32 v[10:11], s[30:31], v14, s23, v[10:11]
	v_lshl_add_u64 v[14:15], v[10:11], 0, v[12:13]
	v_pk_mul_f32 v[10:11], v[142:143], v[38:39] op_sel_hi:[0,1]
	v_pk_mul_f32 v[12:13], v[142:143], v[40:41] op_sel_hi:[0,1]
	v_pk_mul_f32 v[10:11], v[150:151], v[10:11]
	v_pk_mul_f32 v[16:17], v[142:143], v[34:35] op_sel_hi:[0,1]
	v_pk_mul_f32 v[18:19], v[142:143], v[36:37] op_sel_hi:[0,1]
	v_pk_mul_f32 v[12:13], v[148:149], v[12:13]
	v_cvt_pk_bf16_f32 v10, v10, v11
	v_pk_mul_f32 v[2:3], v[142:143], v[2:3] op_sel_hi:[0,1]
	v_cvt_pk_bf16_f32 v11, v12, v13
	v_pk_mul_f32 v[4:5], v[142:143], v[4:5] op_sel_hi:[0,1]
	v_pk_mul_f32 v[18:19], v[152:153], v[18:19]
	v_pk_mul_f32 v[16:17], v[154:155], v[16:17]
	v_pk_mul_f32 v[6:7], v[142:143], v[6:7] op_sel_hi:[0,1]
	v_cvt_pk_bf16_f32 v12, v16, v17
	v_cvt_pk_bf16_f32 v13, v18, v19
	global_store_dwordx4 v[14:15], v[10:13], off
	v_pk_mul_f32 v[8:9], v[142:143], v[8:9] op_sel_hi:[0,1]
	s_and_b64 vcc, exec, s[0:1]
	v_pk_mul_f32 v[10:11], v[160:161], v[4:5]
	v_pk_mul_f32 v[4:5], v[162:163], v[2:3]
	s_mov_b32 s42, s24
	s_mov_b32 s41, s22
	s_mov_b64 s[34:35], s[28:29]
	s_mov_b64 s[30:31], s[26:27]
	v_pk_mul_f32 v[8:9], v[156:157], v[8:9]
	v_pk_mul_f32 v[6:7], v[158:159], v[6:7]
	s_nop 0
	v_cvt_pk_bf16_f32 v2, v6, v7
	v_cvt_pk_bf16_f32 v3, v8, v9
	v_cvt_pk_bf16_f32 v4, v4, v5
	v_cvt_pk_bf16_f32 v5, v10, v11
	global_store_dwordx4 v[14:15], v[2:5], off offset:256
	s_cbranch_vccz .LBB0_538
	s_waitcnt vmcnt(0)
	s_cmpk_gt_u32 s3, 0xff
	s_cbranch_scc1 .LBB0_549
	s_barrier

.LBB0_690:
	s_add_u32 s26, s24, 0x100
	s_addc_u32 s27, s25, 0
	s_add_i32 s45, 0, 0x10000
	v_add_u32_e32 v142, s45, v143
	ds_read_b128 v[146:149], v142
	ds_read_b128 v[152:155], v142 offset:1024
	ds_read_b128 v[156:159], v142 offset:2048
	ds_read_b128 v[160:163], v142 offset:3072
	s_cmp_eq_u32 s44, 6
	s_cselect_b32 s31, s19, s27
	s_cselect_b32 s30, s18, s26
	s_cselect_b32 s29, s23, s43
	s_cselect_b32 s28, s22, s42
	v_lshl_add_u64 v[176:177], s[24:25], 0, v[138:139]
	s_add_i32 m0, s9, 0xc000
	ds_read_b128 v[164:167], v151
	ds_read_b128 v[168:171], v151 offset:1024
	ds_read_b128 v[172:175], v151 offset:2048
	ds_read_b128 v[180:183], v151 offset:3072
	ds_read_b128 v[184:187], v151 offset:4096
	ds_read_b128 v[188:191], v151 offset:5120
	ds_read_b128 v[192:195], v151 offset:6144
	ds_read_b128 v[196:199], v151 offset:7168
	global_load_lds_dwordx4 v[176:177], off
	v_lshl_add_u64 v[176:177], s[24:25], 0, v[140:141]
	s_add_i32 m0, s9, 0xe000
	s_nop 0
	global_load_lds_dwordx4 v[176:177], off
	s_waitcnt lgkmcnt(8)
	s_barrier
	s_waitcnt lgkmcnt(0)
	s_waitcnt lgkmcnt(0)
	v_mfma_f32_16x16x32_bf16 v[128:131], v[146:149], v[164:167], v[128:131]
	v_mfma_f32_16x16x32_bf16 v[124:127], v[156:159], v[164:167], v[124:127]
	v_mfma_f32_16x16x32_bf16 v[112:115], v[146:149], v[172:175], v[112:115]
	v_mfma_f32_16x16x32_bf16 v[108:111], v[156:159], v[172:175], v[108:111]
	v_mfma_f32_16x16x32_bf16 v[94:97], v[146:149], v[184:187], v[94:97]
	v_mfma_f32_16x16x32_bf16 v[90:93], v[156:159], v[184:187], v[90:93]
	v_mfma_f32_16x16x32_bf16 v[78:81], v[146:149], v[192:195], v[78:81]
	v_mfma_f32_16x16x32_bf16 v[74:77], v[156:159], v[192:195], v[74:77]
	v_mfma_f32_16x16x32_bf16 v[128:131], v[152:155], v[168:171], v[128:131]
	v_mfma_f32_16x16x32_bf16 v[124:127], v[160:163], v[168:171], v[124:127]
	v_mfma_f32_16x16x32_bf16 v[112:115], v[152:155], v[180:183], v[112:115]
	v_mfma_f32_16x16x32_bf16 v[108:111], v[160:163], v[180:183], v[108:111]
	v_mfma_f32_16x16x32_bf16 v[94:97], v[152:155], v[188:191], v[94:97]
	v_mfma_f32_16x16x32_bf16 v[90:93], v[160:163], v[188:191], v[90:93]
	v_mfma_f32_16x16x32_bf16 v[78:81], v[152:155], v[196:199], v[78:81]
	v_mfma_f32_16x16x32_bf16 v[74:77], v[160:163], v[196:199], v[74:77]
	s_barrier
	s_add_i32 s46, 0, 0x14000
	s_add_i32 s24, s45, s8
	v_add_u32_e32 v142, s46, v143
	v_lshl_add_u64 v[176:177], s[28:29], 0, v[98:99]
	s_mov_b32 m0, s24
	ds_read_b128 v[200:203], v142
	ds_read_b128 v[204:207], v142 offset:1024
	ds_read_b128 v[208:211], v142 offset:2048
	ds_read_b128 v[230:233], v142 offset:3072
	global_load_lds_dwordx4 v[176:177], off
	v_lshl_add_u64 v[178:179], s[28:29], 0, v[132:133]
	s_add_i32 m0, s24, 0x2000
	s_nop 0
	global_load_lds_dwordx4 v[178:179], off
	s_barrier
	s_waitcnt lgkmcnt(0)
	s_waitcnt lgkmcnt(0)
	v_mfma_f32_16x16x32_bf16 v[120:123], v[200:203], v[164:167], v[120:123]
	v_mfma_f32_16x16x32_bf16 v[116:119], v[208:211], v[164:167], v[116:119]
	v_mfma_f32_16x16x32_bf16 v[104:107], v[200:203], v[172:175], v[104:107]
	v_mfma_f32_16x16x32_bf16 v[100:103], v[208:211], v[172:175], v[100:103]
	v_mfma_f32_16x16x32_bf16 v[86:89], v[200:203], v[184:187], v[86:89]
	v_mfma_f32_16x16x32_bf16 v[82:85], v[208:211], v[184:187], v[82:85]
	v_mfma_f32_16x16x32_bf16 v[70:73], v[200:203], v[192:195], v[70:73]
	v_mfma_f32_16x16x32_bf16 v[66:69], v[208:211], v[192:195], v[66:69]
	v_mfma_f32_16x16x32_bf16 v[120:123], v[204:207], v[168:171], v[120:123]
	v_mfma_f32_16x16x32_bf16 v[116:119], v[230:233], v[168:171], v[116:119]
	v_mfma_f32_16x16x32_bf16 v[104:107], v[204:207], v[180:183], v[104:107]
	v_mfma_f32_16x16x32_bf16 v[100:103], v[230:233], v[180:183], v[100:103]
	v_mfma_f32_16x16x32_bf16 v[86:89], v[204:207], v[188:191], v[86:89]
	v_mfma_f32_16x16x32_bf16 v[82:85], v[230:233], v[188:191], v[82:85]
	v_mfma_f32_16x16x32_bf16 v[70:73], v[204:207], v[196:199], v[70:73]
	v_mfma_f32_16x16x32_bf16 v[66:69], v[230:233], v[196:199], v[66:69]
	s_mov_b32 m0, s9
	v_lshl_add_u64 v[212:213], s[30:31], 0, v[136:137]
	s_barrier
	ds_read_b128 v[164:167], v151 offset:16384
	ds_read_b128 v[168:171], v151 offset:17408
	ds_read_b128 v[172:175], v151 offset:18432
	ds_read_b128 v[180:183], v151 offset:19456
	ds_read_b128 v[184:187], v151 offset:20480
	ds_read_b128 v[188:191], v151 offset:21504
	ds_read_b128 v[192:195], v151 offset:22528
	ds_read_b128 v[196:199], v151 offset:23552
	global_load_lds_dwordx4 v[212:213], off
	v_lshl_add_u64 v[214:215], s[30:31], 0, v[134:135]
	s_mov_b32 m0, s20
	s_nop 0
	global_load_lds_dwordx4 v[214:215], off
	s_barrier
	s_waitcnt lgkmcnt(0)
	s_waitcnt lgkmcnt(0)
	v_mfma_f32_16x16x32_bf16 v[62:65], v[146:149], v[164:167], v[62:65]
	v_mfma_f32_16x16x32_bf16 v[58:61], v[156:159], v[164:167], v[58:61]
	v_mfma_f32_16x16x32_bf16 v[50:53], v[146:149], v[172:175], v[50:53]
	v_mfma_f32_16x16x32_bf16 v[42:45], v[156:159], v[172:175], v[42:45]
	v_mfma_f32_16x16x32_bf16 v[34:37], v[146:149], v[184:187], v[34:37]
	v_mfma_f32_16x16x32_bf16 v[26:29], v[156:159], v[184:187], v[26:29]
	v_mfma_f32_16x16x32_bf16 v[18:21], v[146:149], v[192:195], v[18:21]
	v_mfma_f32_16x16x32_bf16 v[10:13], v[156:159], v[192:195], v[10:13]
	v_mfma_f32_16x16x32_bf16 v[62:65], v[152:155], v[168:171], v[62:65]
	v_mfma_f32_16x16x32_bf16 v[58:61], v[160:163], v[168:171], v[58:61]
	v_mfma_f32_16x16x32_bf16 v[50:53], v[152:155], v[180:183], v[50:53]
	v_mfma_f32_16x16x32_bf16 v[42:45], v[160:163], v[180:183], v[42:45]
	v_mfma_f32_16x16x32_bf16 v[34:37], v[152:155], v[188:191], v[34:37]
	v_mfma_f32_16x16x32_bf16 v[26:29], v[160:163], v[188:191], v[26:29]
	v_mfma_f32_16x16x32_bf16 v[18:21], v[152:155], v[196:199], v[18:21]
	v_mfma_f32_16x16x32_bf16 v[10:13], v[160:163], v[196:199], v[10:13]
	s_barrier
	s_add_u32 s24, s28, 0x28000
	s_addc_u32 s25, s29, 0
	s_add_i32 s45, s46, s8
	v_lshl_add_u64 v[146:147], s[24:25], 0, v[98:99]
	s_mov_b32 m0, s45
	s_nop 0
	global_load_lds_dwordx4 v[146:147], off
	v_lshl_add_u64 v[146:147], s[24:25], 0, v[132:133]
	s_add_i32 m0, s45, 0x2000
	s_nop 0
	global_load_lds_dwordx4 v[146:147], off
	s_waitcnt vmcnt(6)
	s_barrier
	v_mfma_f32_16x16x32_bf16 v[54:57], v[200:203], v[164:167], v[54:57]
	v_mfma_f32_16x16x32_bf16 v[46:49], v[208:211], v[164:167], v[46:49]
	v_mfma_f32_16x16x32_bf16 v[38:41], v[200:203], v[172:175], v[38:41]
	v_mfma_f32_16x16x32_bf16 v[30:33], v[208:211], v[172:175], v[30:33]
	v_mfma_f32_16x16x32_bf16 v[22:25], v[200:203], v[184:187], v[22:25]
	v_mfma_f32_16x16x32_bf16 v[14:17], v[208:211], v[184:187], v[14:17]
	v_mfma_f32_16x16x32_bf16 v[6:9], v[200:203], v[192:195], v[6:9]
	v_mfma_f32_16x16x32_bf16 v[2:5], v[208:211], v[192:195], v[2:5]
	v_mfma_f32_16x16x32_bf16 v[54:57], v[204:207], v[168:171], v[54:57]
	v_mfma_f32_16x16x32_bf16 v[46:49], v[230:233], v[168:171], v[46:49]
	v_mfma_f32_16x16x32_bf16 v[38:41], v[204:207], v[180:183], v[38:41]
	v_mfma_f32_16x16x32_bf16 v[30:33], v[230:233], v[180:183], v[30:33]
	v_mfma_f32_16x16x32_bf16 v[22:25], v[204:207], v[188:191], v[22:25]
	v_mfma_f32_16x16x32_bf16 v[14:17], v[230:233], v[188:191], v[14:17]
	v_mfma_f32_16x16x32_bf16 v[6:9], v[204:207], v[196:199], v[6:9]
	v_mfma_f32_16x16x32_bf16 v[2:5], v[230:233], v[196:199], v[2:5]
	s_add_i32 s45, 0, 0x18000
	v_add_u32_e32 v142, s45, v143
	s_barrier
	ds_read_b128 v[146:149], v142
	ds_read_b128 v[152:155], v142 offset:1024
	ds_read_b128 v[156:159], v142 offset:2048
	ds_read_b128 v[160:163], v142 offset:3072
	s_add_u32 s24, s30, 0x190000
	s_addc_u32 s25, s31, 0
	s_mov_b32 m0, s21
	v_lshl_add_u64 v[200:201], s[24:25], 0, v[136:137]
	ds_read_b128 v[164:167], v151 offset:32768
	ds_read_b128 v[168:171], v151 offset:33792
	ds_read_b128 v[172:175], v151 offset:34816
	ds_read_b128 v[180:183], v151 offset:35840
	ds_read_b128 v[184:187], v151 offset:36864
	ds_read_b128 v[188:191], v151 offset:37888
	ds_read_b128 v[192:195], v151 offset:38912
	ds_read_b128 v[196:199], v151 offset:39936
	global_load_lds_dwordx4 v[200:201], off
	v_lshl_add_u64 v[200:201], s[24:25], 0, v[134:135]
	s_mov_b32 m0, s33
	s_nop 0
	global_load_lds_dwordx4 v[200:201], off
	s_waitcnt lgkmcnt(8)
	s_barrier
	s_waitcnt lgkmcnt(0)
	s_waitcnt lgkmcnt(0)
	v_mfma_f32_16x16x32_bf16 v[128:131], v[146:149], v[164:167], v[128:131]
	v_mfma_f32_16x16x32_bf16 v[124:127], v[156:159], v[164:167], v[124:127]
	v_mfma_f32_16x16x32_bf16 v[112:115], v[146:149], v[172:175], v[112:115]
	v_mfma_f32_16x16x32_bf16 v[108:111], v[156:159], v[172:175], v[108:111]
	v_mfma_f32_16x16x32_bf16 v[94:97], v[146:149], v[184:187], v[94:97]
	v_mfma_f32_16x16x32_bf16 v[90:93], v[156:159], v[184:187], v[90:93]
	v_mfma_f32_16x16x32_bf16 v[78:81], v[146:149], v[192:195], v[78:81]
	v_mfma_f32_16x16x32_bf16 v[74:77], v[156:159], v[192:195], v[74:77]
	v_mfma_f32_16x16x32_bf16 v[128:131], v[152:155], v[168:171], v[128:131]
	v_mfma_f32_16x16x32_bf16 v[124:127], v[160:163], v[168:171], v[124:127]
	v_mfma_f32_16x16x32_bf16 v[112:115], v[152:155], v[180:183], v[112:115]
	v_mfma_f32_16x16x32_bf16 v[108:111], v[160:163], v[180:183], v[108:111]
	v_mfma_f32_16x16x32_bf16 v[94:97], v[152:155], v[188:191], v[94:97]
	v_mfma_f32_16x16x32_bf16 v[90:93], v[160:163], v[188:191], v[90:93]
	v_mfma_f32_16x16x32_bf16 v[78:81], v[152:155], v[196:199], v[78:81]
	v_mfma_f32_16x16x32_bf16 v[74:77], v[160:163], v[196:199], v[74:77]
	s_barrier
	s_add_i32 s30, 0, 0x1c000
	s_add_i32 s24, s45, s8
	v_add_u32_e32 v142, s30, v143
	v_lshl_add_u64 v[176:177], v[176:177], 0, s[68:69]
	s_mov_b32 m0, s24
	ds_read_b128 v[200:203], v142
	ds_read_b128 v[204:207], v142 offset:1024
	ds_read_b128 v[208:211], v142 offset:2048
	ds_read_b128 v[230:233], v142 offset:3072
	global_load_lds_dwordx4 v[176:177], off
	v_lshl_add_u64 v[176:177], v[178:179], 0, s[68:69]
	s_add_i32 m0, s24, 0x2000
	s_nop 0
	global_load_lds_dwordx4 v[176:177], off
	s_barrier
	s_waitcnt lgkmcnt(0)
	s_waitcnt lgkmcnt(0)
	v_mfma_f32_16x16x32_bf16 v[120:123], v[200:203], v[164:167], v[120:123]
	v_mfma_f32_16x16x32_bf16 v[116:119], v[208:211], v[164:167], v[116:119]
	v_mfma_f32_16x16x32_bf16 v[104:107], v[200:203], v[172:175], v[104:107]
	v_mfma_f32_16x16x32_bf16 v[100:103], v[208:211], v[172:175], v[100:103]
	v_mfma_f32_16x16x32_bf16 v[86:89], v[200:203], v[184:187], v[86:89]
	v_mfma_f32_16x16x32_bf16 v[82:85], v[208:211], v[184:187], v[82:85]
	v_mfma_f32_16x16x32_bf16 v[70:73], v[200:203], v[192:195], v[70:73]
	v_mfma_f32_16x16x32_bf16 v[66:69], v[208:211], v[192:195], v[66:69]
	v_mfma_f32_16x16x32_bf16 v[120:123], v[204:207], v[168:171], v[120:123]
	v_mfma_f32_16x16x32_bf16 v[116:119], v[230:233], v[168:171], v[116:119]
	v_mfma_f32_16x16x32_bf16 v[104:107], v[204:207], v[180:183], v[104:107]
	v_mfma_f32_16x16x32_bf16 v[100:103], v[230:233], v[180:183], v[100:103]
	v_mfma_f32_16x16x32_bf16 v[86:89], v[204:207], v[188:191], v[86:89]
	v_mfma_f32_16x16x32_bf16 v[82:85], v[230:233], v[188:191], v[82:85]
	v_mfma_f32_16x16x32_bf16 v[70:73], v[204:207], v[196:199], v[70:73]
	v_mfma_f32_16x16x32_bf16 v[66:69], v[230:233], v[196:199], v[66:69]
	s_mov_b32 m0, s34
	v_lshl_add_u64 v[176:177], v[212:213], 0, s[68:69]
	s_barrier
	ds_read_b128 v[164:167], v151 offset:49152
	ds_read_b128 v[168:171], v151 offset:50176
	ds_read_b128 v[172:175], v151 offset:51200
	ds_read_b128 v[180:183], v151 offset:52224
	ds_read_b128 v[184:187], v151 offset:53248
	ds_read_b128 v[188:191], v151 offset:54272
	ds_read_b128 v[192:195], v151 offset:55296
	ds_read_b128 v[196:199], v151 offset:56320
	global_load_lds_dwordx4 v[176:177], off
	v_lshl_add_u64 v[176:177], v[214:215], 0, s[68:69]
	s_mov_b32 m0, s35
	s_nop 0
	global_load_lds_dwordx4 v[176:177], off
	s_barrier
	s_waitcnt lgkmcnt(0)
	s_waitcnt lgkmcnt(0)
	v_mfma_f32_16x16x32_bf16 v[62:65], v[146:149], v[164:167], v[62:65]
	v_mfma_f32_16x16x32_bf16 v[58:61], v[156:159], v[164:167], v[58:61]
	v_mfma_f32_16x16x32_bf16 v[50:53], v[146:149], v[172:175], v[50:53]
	v_mfma_f32_16x16x32_bf16 v[42:45], v[156:159], v[172:175], v[42:45]
	v_mfma_f32_16x16x32_bf16 v[34:37], v[146:149], v[184:187], v[34:37]
	v_mfma_f32_16x16x32_bf16 v[26:29], v[156:159], v[184:187], v[26:29]
	v_mfma_f32_16x16x32_bf16 v[18:21], v[146:149], v[192:195], v[18:21]
	v_mfma_f32_16x16x32_bf16 v[10:13], v[156:159], v[192:195], v[10:13]
	v_mfma_f32_16x16x32_bf16 v[62:65], v[152:155], v[168:171], v[62:65]
	v_mfma_f32_16x16x32_bf16 v[58:61], v[160:163], v[168:171], v[58:61]
	v_mfma_f32_16x16x32_bf16 v[50:53], v[152:155], v[180:183], v[50:53]
	v_mfma_f32_16x16x32_bf16 v[42:45], v[160:163], v[180:183], v[42:45]
	v_mfma_f32_16x16x32_bf16 v[34:37], v[152:155], v[188:191], v[34:37]
	v_mfma_f32_16x16x32_bf16 v[26:29], v[160:163], v[188:191], v[26:29]
	v_mfma_f32_16x16x32_bf16 v[18:21], v[152:155], v[196:199], v[18:21]
	v_mfma_f32_16x16x32_bf16 v[10:13], v[160:163], v[196:199], v[10:13]
	s_barrier
	s_add_u32 s24, s28, 0x28080
	s_addc_u32 s25, s29, 0
	s_add_i32 s28, s30, s8
	v_lshl_add_u64 v[146:147], s[24:25], 0, v[98:99]
	s_mov_b32 m0, s28
	s_nop 0
	global_load_lds_dwordx4 v[146:147], off
	v_lshl_add_u64 v[146:147], s[24:25], 0, v[132:133]
	s_add_i32 m0, s28, 0x2000
	s_nop 0
	global_load_lds_dwordx4 v[146:147], off
	s_waitcnt vmcnt(6)
	s_barrier
	v_mfma_f32_16x16x32_bf16 v[54:57], v[200:203], v[164:167], v[54:57]
	v_mfma_f32_16x16x32_bf16 v[46:49], v[208:211], v[164:167], v[46:49]
	v_mfma_f32_16x16x32_bf16 v[38:41], v[200:203], v[172:175], v[38:41]
	v_mfma_f32_16x16x32_bf16 v[30:33], v[208:211], v[172:175], v[30:33]
	v_mfma_f32_16x16x32_bf16 v[22:25], v[200:203], v[184:187], v[22:25]
	v_mfma_f32_16x16x32_bf16 v[14:17], v[208:211], v[184:187], v[14:17]
	v_mfma_f32_16x16x32_bf16 v[6:9], v[200:203], v[192:195], v[6:9]
	v_mfma_f32_16x16x32_bf16 v[2:5], v[208:211], v[192:195], v[2:5]
	v_mfma_f32_16x16x32_bf16 v[54:57], v[204:207], v[168:171], v[54:57]
	v_mfma_f32_16x16x32_bf16 v[46:49], v[230:233], v[168:171], v[46:49]
	v_mfma_f32_16x16x32_bf16 v[38:41], v[204:207], v[180:183], v[38:41]
	v_mfma_f32_16x16x32_bf16 v[30:33], v[230:233], v[180:183], v[30:33]
	v_mfma_f32_16x16x32_bf16 v[22:25], v[204:207], v[188:191], v[22:25]
	v_mfma_f32_16x16x32_bf16 v[14:17], v[230:233], v[188:191], v[14:17]
	v_mfma_f32_16x16x32_bf16 v[6:9], v[204:207], v[196:199], v[6:9]
	v_mfma_f32_16x16x32_bf16 v[2:5], v[230:233], v[196:199], v[2:5]
	s_add_i32 s44, s44, 2
	s_add_u32 s42, s42, 0x100
	s_addc_u32 s43, s43, 0
	s_cmp_gt_u32 s44, 7
	s_mov_b64 s[24:25], s[26:27]
	s_barrier
	s_cbranch_scc0 .LBB0_690
	s_cmp_gt_i32 s40, 2
	s_cselect_b64 s[24:25], -1, 0
	v_cndmask_b32_e64 v142, 0, 1, s[24:25]
	v_lshl_add_u32 v153, s41, 8, v1
	v_lshl_or_b32 v146, v153, 1, v142
	v_readlane_b32 s24, v253, 3
	v_ashrrev_i32_e32 v147, 31, v146
	v_readlane_b32 s25, v253, 4
	v_or_b32_e32 v159, 16, v153
	v_or_b32_e32 v161, 32, v153
	v_lshl_add_u64 v[146:147], v[146:147], 2, s[24:25]
	global_load_dword v158, v[146:147], off
	v_lshl_or_b32 v146, v159, 1, v142
	v_ashrrev_i32_e32 v147, 31, v146
	v_lshl_add_u64 v[146:147], v[146:147], 2, s[24:25]
	global_load_dword v160, v[146:147], off
	v_lshl_or_b32 v146, v161, 1, v142
	v_ashrrev_i32_e32 v147, 31, v146
	v_lshl_add_u64 v[146:147], v[146:147], 2, s[24:25]
	v_or_b32_e32 v157, 48, v153
	global_load_dword v156, v[146:147], off
	v_lshl_or_b32 v146, v157, 1, v142
	v_ashrrev_i32_e32 v147, 31, v146
	v_lshl_add_u64 v[146:147], v[146:147], 2, s[24:25]
	global_load_dword v154, v[146:147], off
	v_add_u32_e32 v155, 0x80, v153
	v_lshl_or_b32 v146, v155, 1, v142
	v_ashrrev_i32_e32 v147, 31, v146
	v_lshl_add_u64 v[146:147], v[146:147], 2, s[24:25]
	global_load_dword v152, v[146:147], off
	global_load_dword v150, v[146:147], off offset:128
	global_load_dword v144, v[146:147], off offset:256
	global_load_dword v142, v[146:147], off offset:384
	v_readlane_b32 s24, v253, 7
	v_lshl_or_b32 v148, s40, 8, v145
	v_readlane_b32 s25, v253, 8
	v_ashrrev_i32_e32 v149, 31, v148
	v_lshlrev_b64 v[148:149], 1, v[148:149]
	v_mov_b64_e32 v[146:147], s[24:25]
	v_mad_i64_i32 v[162:163], s[24:25], v153, s49, v[146:147]
	v_lshl_add_u64 v[162:163], v[162:163], 0, v[148:149]
	s_and_b64 vcc, exec, s[0:1]
	s_mov_b32 s41, s39
	s_mov_b32 s40, s37
	s_mov_b64 s[26:27], s[22:23]
	s_waitcnt vmcnt(0)
	v_pk_mul_f32 v[130:131], v[130:131], v[158:159] op_sel_hi:[1,0]
	v_pk_mul_f32 v[128:129], v[128:129], v[158:159] op_sel_hi:[1,0]
	v_pk_mul_f32 v[164:165], v[126:127], v[158:159] op_sel_hi:[1,0]
	v_pk_mul_f32 v[126:127], v[124:125], v[158:159] op_sel_hi:[1,0]
	v_cvt_pk_bf16_f32 v124, v128, v129
	v_cvt_pk_bf16_f32 v125, v130, v131
	v_pk_mul_f32 v[122:123], v[122:123], v[158:159] op_sel_hi:[1,0]
	v_cvt_pk_bf16_f32 v126, v126, v127
	v_cvt_pk_bf16_f32 v127, v164, v165
	global_store_dwordx4 v[162:163], v[124:127], off
	v_pk_mul_f32 v[120:121], v[120:121], v[158:159] op_sel_hi:[1,0]
	v_pk_mul_f32 v[114:115], v[114:115], v[160:161] op_sel_hi:[1,0]
	v_pk_mul_f32 v[124:125], v[118:119], v[158:159] op_sel_hi:[1,0]
	v_pk_mul_f32 v[118:119], v[116:117], v[158:159] op_sel_hi:[1,0]
	v_cvt_pk_bf16_f32 v116, v120, v121
	v_cvt_pk_bf16_f32 v117, v122, v123
	v_pk_mul_f32 v[112:113], v[112:113], v[160:161] op_sel_hi:[1,0]
	v_cvt_pk_bf16_f32 v118, v118, v119
	v_cvt_pk_bf16_f32 v119, v124, v125
	global_store_dwordx4 v[162:163], v[116:119], off offset:256
	v_pk_mul_f32 v[106:107], v[106:107], v[160:161] op_sel_hi:[1,0]
	v_pk_mul_f32 v[104:105], v[104:105], v[160:161] op_sel_hi:[1,0]
	v_mad_i64_i32 v[116:117], s[24:25], v159, s49, v[146:147]
	v_lshl_add_u64 v[116:117], v[116:117], 0, v[148:149]
	v_pk_mul_f32 v[118:119], v[110:111], v[160:161] op_sel_hi:[1,0]
	v_pk_mul_f32 v[110:111], v[108:109], v[160:161] op_sel_hi:[1,0]
	v_cvt_pk_bf16_f32 v108, v112, v113
	v_cvt_pk_bf16_f32 v109, v114, v115
	v_pk_mul_f32 v[96:97], v[96:97], v[156:157] op_sel_hi:[1,0]
	v_cvt_pk_bf16_f32 v110, v110, v111
	v_cvt_pk_bf16_f32 v111, v118, v119
	global_store_dwordx4 v[116:117], v[108:111], off
	v_pk_mul_f32 v[94:95], v[94:95], v[156:157] op_sel_hi:[1,0]
	v_pk_mul_f32 v[88:89], v[88:89], v[156:157] op_sel_hi:[1,0]
	v_pk_mul_f32 v[108:109], v[102:103], v[160:161] op_sel_hi:[1,0]
	v_pk_mul_f32 v[102:103], v[100:101], v[160:161] op_sel_hi:[1,0]
	v_cvt_pk_bf16_f32 v100, v104, v105
	v_cvt_pk_bf16_f32 v101, v106, v107
	v_pk_mul_f32 v[86:87], v[86:87], v[156:157] op_sel_hi:[1,0]
	v_cvt_pk_bf16_f32 v102, v102, v103
	v_cvt_pk_bf16_f32 v103, v108, v109
	global_store_dwordx4 v[116:117], v[100:103], off offset:256
	v_pk_mul_f32 v[80:81], v[80:81], v[154:155] op_sel_hi:[1,0]
	v_pk_mul_f32 v[78:79], v[78:79], v[154:155] op_sel_hi:[1,0]
	v_mad_i64_i32 v[100:101], s[24:25], v161, s49, v[146:147]
	v_lshl_add_u64 v[100:101], v[100:101], 0, v[148:149]
	v_pk_mul_f32 v[102:103], v[92:93], v[156:157] op_sel_hi:[1,0]
	v_pk_mul_f32 v[92:93], v[90:91], v[156:157] op_sel_hi:[1,0]
	v_cvt_pk_bf16_f32 v90, v94, v95
	v_cvt_pk_bf16_f32 v91, v96, v97
	v_pk_mul_f32 v[72:73], v[72:73], v[154:155] op_sel_hi:[1,0]
	v_cvt_pk_bf16_f32 v92, v92, v93
	v_cvt_pk_bf16_f32 v93, v102, v103
	global_store_dwordx4 v[100:101], v[90:93], off
	v_pk_mul_f32 v[70:71], v[70:71], v[154:155] op_sel_hi:[1,0]
	v_pk_mul_f32 v[64:65], v[64:65], v[152:153] op_sel_hi:[1,0]
	v_pk_mul_f32 v[90:91], v[84:85], v[156:157] op_sel_hi:[1,0]
	v_pk_mul_f32 v[84:85], v[82:83], v[156:157] op_sel_hi:[1,0]
	v_cvt_pk_bf16_f32 v82, v86, v87
	v_cvt_pk_bf16_f32 v83, v88, v89
	v_pk_mul_f32 v[62:63], v[62:63], v[152:153] op_sel_hi:[1,0]
	v_cvt_pk_bf16_f32 v84, v84, v85
	v_cvt_pk_bf16_f32 v85, v90, v91
	global_store_dwordx4 v[100:101], v[82:85], off offset:256
	v_pk_mul_f32 v[54:55], v[54:55], v[152:153] op_sel_hi:[1,0]
	v_pk_mul_f32 v[56:57], v[56:57], v[152:153] op_sel_hi:[1,0]
	v_mad_i64_i32 v[82:83], s[24:25], v157, s49, v[146:147]
	v_lshl_add_u64 v[82:83], v[82:83], 0, v[148:149]
	v_pk_mul_f32 v[84:85], v[76:77], v[154:155] op_sel_hi:[1,0]
	v_pk_mul_f32 v[76:77], v[74:75], v[154:155] op_sel_hi:[1,0]
	v_cvt_pk_bf16_f32 v74, v78, v79
	v_cvt_pk_bf16_f32 v75, v80, v81
	v_pk_mul_f32 v[50:51], v[50:51], v[150:151] op_sel_hi:[1,0]
	v_cvt_pk_bf16_f32 v76, v76, v77
	v_cvt_pk_bf16_f32 v77, v84, v85
	global_store_dwordx4 v[82:83], v[74:77], off
	v_pk_mul_f32 v[38:39], v[38:39], v[150:151] op_sel_hi:[1,0]
	v_pk_mul_f32 v[40:41], v[40:41], v[150:151] op_sel_hi:[1,0]
	v_pk_mul_f32 v[74:75], v[68:69], v[154:155] op_sel_hi:[1,0]
	v_pk_mul_f32 v[68:69], v[66:67], v[154:155] op_sel_hi:[1,0]
	v_cvt_pk_bf16_f32 v66, v70, v71
	v_cvt_pk_bf16_f32 v67, v72, v73
	v_pk_mul_f32 v[34:35], v[34:35], v[144:145] op_sel_hi:[1,0]
	v_cvt_pk_bf16_f32 v68, v68, v69
	v_cvt_pk_bf16_f32 v69, v74, v75
	global_store_dwordx4 v[82:83], v[66:69], off offset:256
	v_pk_mul_f32 v[22:23], v[22:23], v[144:145] op_sel_hi:[1,0]
	v_pk_mul_f32 v[24:25], v[24:25], v[144:145] op_sel_hi:[1,0]
	v_mad_i64_i32 v[66:67], s[24:25], v155, s49, v[146:147]
	v_lshl_add_u64 v[66:67], v[66:67], 0, v[148:149]
	v_pk_mul_f32 v[68:69], v[60:61], v[152:153] op_sel_hi:[1,0]
	v_pk_mul_f32 v[60:61], v[58:59], v[152:153] op_sel_hi:[1,0]
	v_cvt_pk_bf16_f32 v58, v62, v63
	v_cvt_pk_bf16_f32 v59, v64, v65
	v_pk_mul_f32 v[18:19], v[18:19], v[142:143] op_sel_hi:[1,0]
	v_cvt_pk_bf16_f32 v60, v60, v61
	v_cvt_pk_bf16_f32 v61, v68, v69
	global_store_dwordx4 v[66:67], v[58:61], off
	v_pk_mul_f32 v[8:9], v[8:9], v[142:143] op_sel_hi:[1,0]
	v_pk_mul_f32 v[6:7], v[6:7], v[142:143] op_sel_hi:[1,0]
	v_pk_mul_f32 v[58:59], v[48:49], v[152:153] op_sel_hi:[1,0]
	v_pk_mul_f32 v[48:49], v[46:47], v[152:153] op_sel_hi:[1,0]
	v_cvt_pk_bf16_f32 v46, v54, v55
	v_cvt_pk_bf16_f32 v47, v56, v57
	s_nop 0
	v_cvt_pk_bf16_f32 v48, v48, v49
	v_cvt_pk_bf16_f32 v49, v58, v59
	global_store_dwordx4 v[66:67], v[46:49], off offset:256
	s_nop 1
	v_add_u32_e32 v46, 0x90, v153
	v_mad_i64_i32 v[46:47], s[24:25], v46, s49, v[146:147]
	v_lshl_add_u64 v[46:47], v[46:47], 0, v[148:149]
	v_pk_mul_f32 v[48:49], v[52:53], v[150:151] op_sel_hi:[1,0]
	v_pk_mul_f32 v[52:53], v[44:45], v[150:151] op_sel_hi:[1,0]
	v_pk_mul_f32 v[44:45], v[42:43], v[150:151] op_sel_hi:[1,0]
	v_cvt_pk_bf16_f32 v42, v50, v51
	v_cvt_pk_bf16_f32 v43, v48, v49
	s_nop 0
	v_cvt_pk_bf16_f32 v44, v44, v45
	v_cvt_pk_bf16_f32 v45, v52, v53
	global_store_dwordx4 v[46:47], v[42:45], off
	s_nop 1
	v_pk_mul_f32 v[42:43], v[32:33], v[150:151] op_sel_hi:[1,0]
	v_pk_mul_f32 v[32:33], v[30:31], v[150:151] op_sel_hi:[1,0]
	v_cvt_pk_bf16_f32 v30, v38, v39
	v_cvt_pk_bf16_f32 v31, v40, v41
	s_nop 0
	v_cvt_pk_bf16_f32 v32, v32, v33
	v_cvt_pk_bf16_f32 v33, v42, v43
	global_store_dwordx4 v[46:47], v[30:33], off offset:256
	s_nop 1
	v_add_u32_e32 v30, 0xa0, v153
	v_mad_i64_i32 v[30:31], s[24:25], v30, s49, v[146:147]
	v_lshl_add_u64 v[30:31], v[30:31], 0, v[148:149]
	v_pk_mul_f32 v[32:33], v[36:37], v[144:145] op_sel_hi:[1,0]
	v_pk_mul_f32 v[36:37], v[28:29], v[144:145] op_sel_hi:[1,0]
	v_pk_mul_f32 v[28:29], v[26:27], v[144:145] op_sel_hi:[1,0]
	v_cvt_pk_bf16_f32 v26, v34, v35
	v_cvt_pk_bf16_f32 v27, v32, v33
	s_nop 0
	v_cvt_pk_bf16_f32 v28, v28, v29
	v_cvt_pk_bf16_f32 v29, v36, v37
	global_store_dwordx4 v[30:31], v[26:29], off
	s_nop 1
	v_pk_mul_f32 v[26:27], v[16:17], v[144:145] op_sel_hi:[1,0]
	v_pk_mul_f32 v[16:17], v[14:15], v[144:145] op_sel_hi:[1,0]
	v_cvt_pk_bf16_f32 v14, v22, v23
	v_cvt_pk_bf16_f32 v15, v24, v25
	s_nop 0
	v_cvt_pk_bf16_f32 v16, v16, v17
	v_cvt_pk_bf16_f32 v17, v26, v27
	global_store_dwordx4 v[30:31], v[14:17], off offset:256
	s_nop 1
	v_add_u32_e32 v14, 0xb0, v153
	v_mad_i64_i32 v[14:15], s[24:25], v14, s49, v[146:147]
	v_lshl_add_u64 v[14:15], v[14:15], 0, v[148:149]
	v_pk_mul_f32 v[16:17], v[20:21], v[142:143] op_sel_hi:[1,0]
	v_pk_mul_f32 v[20:21], v[12:13], v[142:143] op_sel_hi:[1,0]
	v_pk_mul_f32 v[12:13], v[10:11], v[142:143] op_sel_hi:[1,0]
	v_cvt_pk_bf16_f32 v10, v18, v19
	v_cvt_pk_bf16_f32 v11, v16, v17
	s_mov_b64 s[24:25], s[18:19]
	v_cvt_pk_bf16_f32 v12, v12, v13
	v_cvt_pk_bf16_f32 v13, v20, v21
	global_store_dwordx4 v[14:15], v[10:13], off
	s_nop 1
	v_pk_mul_f32 v[10:11], v[4:5], v[142:143] op_sel_hi:[1,0]
	v_pk_mul_f32 v[4:5], v[2:3], v[142:143] op_sel_hi:[1,0]
	v_cvt_pk_bf16_f32 v2, v6, v7
	v_cvt_pk_bf16_f32 v3, v8, v9
	s_nop 0
	v_cvt_pk_bf16_f32 v4, v4, v5
	v_cvt_pk_bf16_f32 v5, v10, v11
	global_store_dwordx4 v[14:15], v[2:5], off offset:256
	s_cbranch_vccz .LBB0_683
	s_waitcnt vmcnt(0)
	s_cmpk_gt_u32 s3, 0xff
	s_cbranch_scc1 .LBB0_694
	s_barrier

.LBB0_1592:
	s_add_u32 s34, s30, 0xfff80080
	s_addc_u32 s35, s31, -1
	s_add_i32 s46, 0, 0x10000
	v_add_u32_e32 v86, s46, v160
	ds_read_b128 v[70:73], v86
	ds_read_b128 v[78:81], v86 offset:1024
	ds_read_b128 v[82:85], v86 offset:2048
	ds_read_b128 v[86:89], v86 offset:3072
	s_cmp_eq_u32 s45, 28
	s_cselect_b32 s37, s25, s35
	s_cselect_b32 s36, s41, s34
	s_cselect_b32 s35, s19, s44
	s_cselect_b32 s34, s42, s43
	v_lshl_add_u64 v[158:159], s[30:31], 0, v[150:151]
	s_add_i32 m0, s5, 0xc000
	ds_read_b128 v[154:157], v162
	ds_read_b128 v[164:167], v162 offset:1024
	ds_read_b128 v[168:171], v162 offset:2048
	ds_read_b128 v[172:175], v162 offset:3072
	ds_read_b128 v[176:179], v162 offset:4096
	ds_read_b128 v[180:183], v162 offset:5120
	ds_read_b128 v[184:187], v162 offset:6144
	ds_read_b128 v[188:191], v162 offset:7168
	global_load_lds_dwordx4 v[158:159], off
	v_lshl_add_u64 v[158:159], s[30:31], 0, v[152:153]
	s_add_i32 m0, s5, 0xe000
	s_nop 0
	global_load_lds_dwordx4 v[158:159], off
	s_waitcnt lgkmcnt(8)
	s_barrier
	s_waitcnt lgkmcnt(0)
	s_waitcnt lgkmcnt(0)
	v_mfma_f32_16x16x32_bf16 v[144:147], v[70:73], v[154:157], v[144:147]
	v_mfma_f32_16x16x32_bf16 v[140:143], v[82:85], v[154:157], v[140:143]
	v_mfma_f32_16x16x32_bf16 v[128:131], v[70:73], v[168:171], v[128:131]
	v_mfma_f32_16x16x32_bf16 v[124:127], v[82:85], v[168:171], v[124:127]
	v_mfma_f32_16x16x32_bf16 v[112:115], v[70:73], v[176:179], v[112:115]
	v_mfma_f32_16x16x32_bf16 v[108:111], v[82:85], v[176:179], v[108:111]
	v_mfma_f32_16x16x32_bf16 v[94:97], v[70:73], v[184:187], v[94:97]
	v_mfma_f32_16x16x32_bf16 v[90:93], v[82:85], v[184:187], v[90:93]
	v_mfma_f32_16x16x32_bf16 v[144:147], v[78:81], v[164:167], v[144:147]
	v_mfma_f32_16x16x32_bf16 v[140:143], v[86:89], v[164:167], v[140:143]
	v_mfma_f32_16x16x32_bf16 v[128:131], v[78:81], v[172:175], v[128:131]
	v_mfma_f32_16x16x32_bf16 v[124:127], v[86:89], v[172:175], v[124:127]
	v_mfma_f32_16x16x32_bf16 v[112:115], v[78:81], v[180:183], v[112:115]
	v_mfma_f32_16x16x32_bf16 v[108:111], v[86:89], v[180:183], v[108:111]
	v_mfma_f32_16x16x32_bf16 v[94:97], v[78:81], v[188:191], v[94:97]
	v_mfma_f32_16x16x32_bf16 v[90:93], v[86:89], v[188:191], v[90:93]
	s_barrier
	s_add_i32 s48, 0, 0x14000
	v_add_u32_e32 v158, s48, v160
	s_add_i32 s46, s46, s4
	ds_read_b128 v[192:195], v158
	ds_read_b128 v[196:199], v158 offset:1024
	ds_read_b128 v[200:203], v158 offset:2048
	ds_read_b128 v[204:207], v158 offset:3072
	v_lshl_add_u64 v[158:159], s[34:35], 0, v[98:99]
	s_mov_b32 m0, s46
	v_lshl_add_u64 v[208:209], s[34:35], 0, v[148:149]
	global_load_lds_dwordx4 v[158:159], off
	s_add_i32 m0, s46, 0x2000
	s_nop 0
	global_load_lds_dwordx4 v[208:209], off
	s_barrier
	s_waitcnt lgkmcnt(0)
	s_waitcnt lgkmcnt(0)
	v_mfma_f32_16x16x32_bf16 v[136:139], v[192:195], v[154:157], v[136:139]
	v_mfma_f32_16x16x32_bf16 v[132:135], v[200:203], v[154:157], v[132:135]
	v_mfma_f32_16x16x32_bf16 v[120:123], v[192:195], v[168:171], v[120:123]
	v_mfma_f32_16x16x32_bf16 v[116:119], v[200:203], v[168:171], v[116:119]
	v_mfma_f32_16x16x32_bf16 v[104:107], v[192:195], v[176:179], v[104:107]
	v_mfma_f32_16x16x32_bf16 v[100:103], v[200:203], v[176:179], v[100:103]
	v_mfma_f32_16x16x32_bf16 v[74:77], v[192:195], v[184:187], v[74:77]
	v_mfma_f32_16x16x32_bf16 v[66:69], v[200:203], v[184:187], v[66:69]
	v_mfma_f32_16x16x32_bf16 v[136:139], v[196:199], v[164:167], v[136:139]
	v_mfma_f32_16x16x32_bf16 v[132:135], v[204:207], v[164:167], v[132:135]
	v_mfma_f32_16x16x32_bf16 v[120:123], v[196:199], v[172:175], v[120:123]
	v_mfma_f32_16x16x32_bf16 v[116:119], v[204:207], v[172:175], v[116:119]
	v_mfma_f32_16x16x32_bf16 v[104:107], v[196:199], v[180:183], v[104:107]
	v_mfma_f32_16x16x32_bf16 v[100:103], v[204:207], v[180:183], v[100:103]
	v_mfma_f32_16x16x32_bf16 v[74:77], v[196:199], v[188:191], v[74:77]
	v_mfma_f32_16x16x32_bf16 v[66:69], v[204:207], v[188:191], v[66:69]
	s_mov_b32 m0, s5
	v_lshl_add_u64 v[210:211], s[36:37], 0, v[98:99]
	s_barrier
	ds_read_b128 v[154:157], v162 offset:16384
	ds_read_b128 v[164:167], v162 offset:17408
	ds_read_b128 v[168:171], v162 offset:18432
	ds_read_b128 v[172:175], v162 offset:19456
	ds_read_b128 v[176:179], v162 offset:20480
	ds_read_b128 v[180:183], v162 offset:21504
	ds_read_b128 v[184:187], v162 offset:22528
	ds_read_b128 v[188:191], v162 offset:23552
	global_load_lds_dwordx4 v[210:211], off
	v_lshl_add_u64 v[212:213], s[36:37], 0, v[148:149]
	s_mov_b32 m0, s8
	s_nop 0
	global_load_lds_dwordx4 v[212:213], off
	s_barrier
	s_waitcnt lgkmcnt(0)
	s_waitcnt lgkmcnt(0)
	v_mfma_f32_16x16x32_bf16 v[62:65], v[70:73], v[154:157], v[62:65]
	v_mfma_f32_16x16x32_bf16 v[58:61], v[82:85], v[154:157], v[58:61]
	v_mfma_f32_16x16x32_bf16 v[46:49], v[70:73], v[168:171], v[46:49]
	v_mfma_f32_16x16x32_bf16 v[42:45], v[82:85], v[168:171], v[42:45]
	v_mfma_f32_16x16x32_bf16 v[30:33], v[70:73], v[176:179], v[30:33]
	v_mfma_f32_16x16x32_bf16 v[26:29], v[82:85], v[176:179], v[26:29]
	v_mfma_f32_16x16x32_bf16 v[22:25], v[70:73], v[184:187], v[22:25]
	v_mfma_f32_16x16x32_bf16 v[18:21], v[82:85], v[184:187], v[18:21]
	v_mfma_f32_16x16x32_bf16 v[62:65], v[78:81], v[164:167], v[62:65]
	v_mfma_f32_16x16x32_bf16 v[58:61], v[86:89], v[164:167], v[58:61]
	v_mfma_f32_16x16x32_bf16 v[46:49], v[78:81], v[172:175], v[46:49]
	v_mfma_f32_16x16x32_bf16 v[42:45], v[86:89], v[172:175], v[42:45]
	v_mfma_f32_16x16x32_bf16 v[30:33], v[78:81], v[180:183], v[30:33]
	v_mfma_f32_16x16x32_bf16 v[26:29], v[86:89], v[180:183], v[26:29]
	v_mfma_f32_16x16x32_bf16 v[22:25], v[78:81], v[188:191], v[22:25]
	v_mfma_f32_16x16x32_bf16 v[18:21], v[86:89], v[188:191], v[18:21]
	s_barrier
	s_add_u32 s46, s34, 0x80000
	s_addc_u32 s47, s35, 0
	s_add_i32 s48, s48, s4
	v_lshl_add_u64 v[70:71], s[46:47], 0, v[98:99]
	s_mov_b32 m0, s48
	s_nop 0
	global_load_lds_dwordx4 v[70:71], off
	v_lshl_add_u64 v[70:71], s[46:47], 0, v[148:149]
	s_add_i32 m0, s48, 0x2000
	s_nop 0
	global_load_lds_dwordx4 v[70:71], off
	s_waitcnt vmcnt(6)
	s_barrier
	v_mfma_f32_16x16x32_bf16 v[54:57], v[192:195], v[154:157], v[54:57]
	v_mfma_f32_16x16x32_bf16 v[50:53], v[200:203], v[154:157], v[50:53]
	v_mfma_f32_16x16x32_bf16 v[38:41], v[192:195], v[168:171], v[38:41]
	v_mfma_f32_16x16x32_bf16 v[34:37], v[200:203], v[168:171], v[34:37]
	v_mfma_f32_16x16x32_bf16 v[14:17], v[192:195], v[176:179], v[14:17]
	v_mfma_f32_16x16x32_bf16 v[10:13], v[200:203], v[176:179], v[10:13]
	v_mfma_f32_16x16x32_bf16 v[6:9], v[192:195], v[184:187], v[6:9]
	v_mfma_f32_16x16x32_bf16 v[2:5], v[200:203], v[184:187], v[2:5]
	v_mfma_f32_16x16x32_bf16 v[54:57], v[196:199], v[164:167], v[54:57]
	v_mfma_f32_16x16x32_bf16 v[50:53], v[204:207], v[164:167], v[50:53]
	v_mfma_f32_16x16x32_bf16 v[38:41], v[196:199], v[172:175], v[38:41]
	v_mfma_f32_16x16x32_bf16 v[34:37], v[204:207], v[172:175], v[34:37]
	v_mfma_f32_16x16x32_bf16 v[14:17], v[196:199], v[180:183], v[14:17]
	v_mfma_f32_16x16x32_bf16 v[10:13], v[204:207], v[180:183], v[10:13]
	v_mfma_f32_16x16x32_bf16 v[6:9], v[196:199], v[188:191], v[6:9]
	v_mfma_f32_16x16x32_bf16 v[2:5], v[204:207], v[188:191], v[2:5]
	s_add_i32 s46, 0, 0x18000
	v_add_u32_e32 v86, s46, v160
	s_barrier
	ds_read_b128 v[70:73], v86
	ds_read_b128 v[78:81], v86 offset:1024
	ds_read_b128 v[82:85], v86 offset:2048
	ds_read_b128 v[86:89], v86 offset:3072
	s_add_u32 s36, s36, 0x80000
	s_addc_u32 s37, s37, 0
	s_mov_b32 m0, s9
	v_lshl_add_u64 v[192:193], s[36:37], 0, v[98:99]
	ds_read_b128 v[154:157], v162 offset:32768
	ds_read_b128 v[164:167], v162 offset:33792
	ds_read_b128 v[168:171], v162 offset:34816
	ds_read_b128 v[172:175], v162 offset:35840
	ds_read_b128 v[176:179], v162 offset:36864
	ds_read_b128 v[180:183], v162 offset:37888
	ds_read_b128 v[184:187], v162 offset:38912
	ds_read_b128 v[188:191], v162 offset:39936
	global_load_lds_dwordx4 v[192:193], off
	v_lshl_add_u64 v[192:193], s[36:37], 0, v[148:149]
	s_mov_b32 m0, s20
	s_nop 0
	global_load_lds_dwordx4 v[192:193], off
	s_waitcnt lgkmcnt(8)
	s_barrier
	s_waitcnt lgkmcnt(0)
	s_waitcnt lgkmcnt(0)
	v_mfma_f32_16x16x32_bf16 v[144:147], v[70:73], v[154:157], v[144:147]
	v_mfma_f32_16x16x32_bf16 v[140:143], v[82:85], v[154:157], v[140:143]
	v_mfma_f32_16x16x32_bf16 v[128:131], v[70:73], v[168:171], v[128:131]
	v_mfma_f32_16x16x32_bf16 v[124:127], v[82:85], v[168:171], v[124:127]
	v_mfma_f32_16x16x32_bf16 v[112:115], v[70:73], v[176:179], v[112:115]
	v_mfma_f32_16x16x32_bf16 v[108:111], v[82:85], v[176:179], v[108:111]
	v_mfma_f32_16x16x32_bf16 v[94:97], v[70:73], v[184:187], v[94:97]
	v_mfma_f32_16x16x32_bf16 v[90:93], v[82:85], v[184:187], v[90:93]
	v_mfma_f32_16x16x32_bf16 v[144:147], v[78:81], v[164:167], v[144:147]
	v_mfma_f32_16x16x32_bf16 v[140:143], v[86:89], v[164:167], v[140:143]
	v_mfma_f32_16x16x32_bf16 v[128:131], v[78:81], v[172:175], v[128:131]
	v_mfma_f32_16x16x32_bf16 v[124:127], v[86:89], v[172:175], v[124:127]
	v_mfma_f32_16x16x32_bf16 v[112:115], v[78:81], v[180:183], v[112:115]
	v_mfma_f32_16x16x32_bf16 v[108:111], v[86:89], v[180:183], v[108:111]
	v_mfma_f32_16x16x32_bf16 v[94:97], v[78:81], v[188:191], v[94:97]
	v_mfma_f32_16x16x32_bf16 v[90:93], v[86:89], v[188:191], v[90:93]
	s_barrier
	s_add_i32 s36, 0, 0x1c000
	s_add_i32 s37, s46, s4
	v_add_u32_e32 v163, s36, v160
	v_lshl_add_u64 v[158:159], v[158:159], 0, s[68:69]
	s_mov_b32 m0, s37
	ds_read_b128 v[192:195], v163
	ds_read_b128 v[196:199], v163 offset:1024
	ds_read_b128 v[200:203], v163 offset:2048
	ds_read_b128 v[204:207], v163 offset:3072
	global_load_lds_dwordx4 v[158:159], off
	v_lshl_add_u64 v[158:159], v[208:209], 0, s[68:69]
	s_add_i32 m0, s37, 0x2000
	s_nop 0
	global_load_lds_dwordx4 v[158:159], off
	s_barrier
	s_waitcnt lgkmcnt(0)
	s_waitcnt lgkmcnt(0)
	v_mfma_f32_16x16x32_bf16 v[136:139], v[192:195], v[154:157], v[136:139]
	v_mfma_f32_16x16x32_bf16 v[132:135], v[200:203], v[154:157], v[132:135]
	v_mfma_f32_16x16x32_bf16 v[120:123], v[192:195], v[168:171], v[120:123]
	v_mfma_f32_16x16x32_bf16 v[116:119], v[200:203], v[168:171], v[116:119]
	v_mfma_f32_16x16x32_bf16 v[104:107], v[192:195], v[176:179], v[104:107]
	v_mfma_f32_16x16x32_bf16 v[100:103], v[200:203], v[176:179], v[100:103]
	v_mfma_f32_16x16x32_bf16 v[74:77], v[192:195], v[184:187], v[74:77]
	v_mfma_f32_16x16x32_bf16 v[66:69], v[200:203], v[184:187], v[66:69]
	v_mfma_f32_16x16x32_bf16 v[136:139], v[196:199], v[164:167], v[136:139]
	v_mfma_f32_16x16x32_bf16 v[132:135], v[204:207], v[164:167], v[132:135]
	v_mfma_f32_16x16x32_bf16 v[120:123], v[196:199], v[172:175], v[120:123]
	v_mfma_f32_16x16x32_bf16 v[116:119], v[204:207], v[172:175], v[116:119]
	v_mfma_f32_16x16x32_bf16 v[104:107], v[196:199], v[180:183], v[104:107]
	v_mfma_f32_16x16x32_bf16 v[100:103], v[204:207], v[180:183], v[100:103]
	v_mfma_f32_16x16x32_bf16 v[74:77], v[196:199], v[188:191], v[74:77]
	v_mfma_f32_16x16x32_bf16 v[66:69], v[204:207], v[188:191], v[66:69]
	s_mov_b32 m0, s21
	v_lshl_add_u64 v[158:159], v[210:211], 0, s[68:69]
	s_barrier
	ds_read_b128 v[154:157], v162 offset:49152
	ds_read_b128 v[164:167], v162 offset:50176
	ds_read_b128 v[168:171], v162 offset:51200
	ds_read_b128 v[172:175], v162 offset:52224
	ds_read_b128 v[176:179], v162 offset:53248
	ds_read_b128 v[180:183], v162 offset:54272
	ds_read_b128 v[184:187], v162 offset:55296
	ds_read_b128 v[188:191], v162 offset:56320
	global_load_lds_dwordx4 v[158:159], off
	v_lshl_add_u64 v[158:159], v[212:213], 0, s[68:69]
	s_mov_b32 m0, s33
	s_nop 0
	global_load_lds_dwordx4 v[158:159], off
	s_barrier
	s_waitcnt lgkmcnt(0)
	s_waitcnt lgkmcnt(0)
	v_mfma_f32_16x16x32_bf16 v[62:65], v[70:73], v[154:157], v[62:65]
	v_mfma_f32_16x16x32_bf16 v[58:61], v[82:85], v[154:157], v[58:61]
	v_mfma_f32_16x16x32_bf16 v[46:49], v[70:73], v[168:171], v[46:49]
	v_mfma_f32_16x16x32_bf16 v[42:45], v[82:85], v[168:171], v[42:45]
	v_mfma_f32_16x16x32_bf16 v[30:33], v[70:73], v[176:179], v[30:33]
	v_mfma_f32_16x16x32_bf16 v[26:29], v[82:85], v[176:179], v[26:29]
	v_mfma_f32_16x16x32_bf16 v[22:25], v[70:73], v[184:187], v[22:25]
	v_mfma_f32_16x16x32_bf16 v[18:21], v[82:85], v[184:187], v[18:21]
	v_mfma_f32_16x16x32_bf16 v[62:65], v[78:81], v[164:167], v[62:65]
	v_mfma_f32_16x16x32_bf16 v[58:61], v[86:89], v[164:167], v[58:61]
	v_mfma_f32_16x16x32_bf16 v[46:49], v[78:81], v[172:175], v[46:49]
	v_mfma_f32_16x16x32_bf16 v[42:45], v[86:89], v[172:175], v[42:45]
	v_mfma_f32_16x16x32_bf16 v[30:33], v[78:81], v[180:183], v[30:33]
	v_mfma_f32_16x16x32_bf16 v[26:29], v[86:89], v[180:183], v[26:29]
	v_mfma_f32_16x16x32_bf16 v[22:25], v[78:81], v[188:191], v[22:25]
	v_mfma_f32_16x16x32_bf16 v[18:21], v[86:89], v[188:191], v[18:21]
	s_barrier
	s_add_u32 s34, s34, 0x80080
	s_addc_u32 s35, s35, 0
	s_add_i32 s36, s36, s4
	v_lshl_add_u64 v[70:71], s[34:35], 0, v[98:99]
	s_mov_b32 m0, s36
	s_nop 0
	global_load_lds_dwordx4 v[70:71], off
	v_lshl_add_u64 v[70:71], s[34:35], 0, v[148:149]
	s_add_i32 m0, s36, 0x2000
	s_nop 0
	global_load_lds_dwordx4 v[70:71], off
	s_waitcnt vmcnt(6)
	s_barrier
	v_mfma_f32_16x16x32_bf16 v[54:57], v[192:195], v[154:157], v[54:57]
	v_mfma_f32_16x16x32_bf16 v[50:53], v[200:203], v[154:157], v[50:53]
	v_mfma_f32_16x16x32_bf16 v[38:41], v[192:195], v[168:171], v[38:41]
	v_mfma_f32_16x16x32_bf16 v[34:37], v[200:203], v[168:171], v[34:37]
	v_mfma_f32_16x16x32_bf16 v[14:17], v[192:195], v[176:179], v[14:17]
	v_mfma_f32_16x16x32_bf16 v[10:13], v[200:203], v[176:179], v[10:13]
	v_mfma_f32_16x16x32_bf16 v[6:9], v[192:195], v[184:187], v[6:9]
	v_mfma_f32_16x16x32_bf16 v[2:5], v[200:203], v[184:187], v[2:5]
	v_mfma_f32_16x16x32_bf16 v[54:57], v[196:199], v[164:167], v[54:57]
	v_mfma_f32_16x16x32_bf16 v[50:53], v[204:207], v[164:167], v[50:53]
	v_mfma_f32_16x16x32_bf16 v[38:41], v[196:199], v[172:175], v[38:41]
	v_mfma_f32_16x16x32_bf16 v[34:37], v[204:207], v[172:175], v[34:37]
	v_mfma_f32_16x16x32_bf16 v[14:17], v[196:199], v[180:183], v[14:17]
	v_mfma_f32_16x16x32_bf16 v[10:13], v[204:207], v[180:183], v[10:13]
	v_mfma_f32_16x16x32_bf16 v[6:9], v[196:199], v[188:191], v[6:9]
	v_mfma_f32_16x16x32_bf16 v[2:5], v[204:207], v[188:191], v[2:5]
	s_add_i32 s45, s45, 2
	s_add_u32 s30, s30, 0x100
	s_addc_u32 s31, s31, 0
	s_add_u32 s43, s43, 0x100
	s_addc_u32 s44, s44, 0
	s_cmp_gt_u32 s45, 29
	s_barrier
	s_cbranch_scc0 .LBB0_1592
	v_lshl_or_b32 v70, s39, 8, v161
	v_lshl_add_u32 v154, s40, 8, v1
	v_ashrrev_i32_e32 v71, 31, v70
	v_readlane_b32 s30, v253, 28
	v_lshlrev_b64 v[156:157], 2, v[70:71]
	v_readlane_b32 s31, v253, 29
	v_ashrrev_i32_e32 v155, 31, v154
	v_lshlrev_b64 v[164:165], 13, v[154:155]
	v_lshl_add_u64 v[158:159], s[30:31], 0, v[156:157]
	v_lshl_add_u64 v[70:71], s[22:23], 0, v[156:157]
	v_lshl_add_u64 v[176:177], v[158:159], 0, v[164:165]
	global_load_dwordx4 v[86:89], v[70:71], off
	global_load_dwordx4 v[82:85], v[70:71], off offset:64
	global_load_dwordx4 v[78:81], v[70:71], off offset:512
	s_nop 0
	global_load_dwordx4 v[70:73], v[70:71], off offset:576
	s_nop 0
	global_load_dwordx4 v[164:167], v[176:177], off
	global_load_dwordx4 v[168:171], v[176:177], off offset:64
	global_load_dwordx4 v[172:175], v[176:177], off offset:512
	s_nop 0
	global_load_dwordx4 v[176:179], v[176:177], off offset:576
	v_or_b32_e32 v180, 16, v154
	v_ashrrev_i32_e32 v181, 31, v180
	v_lshlrev_b64 v[180:181], 13, v[180:181]
	v_lshl_add_u64 v[192:193], v[158:159], 0, v[180:181]
	global_load_dwordx4 v[180:183], v[192:193], off
	global_load_dwordx4 v[184:187], v[192:193], off offset:64
	global_load_dwordx4 v[188:191], v[192:193], off offset:512
	s_nop 0
	global_load_dwordx4 v[192:195], v[192:193], off offset:576
	v_add_u32_e32 v196, 0x100, v154
	v_ashrrev_i32_e32 v197, 31, v196
	v_lshlrev_b64 v[196:197], 13, v[196:197]
	v_lshl_add_u64 v[196:197], s[76:77], 0, v[196:197]
	v_lshl_add_u64 v[196:197], v[196:197], 0, v[156:157]
	s_and_b64 vcc, exec, s[0:1]
	s_mov_b32 s39, s18
	s_mov_b32 s40, s24
	s_mov_b64 s[34:35], s[28:29]
	s_mov_b64 s[30:31], s[26:27]
	s_waitcnt vmcnt(0)
	v_pk_fma_f32 v[146:147], v[146:147], v[88:89], v[166:167]
	v_pk_fma_f32 v[144:145], v[144:145], v[86:87], v[164:165]
	v_pk_fma_f32 v[142:143], v[142:143], v[84:85], v[170:171]
	v_pk_fma_f32 v[134:135], v[134:135], v[72:73], v[178:179]
	v_pk_fma_f32 v[132:133], v[132:133], v[70:71], v[176:177]
	global_store_dwordx4 v[196:197], v[132:135], off offset:576
	v_pk_fma_f32 v[140:141], v[140:141], v[82:83], v[168:169]
	v_pk_fma_f32 v[138:139], v[138:139], v[80:81], v[174:175]
	v_add_u32_e32 v132, 0x110, v154
	v_ashrrev_i32_e32 v133, 31, v132
	v_lshlrev_b64 v[132:133], 13, v[132:133]
	v_lshl_add_u64 v[132:133], s[76:77], 0, v[132:133]
	v_lshl_add_u64 v[132:133], v[132:133], 0, v[156:157]
	v_pk_fma_f32 v[118:119], v[118:119], v[72:73], v[194:195]
	v_pk_fma_f32 v[116:117], v[116:117], v[70:71], v[192:193]
	global_store_dwordx4 v[132:133], v[116:119], off offset:576
	v_pk_fma_f32 v[136:137], v[136:137], v[78:79], v[172:173]
	v_pk_fma_f32 v[130:131], v[130:131], v[88:89], v[182:183]
	v_or_b32_e32 v116, 32, v154
	v_ashrrev_i32_e32 v117, 31, v116
	v_pk_fma_f32 v[128:129], v[128:129], v[86:87], v[180:181]
	v_pk_fma_f32 v[126:127], v[126:127], v[84:85], v[186:187]
	v_pk_fma_f32 v[124:125], v[124:125], v[82:83], v[184:185]
	v_pk_fma_f32 v[122:123], v[122:123], v[80:81], v[190:191]
	v_pk_fma_f32 v[120:121], v[120:121], v[78:79], v[188:189]
	v_lshlrev_b64 v[116:117], 13, v[116:117]
	global_store_dwordx4 v[196:197], v[144:147], off
	global_store_dwordx4 v[196:197], v[140:143], off offset:64
	global_store_dwordx4 v[196:197], v[136:139], off offset:512
	global_store_dwordx4 v[132:133], v[128:131], off
	global_store_dwordx4 v[132:133], v[124:127], off offset:64
	global_store_dwordx4 v[132:133], v[120:123], off offset:512
	v_lshl_add_u64 v[128:129], v[158:159], 0, v[116:117]
	global_load_dwordx4 v[116:119], v[128:129], off
	global_load_dwordx4 v[120:123], v[128:129], off offset:64
	global_load_dwordx4 v[124:127], v[128:129], off offset:512
	s_nop 0
	global_load_dwordx4 v[128:131], v[128:129], off offset:576
	v_or_b32_e32 v132, 48, v154
	v_ashrrev_i32_e32 v133, 31, v132
	v_lshlrev_b64 v[132:133], 13, v[132:133]
	v_lshl_add_u64 v[144:145], v[158:159], 0, v[132:133]
	global_load_dwordx4 v[132:135], v[144:145], off
	global_load_dwordx4 v[136:139], v[144:145], off offset:64
	global_load_dwordx4 v[140:143], v[144:145], off offset:512
	s_nop 0
	global_load_dwordx4 v[144:147], v[144:145], off offset:576
	v_add_u32_e32 v164, 0x120, v154
	v_ashrrev_i32_e32 v165, 31, v164
	v_lshlrev_b64 v[164:165], 13, v[164:165]
	v_lshl_add_u64 v[164:165], s[76:77], 0, v[164:165]
	v_lshl_add_u64 v[164:165], v[164:165], 0, v[156:157]
	s_waitcnt vmcnt(0)
	v_pk_fma_f32 v[114:115], v[114:115], v[88:89], v[118:119]
	v_pk_fma_f32 v[112:113], v[112:113], v[86:87], v[116:117]
	v_pk_fma_f32 v[110:111], v[110:111], v[84:85], v[122:123]
	v_pk_fma_f32 v[102:103], v[102:103], v[72:73], v[130:131]
	v_pk_fma_f32 v[100:101], v[100:101], v[70:71], v[128:129]
	global_store_dwordx4 v[164:165], v[100:103], off offset:576
	v_pk_fma_f32 v[108:109], v[108:109], v[82:83], v[120:121]
	v_pk_fma_f32 v[106:107], v[106:107], v[80:81], v[126:127]
	v_add_u32_e32 v100, 0x130, v154
	v_ashrrev_i32_e32 v101, 31, v100
	v_lshlrev_b64 v[100:101], 13, v[100:101]
	v_lshl_add_u64 v[100:101], s[76:77], 0, v[100:101]
	v_lshl_add_u64 v[100:101], v[100:101], 0, v[156:157]
	v_pk_fma_f32 v[68:69], v[68:69], v[72:73], v[146:147]
	v_pk_fma_f32 v[66:67], v[66:67], v[70:71], v[144:145]
	global_store_dwordx4 v[100:101], v[66:69], off offset:576
	v_pk_fma_f32 v[104:105], v[104:105], v[78:79], v[124:125]
	v_pk_fma_f32 v[96:97], v[96:97], v[88:89], v[134:135]
	v_add_u32_e32 v66, 0x80, v154
	v_ashrrev_i32_e32 v67, 31, v66
	v_pk_fma_f32 v[94:95], v[94:95], v[86:87], v[132:133]
	v_pk_fma_f32 v[92:93], v[92:93], v[84:85], v[138:139]
	v_pk_fma_f32 v[90:91], v[90:91], v[82:83], v[136:137]
	v_pk_fma_f32 v[76:77], v[76:77], v[80:81], v[142:143]
	v_pk_fma_f32 v[74:75], v[74:75], v[78:79], v[140:141]
	v_lshlrev_b64 v[66:67], 13, v[66:67]
	global_store_dwordx4 v[164:165], v[112:115], off
	global_store_dwordx4 v[164:165], v[108:111], off offset:64
	global_store_dwordx4 v[164:165], v[104:107], off offset:512
	global_store_dwordx4 v[100:101], v[94:97], off
	global_store_dwordx4 v[100:101], v[90:93], off offset:64
	global_store_dwordx4 v[100:101], v[74:77], off offset:512
	v_lshl_add_u64 v[94:95], v[158:159], 0, v[66:67]
	global_load_dwordx4 v[66:69], v[94:95], off
	global_load_dwordx4 v[74:77], v[94:95], off offset:64
	global_load_dwordx4 v[90:93], v[94:95], off offset:512
	s_nop 0
	global_load_dwordx4 v[94:97], v[94:95], off offset:576
	v_add_u32_e32 v100, 0x90, v154
	v_ashrrev_i32_e32 v101, 31, v100
	v_lshlrev_b64 v[100:101], 13, v[100:101]
	v_lshl_add_u64 v[112:113], v[158:159], 0, v[100:101]
	global_load_dwordx4 v[100:103], v[112:113], off
	global_load_dwordx4 v[104:107], v[112:113], off offset:64
	global_load_dwordx4 v[108:111], v[112:113], off offset:512
	s_nop 0
	global_load_dwordx4 v[112:115], v[112:113], off offset:576
	v_add_u32_e32 v116, 0x180, v154
	v_ashrrev_i32_e32 v117, 31, v116
	v_lshlrev_b64 v[116:117], 13, v[116:117]
	v_lshl_add_u64 v[116:117], s[76:77], 0, v[116:117]
	v_lshl_add_u64 v[116:117], v[116:117], 0, v[156:157]
	s_waitcnt vmcnt(0)
	v_pk_fma_f32 v[64:65], v[64:65], v[88:89], v[68:69]
	v_pk_fma_f32 v[62:63], v[62:63], v[86:87], v[66:67]
	v_pk_fma_f32 v[60:61], v[60:61], v[84:85], v[76:77]
	v_pk_fma_f32 v[52:53], v[52:53], v[72:73], v[96:97]
	v_pk_fma_f32 v[50:51], v[50:51], v[70:71], v[94:95]
	global_store_dwordx4 v[116:117], v[50:53], off offset:576
	v_pk_fma_f32 v[58:59], v[58:59], v[82:83], v[74:75]
	v_pk_fma_f32 v[56:57], v[56:57], v[80:81], v[92:93]
	v_add_u32_e32 v50, 0x190, v154
	v_ashrrev_i32_e32 v51, 31, v50
	v_lshlrev_b64 v[50:51], 13, v[50:51]
	v_lshl_add_u64 v[50:51], s[76:77], 0, v[50:51]
	v_lshl_add_u64 v[50:51], v[50:51], 0, v[156:157]
	v_pk_fma_f32 v[36:37], v[36:37], v[72:73], v[114:115]
	v_pk_fma_f32 v[34:35], v[34:35], v[70:71], v[112:113]
	global_store_dwordx4 v[50:51], v[34:37], off offset:576
	v_pk_fma_f32 v[54:55], v[54:55], v[78:79], v[90:91]
	v_pk_fma_f32 v[48:49], v[48:49], v[88:89], v[102:103]
	v_add_u32_e32 v34, 0xa0, v154
	v_ashrrev_i32_e32 v35, 31, v34
	v_pk_fma_f32 v[46:47], v[46:47], v[86:87], v[100:101]
	v_pk_fma_f32 v[44:45], v[44:45], v[84:85], v[106:107]
	v_pk_fma_f32 v[42:43], v[42:43], v[82:83], v[104:105]
	v_pk_fma_f32 v[40:41], v[40:41], v[80:81], v[110:111]
	v_pk_fma_f32 v[38:39], v[38:39], v[78:79], v[108:109]
	v_lshlrev_b64 v[34:35], 13, v[34:35]
	global_store_dwordx4 v[116:117], v[62:65], off
	global_store_dwordx4 v[116:117], v[58:61], off offset:64
	global_store_dwordx4 v[116:117], v[54:57], off offset:512
	global_store_dwordx4 v[50:51], v[46:49], off
	global_store_dwordx4 v[50:51], v[42:45], off offset:64
	global_store_dwordx4 v[50:51], v[38:41], off offset:512
	v_lshl_add_u64 v[46:47], v[158:159], 0, v[34:35]
	global_load_dwordx4 v[34:37], v[46:47], off
	global_load_dwordx4 v[38:41], v[46:47], off offset:64
	global_load_dwordx4 v[42:45], v[46:47], off offset:512
	s_nop 0
	global_load_dwordx4 v[46:49], v[46:47], off offset:576
	v_add_u32_e32 v50, 0xb0, v154
	v_ashrrev_i32_e32 v51, 31, v50
	v_lshlrev_b64 v[50:51], 13, v[50:51]
	v_lshl_add_u64 v[62:63], v[158:159], 0, v[50:51]
	global_load_dwordx4 v[50:53], v[62:63], off
	global_load_dwordx4 v[54:57], v[62:63], off offset:64
	global_load_dwordx4 v[58:61], v[62:63], off offset:512
	s_nop 0
	global_load_dwordx4 v[62:65], v[62:63], off offset:576
	v_add_u32_e32 v66, 0x1a0, v154
	v_ashrrev_i32_e32 v67, 31, v66
	v_lshlrev_b64 v[66:67], 13, v[66:67]
	v_lshl_add_u64 v[66:67], s[76:77], 0, v[66:67]
	v_lshl_add_u64 v[66:67], v[66:67], 0, v[156:157]
	s_waitcnt vmcnt(0)
	v_pk_fma_f32 v[32:33], v[32:33], v[88:89], v[36:37]
	v_pk_fma_f32 v[30:31], v[30:31], v[86:87], v[34:35]
	v_pk_fma_f32 v[16:17], v[16:17], v[80:81], v[44:45]
	v_pk_fma_f32 v[12:13], v[12:13], v[72:73], v[48:49]
	v_pk_fma_f32 v[10:11], v[10:11], v[70:71], v[46:47]
	global_store_dwordx4 v[66:67], v[10:13], off offset:576
	v_pk_fma_f32 v[14:15], v[14:15], v[78:79], v[42:43]
	global_store_dwordx4 v[66:67], v[14:17], off offset:512
	v_add_u32_e32 v10, 0x1b0, v154
	v_ashrrev_i32_e32 v11, 31, v10
	v_lshlrev_b64 v[10:11], 13, v[10:11]
	v_lshl_add_u64 v[10:11], s[76:77], 0, v[10:11]
	v_lshl_add_u64 v[14:15], v[10:11], 0, v[156:157]
	v_pk_fma_f32 v[12:13], v[24:25], v[88:89], v[52:53]
	v_pk_fma_f32 v[10:11], v[22:23], v[86:87], v[50:51]
	v_pk_fma_f32 v[28:29], v[28:29], v[84:85], v[40:41]
	v_pk_fma_f32 v[26:27], v[26:27], v[82:83], v[38:39]
	global_store_dwordx4 v[14:15], v[10:13], off
	v_pk_fma_f32 v[8:9], v[8:9], v[80:81], v[60:61]
	v_pk_fma_f32 v[6:7], v[6:7], v[78:79], v[58:59]
	v_pk_fma_f32 v[12:13], v[20:21], v[84:85], v[56:57]
	v_pk_fma_f32 v[10:11], v[18:19], v[82:83], v[54:55]
	v_pk_fma_f32 v[4:5], v[4:5], v[72:73], v[64:65]
	v_pk_fma_f32 v[2:3], v[2:3], v[70:71], v[62:63]
	global_store_dwordx4 v[66:67], v[30:33], off
	global_store_dwordx4 v[66:67], v[26:29], off offset:64
	global_store_dwordx4 v[14:15], v[10:13], off offset:64
	global_store_dwordx4 v[14:15], v[6:9], off offset:512
	global_store_dwordx4 v[14:15], v[2:5], off offset:576
	s_cbranch_vccz .LBB0_1585
	s_waitcnt vmcnt(0)
	s_cmpk_gt_u32 s3, 0xff
	v_readlane_b32 s33, v255, 42
	s_cbranch_scc1 .LBB0_1596
	s_barrier

.LBB0_1616:
	s_add_i32 s50, s42, 2
	s_add_u32 s43, s40, 0xfff80080
	s_addc_u32 s44, s41, -1
	s_add_i32 s51, 0, 0x10000
	v_add_u32_e32 v144, s51, v1
	ds_read_b128 v[132:135], v144
	ds_read_b128 v[136:139], v144 offset:1024
	ds_read_b128 v[140:143], v144 offset:2048
	ds_read_b128 v[144:147], v144 offset:3072
	s_cmp_eq_u32 s47, s42
	s_cselect_b32 s42, s39, s48
	s_cselect_b32 s45, s1, s44
	s_cselect_b32 s44, s27, s43
	s_cselect_b32 s43, s25, s49
	v_lshl_add_u64 v[166:167], s[40:41], 0, v[154:155]
	s_add_i32 m0, s5, 0xc000
	ds_read_b128 v[158:161], v168
	ds_read_b128 v[162:165], v168 offset:1024
	ds_read_b128 v[170:173], v168 offset:2048
	ds_read_b128 v[174:177], v168 offset:3072
	ds_read_b128 v[178:181], v168 offset:4096
	ds_read_b128 v[182:185], v168 offset:5120
	ds_read_b128 v[186:189], v168 offset:6144
	ds_read_b128 v[190:193], v168 offset:7168
	global_load_lds_dwordx4 v[166:167], off
	v_lshl_add_u64 v[166:167], s[40:41], 0, v[156:157]
	s_add_i32 m0, s5, 0xe000
	s_nop 0
	global_load_lds_dwordx4 v[166:167], off
	s_waitcnt lgkmcnt(8)
	s_barrier
	s_waitcnt lgkmcnt(0)
	s_waitcnt lgkmcnt(0)
	v_mfma_f32_16x16x32_bf16 v[128:131], v[132:135], v[158:161], v[128:131]
	v_mfma_f32_16x16x32_bf16 v[124:127], v[140:143], v[158:161], v[124:127]
	v_mfma_f32_16x16x32_bf16 v[120:123], v[132:135], v[170:173], v[120:123]
	v_mfma_f32_16x16x32_bf16 v[116:119], v[140:143], v[170:173], v[116:119]
	v_mfma_f32_16x16x32_bf16 v[108:111], v[132:135], v[178:181], v[108:111]
	v_mfma_f32_16x16x32_bf16 v[100:103], v[140:143], v[178:181], v[100:103]
	v_mfma_f32_16x16x32_bf16 v[90:93], v[132:135], v[186:189], v[90:93]
	v_mfma_f32_16x16x32_bf16 v[82:85], v[140:143], v[186:189], v[82:85]
	v_mfma_f32_16x16x32_bf16 v[128:131], v[136:139], v[162:165], v[128:131]
	v_mfma_f32_16x16x32_bf16 v[124:127], v[144:147], v[162:165], v[124:127]
	v_mfma_f32_16x16x32_bf16 v[120:123], v[136:139], v[174:177], v[120:123]
	v_mfma_f32_16x16x32_bf16 v[116:119], v[144:147], v[174:177], v[116:119]
	v_mfma_f32_16x16x32_bf16 v[108:111], v[136:139], v[182:185], v[108:111]
	v_mfma_f32_16x16x32_bf16 v[100:103], v[144:147], v[182:185], v[100:103]
	v_mfma_f32_16x16x32_bf16 v[90:93], v[136:139], v[190:193], v[90:93]
	v_mfma_f32_16x16x32_bf16 v[82:85], v[144:147], v[190:193], v[82:85]
	s_barrier
	s_add_i32 s64, 0, 0x14000
	v_add_u32_e32 v166, s64, v1
	s_add_i32 s51, s51, s4
	ds_read_b128 v[194:197], v166
	ds_read_b128 v[198:201], v166 offset:1024
	ds_read_b128 v[202:205], v166 offset:2048
	ds_read_b128 v[206:209], v166 offset:3072
	v_lshl_add_u64 v[166:167], s[42:43], 0, v[98:99]
	s_mov_b32 m0, s51
	v_lshl_add_u64 v[210:211], s[42:43], 0, v[148:149]
	global_load_lds_dwordx4 v[166:167], off
	s_add_i32 m0, s51, 0x2000
	s_nop 0
	global_load_lds_dwordx4 v[210:211], off
	s_barrier
	s_waitcnt lgkmcnt(0)
	s_waitcnt lgkmcnt(0)
	v_mfma_f32_16x16x32_bf16 v[112:115], v[194:197], v[158:161], v[112:115]
	v_mfma_f32_16x16x32_bf16 v[104:107], v[202:205], v[158:161], v[104:107]
	v_mfma_f32_16x16x32_bf16 v[94:97], v[194:197], v[170:173], v[94:97]
	v_mfma_f32_16x16x32_bf16 v[86:89], v[202:205], v[170:173], v[86:89]
	v_mfma_f32_16x16x32_bf16 v[78:81], v[194:197], v[178:181], v[78:81]
	v_mfma_f32_16x16x32_bf16 v[74:77], v[202:205], v[178:181], v[74:77]
	v_mfma_f32_16x16x32_bf16 v[70:73], v[194:197], v[186:189], v[70:73]
	v_mfma_f32_16x16x32_bf16 v[66:69], v[202:205], v[186:189], v[66:69]
	v_mfma_f32_16x16x32_bf16 v[112:115], v[198:201], v[162:165], v[112:115]
	v_mfma_f32_16x16x32_bf16 v[104:107], v[206:209], v[162:165], v[104:107]
	v_mfma_f32_16x16x32_bf16 v[94:97], v[198:201], v[174:177], v[94:97]
	v_mfma_f32_16x16x32_bf16 v[86:89], v[206:209], v[174:177], v[86:89]
	v_mfma_f32_16x16x32_bf16 v[78:81], v[198:201], v[182:185], v[78:81]
	v_mfma_f32_16x16x32_bf16 v[74:77], v[206:209], v[182:185], v[74:77]
	v_mfma_f32_16x16x32_bf16 v[70:73], v[198:201], v[190:193], v[70:73]
	v_mfma_f32_16x16x32_bf16 v[66:69], v[206:209], v[190:193], v[66:69]
	s_mov_b32 m0, s5
	v_lshl_add_u64 v[212:213], s[44:45], 0, v[98:99]
	s_barrier
	ds_read_b128 v[158:161], v168 offset:16384
	ds_read_b128 v[162:165], v168 offset:17408
	ds_read_b128 v[170:173], v168 offset:18432
	ds_read_b128 v[174:177], v168 offset:19456
	ds_read_b128 v[178:181], v168 offset:20480
	ds_read_b128 v[182:185], v168 offset:21504
	ds_read_b128 v[186:189], v168 offset:22528
	ds_read_b128 v[190:193], v168 offset:23552
	global_load_lds_dwordx4 v[212:213], off
	v_lshl_add_u64 v[214:215], s[44:45], 0, v[148:149]
	s_mov_b32 m0, s8
	s_nop 0
	global_load_lds_dwordx4 v[214:215], off
	s_barrier
	s_waitcnt lgkmcnt(0)
	s_waitcnt lgkmcnt(0)
	v_mfma_f32_16x16x32_bf16 v[62:65], v[132:135], v[158:161], v[62:65]
	v_mfma_f32_16x16x32_bf16 v[58:61], v[140:143], v[158:161], v[58:61]
	v_mfma_f32_16x16x32_bf16 v[54:57], v[132:135], v[170:173], v[54:57]
	v_mfma_f32_16x16x32_bf16 v[50:53], v[140:143], v[170:173], v[50:53]
	v_mfma_f32_16x16x32_bf16 v[42:45], v[132:135], v[178:181], v[42:45]
	v_mfma_f32_16x16x32_bf16 v[34:37], v[140:143], v[178:181], v[34:37]
	v_mfma_f32_16x16x32_bf16 v[26:29], v[132:135], v[186:189], v[26:29]
	v_mfma_f32_16x16x32_bf16 v[18:21], v[140:143], v[186:189], v[18:21]
	v_mfma_f32_16x16x32_bf16 v[62:65], v[136:139], v[162:165], v[62:65]
	v_mfma_f32_16x16x32_bf16 v[58:61], v[144:147], v[162:165], v[58:61]
	v_mfma_f32_16x16x32_bf16 v[54:57], v[136:139], v[174:177], v[54:57]
	v_mfma_f32_16x16x32_bf16 v[50:53], v[144:147], v[174:177], v[50:53]
	v_mfma_f32_16x16x32_bf16 v[42:45], v[136:139], v[182:185], v[42:45]
	v_mfma_f32_16x16x32_bf16 v[34:37], v[144:147], v[182:185], v[34:37]
	v_mfma_f32_16x16x32_bf16 v[26:29], v[136:139], v[190:193], v[26:29]
	v_mfma_f32_16x16x32_bf16 v[18:21], v[144:147], v[190:193], v[18:21]
	s_barrier
	s_add_u32 s52, s42, 0x80000
	s_addc_u32 s53, s43, 0
	s_add_i32 s51, s64, s4
	v_lshl_add_u64 v[132:133], s[52:53], 0, v[98:99]
	s_mov_b32 m0, s51
	s_nop 0
	global_load_lds_dwordx4 v[132:133], off
	v_lshl_add_u64 v[132:133], s[52:53], 0, v[148:149]
	s_add_i32 m0, s51, 0x2000
	s_nop 0
	global_load_lds_dwordx4 v[132:133], off
	s_waitcnt vmcnt(6)
	s_barrier
	v_mfma_f32_16x16x32_bf16 v[46:49], v[194:197], v[158:161], v[46:49]
	v_mfma_f32_16x16x32_bf16 v[38:41], v[202:205], v[158:161], v[38:41]
	v_mfma_f32_16x16x32_bf16 v[30:33], v[194:197], v[170:173], v[30:33]
	v_mfma_f32_16x16x32_bf16 v[22:25], v[202:205], v[170:173], v[22:25]
	v_mfma_f32_16x16x32_bf16 v[14:17], v[194:197], v[178:181], v[14:17]
	v_mfma_f32_16x16x32_bf16 v[10:13], v[202:205], v[178:181], v[10:13]
	v_mfma_f32_16x16x32_bf16 v[6:9], v[194:197], v[186:189], v[6:9]
	v_mfma_f32_16x16x32_bf16 v[2:5], v[202:205], v[186:189], v[2:5]
	v_mfma_f32_16x16x32_bf16 v[46:49], v[198:201], v[162:165], v[46:49]
	v_mfma_f32_16x16x32_bf16 v[38:41], v[206:209], v[162:165], v[38:41]
	v_mfma_f32_16x16x32_bf16 v[30:33], v[198:201], v[174:177], v[30:33]
	v_mfma_f32_16x16x32_bf16 v[22:25], v[206:209], v[174:177], v[22:25]
	v_mfma_f32_16x16x32_bf16 v[14:17], v[198:201], v[182:185], v[14:17]
	v_mfma_f32_16x16x32_bf16 v[10:13], v[206:209], v[182:185], v[10:13]
	v_mfma_f32_16x16x32_bf16 v[6:9], v[198:201], v[190:193], v[6:9]
	v_mfma_f32_16x16x32_bf16 v[2:5], v[206:209], v[190:193], v[2:5]
	s_add_i32 s51, 0, 0x18000
	v_add_u32_e32 v144, s51, v1
	s_barrier
	ds_read_b128 v[132:135], v144
	ds_read_b128 v[136:139], v144 offset:1024
	ds_read_b128 v[140:143], v144 offset:2048
	ds_read_b128 v[144:147], v144 offset:3072
	s_add_u32 s44, s44, 0x80000
	s_addc_u32 s45, s45, 0
	s_mov_b32 m0, s9
	v_lshl_add_u64 v[194:195], s[44:45], 0, v[98:99]
	ds_read_b128 v[158:161], v168 offset:32768
	ds_read_b128 v[162:165], v168 offset:33792
	ds_read_b128 v[170:173], v168 offset:34816
	ds_read_b128 v[174:177], v168 offset:35840
	ds_read_b128 v[178:181], v168 offset:36864
	ds_read_b128 v[182:185], v168 offset:37888
	ds_read_b128 v[186:189], v168 offset:38912
	ds_read_b128 v[190:193], v168 offset:39936
	global_load_lds_dwordx4 v[194:195], off
	v_lshl_add_u64 v[194:195], s[44:45], 0, v[148:149]
	s_mov_b32 m0, s18
	s_nop 0
	global_load_lds_dwordx4 v[194:195], off
	s_waitcnt lgkmcnt(8)
	s_barrier
	s_waitcnt lgkmcnt(0)
	s_waitcnt lgkmcnt(0)
	v_mfma_f32_16x16x32_bf16 v[128:131], v[132:135], v[158:161], v[128:131]
	v_mfma_f32_16x16x32_bf16 v[124:127], v[140:143], v[158:161], v[124:127]
	v_mfma_f32_16x16x32_bf16 v[120:123], v[132:135], v[170:173], v[120:123]
	v_mfma_f32_16x16x32_bf16 v[116:119], v[140:143], v[170:173], v[116:119]
	v_mfma_f32_16x16x32_bf16 v[108:111], v[132:135], v[178:181], v[108:111]
	v_mfma_f32_16x16x32_bf16 v[100:103], v[140:143], v[178:181], v[100:103]
	v_mfma_f32_16x16x32_bf16 v[90:93], v[132:135], v[186:189], v[90:93]
	v_mfma_f32_16x16x32_bf16 v[82:85], v[140:143], v[186:189], v[82:85]
	v_mfma_f32_16x16x32_bf16 v[128:131], v[136:139], v[162:165], v[128:131]
	v_mfma_f32_16x16x32_bf16 v[124:127], v[144:147], v[162:165], v[124:127]
	v_mfma_f32_16x16x32_bf16 v[120:123], v[136:139], v[174:177], v[120:123]
	v_mfma_f32_16x16x32_bf16 v[116:119], v[144:147], v[174:177], v[116:119]
	v_mfma_f32_16x16x32_bf16 v[108:111], v[136:139], v[182:185], v[108:111]
	v_mfma_f32_16x16x32_bf16 v[100:103], v[144:147], v[182:185], v[100:103]
	v_mfma_f32_16x16x32_bf16 v[90:93], v[136:139], v[190:193], v[90:93]
	v_mfma_f32_16x16x32_bf16 v[82:85], v[144:147], v[190:193], v[82:85]
	s_barrier
	s_add_i32 s44, 0, 0x1c000
	s_add_i32 s45, s51, s4
	v_add_u32_e32 v169, s44, v1
	v_lshl_add_u64 v[166:167], v[166:167], 0, s[68:69]
	s_mov_b32 m0, s45
	ds_read_b128 v[194:197], v169
	ds_read_b128 v[198:201], v169 offset:1024
	ds_read_b128 v[202:205], v169 offset:2048
	ds_read_b128 v[206:209], v169 offset:3072
	global_load_lds_dwordx4 v[166:167], off
	v_lshl_add_u64 v[166:167], v[210:211], 0, s[68:69]
	s_add_i32 m0, s45, 0x2000
	s_nop 0
	global_load_lds_dwordx4 v[166:167], off
	s_barrier
	s_waitcnt lgkmcnt(0)
	s_waitcnt lgkmcnt(0)
	v_mfma_f32_16x16x32_bf16 v[112:115], v[194:197], v[158:161], v[112:115]
	v_mfma_f32_16x16x32_bf16 v[104:107], v[202:205], v[158:161], v[104:107]
	v_mfma_f32_16x16x32_bf16 v[94:97], v[194:197], v[170:173], v[94:97]
	v_mfma_f32_16x16x32_bf16 v[86:89], v[202:205], v[170:173], v[86:89]
	v_mfma_f32_16x16x32_bf16 v[78:81], v[194:197], v[178:181], v[78:81]
	v_mfma_f32_16x16x32_bf16 v[74:77], v[202:205], v[178:181], v[74:77]
	v_mfma_f32_16x16x32_bf16 v[70:73], v[194:197], v[186:189], v[70:73]
	v_mfma_f32_16x16x32_bf16 v[66:69], v[202:205], v[186:189], v[66:69]
	v_mfma_f32_16x16x32_bf16 v[112:115], v[198:201], v[162:165], v[112:115]
	v_mfma_f32_16x16x32_bf16 v[104:107], v[206:209], v[162:165], v[104:107]
	v_mfma_f32_16x16x32_bf16 v[94:97], v[198:201], v[174:177], v[94:97]
	v_mfma_f32_16x16x32_bf16 v[86:89], v[206:209], v[174:177], v[86:89]
	v_mfma_f32_16x16x32_bf16 v[78:81], v[198:201], v[182:185], v[78:81]
	v_mfma_f32_16x16x32_bf16 v[74:77], v[206:209], v[182:185], v[74:77]
	v_mfma_f32_16x16x32_bf16 v[70:73], v[198:201], v[190:193], v[70:73]
	v_mfma_f32_16x16x32_bf16 v[66:69], v[206:209], v[190:193], v[66:69]
	s_mov_b32 m0, s19
	v_lshl_add_u64 v[166:167], v[212:213], 0, s[68:69]
	s_barrier
	ds_read_b128 v[158:161], v168 offset:49152
	ds_read_b128 v[162:165], v168 offset:50176
	ds_read_b128 v[170:173], v168 offset:51200
	ds_read_b128 v[174:177], v168 offset:52224
	ds_read_b128 v[178:181], v168 offset:53248
	ds_read_b128 v[182:185], v168 offset:54272
	ds_read_b128 v[186:189], v168 offset:55296
	ds_read_b128 v[190:193], v168 offset:56320
	global_load_lds_dwordx4 v[166:167], off
	v_lshl_add_u64 v[166:167], v[214:215], 0, s[68:69]
	s_mov_b32 m0, s20
	s_nop 0
	global_load_lds_dwordx4 v[166:167], off
	s_barrier
	s_waitcnt lgkmcnt(0)
	s_waitcnt lgkmcnt(0)
	v_mfma_f32_16x16x32_bf16 v[62:65], v[132:135], v[158:161], v[62:65]
	v_mfma_f32_16x16x32_bf16 v[58:61], v[140:143], v[158:161], v[58:61]
	v_mfma_f32_16x16x32_bf16 v[54:57], v[132:135], v[170:173], v[54:57]
	v_mfma_f32_16x16x32_bf16 v[50:53], v[140:143], v[170:173], v[50:53]
	v_mfma_f32_16x16x32_bf16 v[42:45], v[132:135], v[178:181], v[42:45]
	v_mfma_f32_16x16x32_bf16 v[34:37], v[140:143], v[178:181], v[34:37]
	v_mfma_f32_16x16x32_bf16 v[26:29], v[132:135], v[186:189], v[26:29]
	v_mfma_f32_16x16x32_bf16 v[18:21], v[140:143], v[186:189], v[18:21]
	v_mfma_f32_16x16x32_bf16 v[62:65], v[136:139], v[162:165], v[62:65]
	v_mfma_f32_16x16x32_bf16 v[58:61], v[144:147], v[162:165], v[58:61]
	v_mfma_f32_16x16x32_bf16 v[54:57], v[136:139], v[174:177], v[54:57]
	v_mfma_f32_16x16x32_bf16 v[50:53], v[144:147], v[174:177], v[50:53]
	v_mfma_f32_16x16x32_bf16 v[42:45], v[136:139], v[182:185], v[42:45]
	v_mfma_f32_16x16x32_bf16 v[34:37], v[144:147], v[182:185], v[34:37]
	v_mfma_f32_16x16x32_bf16 v[26:29], v[136:139], v[190:193], v[26:29]
	v_mfma_f32_16x16x32_bf16 v[18:21], v[144:147], v[190:193], v[18:21]
	s_barrier
	s_add_u32 s42, s42, 0x80080
	s_addc_u32 s43, s43, 0
	s_add_i32 s44, s44, s4
	v_lshl_add_u64 v[132:133], s[42:43], 0, v[98:99]
	s_mov_b32 m0, s44
	s_nop 0
	global_load_lds_dwordx4 v[132:133], off
	v_lshl_add_u64 v[132:133], s[42:43], 0, v[148:149]
	s_add_i32 m0, s44, 0x2000
	s_nop 0
	global_load_lds_dwordx4 v[132:133], off
	s_waitcnt vmcnt(6)
	s_barrier
	v_mfma_f32_16x16x32_bf16 v[46:49], v[194:197], v[158:161], v[46:49]
	v_mfma_f32_16x16x32_bf16 v[38:41], v[202:205], v[158:161], v[38:41]
	v_mfma_f32_16x16x32_bf16 v[30:33], v[194:197], v[170:173], v[30:33]
	v_mfma_f32_16x16x32_bf16 v[22:25], v[202:205], v[170:173], v[22:25]
	v_mfma_f32_16x16x32_bf16 v[14:17], v[194:197], v[178:181], v[14:17]
	v_mfma_f32_16x16x32_bf16 v[10:13], v[202:205], v[178:181], v[10:13]
	v_mfma_f32_16x16x32_bf16 v[6:9], v[194:197], v[186:189], v[6:9]
	v_mfma_f32_16x16x32_bf16 v[2:5], v[202:205], v[186:189], v[2:5]
	v_mfma_f32_16x16x32_bf16 v[46:49], v[198:201], v[162:165], v[46:49]
	v_mfma_f32_16x16x32_bf16 v[38:41], v[206:209], v[162:165], v[38:41]
	v_mfma_f32_16x16x32_bf16 v[30:33], v[198:201], v[174:177], v[30:33]
	v_mfma_f32_16x16x32_bf16 v[22:25], v[206:209], v[174:177], v[22:25]
	v_mfma_f32_16x16x32_bf16 v[14:17], v[198:201], v[182:185], v[14:17]
	v_mfma_f32_16x16x32_bf16 v[10:13], v[206:209], v[182:185], v[10:13]
	v_mfma_f32_16x16x32_bf16 v[6:9], v[198:201], v[190:193], v[6:9]
	v_mfma_f32_16x16x32_bf16 v[2:5], v[206:209], v[190:193], v[2:5]
	s_add_u32 s40, s40, 0x100
	s_addc_u32 s41, s41, 0
	s_add_u32 s48, s48, 0x100
	s_addc_u32 s49, s49, 0
	s_cmp_ge_i32 s50, s46
	s_mov_b32 s42, s50
	s_barrier
	s_cbranch_scc0 .LBB0_1616
	v_lshl_or_b32 v158, s38, 8, v151
	v_ashrrev_i32_e32 v159, 31, v158
	s_cmp_lt_i32 s62, 0
	s_mov_b64 s[38:39], -1
	s_cbranch_scc0 .LBB0_1619
	v_lshl_add_u32 v162, s36, 8, v150
	v_add_u32_e32 v160, 0xffffff00, v162
	v_readlane_b32 s40, v251, 9
	v_lshlrev_b64 v[166:167], 2, v[158:159]
	v_readlane_b32 s41, v251, 10
	v_ashrrev_i32_e32 v161, 31, v160
	v_lshlrev_b64 v[160:161], 13, v[160:161]
	v_lshl_add_u64 v[164:165], s[40:41], 0, v[166:167]
	v_lshl_add_u64 v[132:133], s[22:23], 0, v[166:167]
	v_lshl_add_u64 v[160:161], v[164:165], 0, v[160:161]
	global_load_dwordx4 v[144:147], v[132:133], off
	global_load_dwordx4 v[140:143], v[132:133], off offset:64
	global_load_dwordx4 v[136:139], v[132:133], off offset:512
	s_nop 0
	global_load_dwordx4 v[132:135], v[132:133], off offset:576
	s_nop 0
	global_load_dwordx4 v[170:173], v[160:161], off
	global_load_dwordx4 v[174:177], v[160:161], off offset:64
	global_load_dwordx4 v[178:181], v[160:161], off offset:512
	global_load_dwordx4 v[182:185], v[160:161], off offset:576
	v_add_u32_e32 v160, 0xffffff10, v162
	v_ashrrev_i32_e32 v161, 31, v160
	v_lshlrev_b64 v[160:161], 13, v[160:161]
	v_lshl_add_u64 v[160:161], v[164:165], 0, v[160:161]
	global_load_dwordx4 v[186:189], v[160:161], off
	global_load_dwordx4 v[190:193], v[160:161], off offset:64
	global_load_dwordx4 v[194:197], v[160:161], off offset:512
	global_load_dwordx4 v[198:201], v[160:161], off offset:576
	v_ashrrev_i32_e32 v163, 31, v162
	v_lshlrev_b64 v[160:161], 13, v[162:163]
	v_lshl_add_u64 v[160:161], s[76:77], 0, v[160:161]
	v_lshl_add_u64 v[160:161], v[160:161], 0, v[166:167]
	v_or_b32_e32 v202, 32, v162
	v_ashrrev_i32_e32 v203, 31, v202
	v_lshlrev_b64 v[202:203], 13, v[202:203]
	v_lshl_add_u64 v[202:203], s[76:77], 0, v[202:203]
	v_lshl_add_u64 v[202:203], v[202:203], 0, v[166:167]
	s_mov_b32 s1, 0x100000
	s_mov_b64 s[38:39], 0x100000
	v_readlane_b32 s54, v251, 23
	v_readlane_b32 s55, v251, 24
	v_readlane_b32 s54, v255, 43
	v_readlane_b32 s42, v251, 11
	v_readlane_b32 s43, v251, 12
	v_readlane_b32 s44, v251, 13
	v_readlane_b32 s45, v251, 14
	v_readlane_b32 s46, v251, 15
	v_readlane_b32 s47, v251, 16
	v_readlane_b32 s48, v251, 17
	v_readlane_b32 s49, v251, 18
	v_readlane_b32 s50, v251, 19
	v_readlane_b32 s51, v251, 20
	v_readlane_b32 s52, v251, 21
	v_readlane_b32 s53, v251, 22
	v_readlane_b32 s55, v255, 44
	s_waitcnt vmcnt(0)
	v_pk_fma_f32 v[172:173], v[130:131], v[146:147], v[172:173]
	v_pk_fma_f32 v[170:171], v[128:129], v[144:145], v[170:171]
	global_store_dwordx4 v[160:161], v[170:173], off
	s_nop 1
	v_pk_fma_f32 v[172:173], v[126:127], v[142:143], v[176:177]
	v_pk_fma_f32 v[170:171], v[124:125], v[140:141], v[174:175]
	global_store_dwordx4 v[160:161], v[170:173], off offset:64
	s_nop 1
	v_pk_fma_f32 v[172:173], v[114:115], v[138:139], v[180:181]
	v_pk_fma_f32 v[170:171], v[112:113], v[136:137], v[178:179]
	global_store_dwordx4 v[160:161], v[170:173], off offset:512
	s_nop 1
	v_pk_fma_f32 v[172:173], v[106:107], v[134:135], v[184:185]
	v_pk_fma_f32 v[170:171], v[104:105], v[132:133], v[182:183]
	global_store_dwordx4 v[160:161], v[170:173], off offset:576
	s_nop 1
	v_or_b32_e32 v170, 16, v162
	v_ashrrev_i32_e32 v171, 31, v170
	v_lshlrev_b64 v[170:171], 13, v[170:171]
	v_lshl_add_u64 v[170:171], s[76:77], 0, v[170:171]
	v_lshl_add_u64 v[174:175], v[170:171], 0, v[166:167]
	v_pk_fma_f32 v[172:173], v[122:123], v[146:147], v[188:189]
	v_pk_fma_f32 v[170:171], v[120:121], v[144:145], v[186:187]
	global_store_dwordx4 v[174:175], v[170:173], off
	v_add_u32_e32 v186, 0xffffff30, v162
	v_ashrrev_i32_e32 v187, 31, v186
	v_pk_fma_f32 v[172:173], v[118:119], v[142:143], v[192:193]
	v_pk_fma_f32 v[170:171], v[116:117], v[140:141], v[190:191]
	global_store_dwordx4 v[174:175], v[170:173], off offset:64
	v_lshlrev_b64 v[186:187], 13, v[186:187]
	s_nop 0
	v_pk_fma_f32 v[172:173], v[96:97], v[138:139], v[196:197]
	v_pk_fma_f32 v[170:171], v[94:95], v[136:137], v[194:195]
	global_store_dwordx4 v[174:175], v[170:173], off offset:512
	s_nop 1
	v_pk_fma_f32 v[172:173], v[88:89], v[134:135], v[200:201]
	v_pk_fma_f32 v[170:171], v[86:87], v[132:133], v[198:199]
	global_store_dwordx4 v[174:175], v[170:173], off offset:576
	v_lshl_add_u64 v[198:199], v[164:165], 0, v[186:187]
	s_nop 0
	v_add_u32_e32 v170, 0xffffff20, v162
	v_ashrrev_i32_e32 v171, 31, v170
	v_lshlrev_b64 v[170:171], 13, v[170:171]
	v_lshl_add_u64 v[182:183], v[164:165], 0, v[170:171]
	global_load_dwordx4 v[170:173], v[182:183], off
	global_load_dwordx4 v[174:177], v[182:183], off offset:64
	global_load_dwordx4 v[178:181], v[182:183], off offset:512
	s_nop 0
	global_load_dwordx4 v[182:185], v[182:183], off offset:576
	s_nop 0
	global_load_dwordx4 v[186:189], v[198:199], off
	global_load_dwordx4 v[190:193], v[198:199], off offset:64
	global_load_dwordx4 v[194:197], v[198:199], off offset:512
	s_nop 0
	global_load_dwordx4 v[198:201], v[198:199], off offset:576
	s_waitcnt vmcnt(0)
	v_pk_fma_f32 v[172:173], v[110:111], v[146:147], v[172:173]
	v_pk_fma_f32 v[170:171], v[108:109], v[144:145], v[170:171]
	global_store_dwordx4 v[202:203], v[170:173], off
	s_nop 1
	v_pk_fma_f32 v[172:173], v[102:103], v[142:143], v[176:177]
	v_pk_fma_f32 v[170:171], v[100:101], v[140:141], v[174:175]
	global_store_dwordx4 v[202:203], v[170:173], off offset:64
	s_nop 1
	v_pk_fma_f32 v[172:173], v[80:81], v[138:139], v[180:181]
	v_pk_fma_f32 v[170:171], v[78:79], v[136:137], v[178:179]
	global_store_dwordx4 v[202:203], v[170:173], off offset:512
	s_nop 1
	v_pk_fma_f32 v[172:173], v[76:77], v[134:135], v[184:185]
	v_pk_fma_f32 v[170:171], v[74:75], v[132:133], v[182:183]
	global_store_dwordx4 v[202:203], v[170:173], off offset:576
	v_add_co_u32_e32 v202, vcc, s1, v160
	s_nop 0
	v_or_b32_e32 v170, 48, v162
	v_ashrrev_i32_e32 v171, 31, v170
	v_lshlrev_b64 v[170:171], 13, v[170:171]
	v_lshl_add_u64 v[170:171], s[76:77], 0, v[170:171]
	v_lshl_add_u64 v[166:167], v[170:171], 0, v[166:167]
	v_pk_fma_f32 v[172:173], v[92:93], v[146:147], v[188:189]
	v_pk_fma_f32 v[170:171], v[90:91], v[144:145], v[186:187]
	global_store_dwordx4 v[166:167], v[170:173], off
	v_addc_co_u32_e32 v203, vcc, 0, v161, vcc
	s_nop 0
	v_pk_fma_f32 v[172:173], v[84:85], v[142:143], v[192:193]
	v_pk_fma_f32 v[170:171], v[82:83], v[140:141], v[190:191]
	global_store_dwordx4 v[166:167], v[170:173], off offset:64
	s_mov_b32 s1, 0x120000
	s_nop 0
	v_pk_fma_f32 v[172:173], v[72:73], v[138:139], v[196:197]
	v_pk_fma_f32 v[170:171], v[70:71], v[136:137], v[194:195]
	global_store_dwordx4 v[166:167], v[170:173], off offset:512
	s_nop 1
	v_pk_fma_f32 v[172:173], v[68:69], v[134:135], v[200:201]
	v_pk_fma_f32 v[170:171], v[66:67], v[132:133], v[198:199]
	global_store_dwordx4 v[166:167], v[170:173], off offset:576
	v_add_u32_e32 v166, 0xffffff80, v162
	v_ashrrev_i32_e32 v167, 31, v166
	v_lshlrev_b64 v[166:167], 13, v[166:167]
	v_lshl_add_u64 v[166:167], v[164:165], 0, v[166:167]
	global_load_dwordx4 v[170:173], v[166:167], off
	global_load_dwordx4 v[174:177], v[166:167], off offset:64
	global_load_dwordx4 v[178:181], v[166:167], off offset:512
	global_load_dwordx4 v[182:185], v[166:167], off offset:576
	v_add_u32_e32 v166, 0xffffff90, v162
	v_ashrrev_i32_e32 v167, 31, v166
	v_lshlrev_b64 v[166:167], 13, v[166:167]
	v_lshl_add_u64 v[166:167], v[164:165], 0, v[166:167]
	global_load_dwordx4 v[186:189], v[166:167], off
	global_load_dwordx4 v[190:193], v[166:167], off offset:64
	global_load_dwordx4 v[194:197], v[166:167], off offset:512
	global_load_dwordx4 v[198:201], v[166:167], off offset:576
	v_lshl_add_u64 v[166:167], v[160:161], 0, s[38:39]
	s_mov_b64 s[38:39], 0x120000
	s_waitcnt vmcnt(0)
	v_pk_fma_f32 v[172:173], v[64:65], v[146:147], v[172:173]
	v_pk_fma_f32 v[170:171], v[62:63], v[144:145], v[170:171]
	global_store_dwordx4 v[202:203], v[170:173], off
	s_nop 1
	v_pk_fma_f32 v[172:173], v[60:61], v[142:143], v[176:177]
	v_pk_fma_f32 v[170:171], v[58:59], v[140:141], v[174:175]
	global_store_dwordx4 v[166:167], v[170:173], off offset:64
	v_add_co_u32_e32 v174, vcc, s1, v160
	s_nop 0
	v_pk_fma_f32 v[172:173], v[48:49], v[138:139], v[180:181]
	v_pk_fma_f32 v[170:171], v[46:47], v[136:137], v[178:179]
	global_store_dwordx4 v[166:167], v[170:173], off offset:512
	v_addc_co_u32_e32 v175, vcc, 0, v161, vcc
	s_nop 0
	v_pk_fma_f32 v[172:173], v[40:41], v[134:135], v[184:185]
	v_pk_fma_f32 v[170:171], v[38:39], v[132:133], v[182:183]
	global_store_dwordx4 v[166:167], v[170:173], off offset:576
	v_lshl_add_u64 v[166:167], v[160:161], 0, s[38:39]
	s_mov_b32 s1, 0x140000
	v_pk_fma_f32 v[172:173], v[56:57], v[146:147], v[188:189]
	v_pk_fma_f32 v[170:171], v[54:55], v[144:145], v[186:187]
	global_store_dwordx4 v[174:175], v[170:173], off
	s_mov_b64 s[38:39], 0x140000
	s_nop 0
	v_pk_fma_f32 v[172:173], v[52:53], v[142:143], v[192:193]
	v_pk_fma_f32 v[170:171], v[50:51], v[140:141], v[190:191]
	global_store_dwordx4 v[166:167], v[170:173], off offset:64
	s_nop 1
	v_pk_fma_f32 v[172:173], v[32:33], v[138:139], v[196:197]
	v_pk_fma_f32 v[170:171], v[30:31], v[136:137], v[194:195]
	global_store_dwordx4 v[166:167], v[170:173], off offset:512
	s_nop 1
	v_pk_fma_f32 v[172:173], v[24:25], v[134:135], v[200:201]
	v_pk_fma_f32 v[170:171], v[22:23], v[132:133], v[198:199]
	global_store_dwordx4 v[166:167], v[170:173], off offset:576
	v_add_u32_e32 v166, 0xffffffa0, v162
	v_ashrrev_i32_e32 v167, 31, v166
	v_lshlrev_b64 v[166:167], 13, v[166:167]
	v_add_u32_e32 v162, 0xffffffb0, v162
	v_lshl_add_u64 v[166:167], v[164:165], 0, v[166:167]
	v_ashrrev_i32_e32 v163, 31, v162
	global_load_dwordx4 v[170:173], v[166:167], off
	global_load_dwordx4 v[174:177], v[166:167], off offset:64
	global_load_dwordx4 v[178:181], v[166:167], off offset:512
	global_load_dwordx4 v[182:185], v[166:167], off offset:576
	v_lshlrev_b64 v[162:163], 13, v[162:163]
	v_lshl_add_u64 v[166:167], v[164:165], 0, v[162:163]
	global_load_dwordx4 v[162:165], v[166:167], off
	global_load_dwordx4 v[186:189], v[166:167], off offset:64
	global_load_dwordx4 v[190:193], v[166:167], off offset:512
	global_load_dwordx4 v[194:197], v[166:167], off offset:576
	v_add_co_u32_e32 v198, vcc, s1, v160
	v_lshl_add_u64 v[166:167], v[160:161], 0, s[38:39]
	s_nop 0
	v_addc_co_u32_e32 v199, vcc, 0, v161, vcc
	s_mov_b64 s[38:39], 0x160000
	s_mov_b32 s1, 0x160000
	s_waitcnt vmcnt(0)
	v_pk_fma_f32 v[172:173], v[44:45], v[146:147], v[172:173]
	v_pk_fma_f32 v[170:171], v[42:43], v[144:145], v[170:171]
	global_store_dwordx4 v[198:199], v[170:173], off
	v_pk_fma_f32 v[146:147], v[28:29], v[146:147], v[164:165]
	v_pk_fma_f32 v[144:145], v[26:27], v[144:145], v[162:163]
	v_pk_fma_f32 v[172:173], v[36:37], v[142:143], v[176:177]
	v_pk_fma_f32 v[170:171], v[34:35], v[140:141], v[174:175]
	global_store_dwordx4 v[166:167], v[170:173], off offset:64
	v_pk_fma_f32 v[142:143], v[20:21], v[142:143], v[188:189]
	v_pk_fma_f32 v[140:141], v[18:19], v[140:141], v[186:187]
	v_pk_fma_f32 v[172:173], v[16:17], v[138:139], v[180:181]
	v_pk_fma_f32 v[170:171], v[14:15], v[136:137], v[178:179]
	global_store_dwordx4 v[166:167], v[170:173], off offset:512
	v_pk_fma_f32 v[138:139], v[8:9], v[138:139], v[192:193]
	v_pk_fma_f32 v[136:137], v[6:7], v[136:137], v[190:191]
	v_pk_fma_f32 v[172:173], v[12:13], v[134:135], v[184:185]
	v_pk_fma_f32 v[170:171], v[10:11], v[132:133], v[182:183]
	global_store_dwordx4 v[166:167], v[170:173], off offset:576
	v_lshl_add_u64 v[166:167], v[160:161], 0, s[38:39]
	v_add_co_u32_e32 v160, vcc, s1, v160
	v_pk_fma_f32 v[134:135], v[4:5], v[134:135], v[196:197]
	s_nop 0
	v_addc_co_u32_e32 v161, vcc, 0, v161, vcc
	v_pk_fma_f32 v[132:133], v[2:3], v[132:133], v[194:195]
	global_store_dwordx4 v[160:161], v[144:147], off
	global_store_dwordx4 v[166:167], v[140:143], off offset:64
	global_store_dwordx4 v[166:167], v[136:139], off offset:512
	global_store_dwordx4 v[166:167], v[132:135], off offset:576
	s_mov_b64 s[38:39], 0

.LBB0_1870:
	s_add_u32 s36, s26, 0x100
	s_addc_u32 s37, s27, 0
	s_add_u32 s40, s31, s26
	s_addc_u32 s41, s20, s27
	s_cmpk_eq_i32 s26, 0x700
	s_cselect_b64 vcc, -1, 0
	s_and_b64 s[38:39], vcc, exec
	s_cselect_b32 s48, 0, s36
	s_cselect_b32 s45, 0, s37
	s_cselect_b32 s38, s24, s40
	s_cselect_b32 s39, s25, s41
	s_add_u32 s40, s94, s48
	s_addc_u32 s41, s95, s45
	s_add_i32 s45, 0, 0x10000
	v_add_u32_e32 v98, s45, v165
	ds_read_b128 v[148:151], v98
	ds_read_b128 v[154:157], v98 offset:1024
	ds_read_b128 v[176:179], v98 offset:2048
	ds_read_b128 v[182:185], v98 offset:3072
	v_lshl_add_u64 v[170:171], v[144:145], 0, s[26:27]
	s_add_i32 m0, s35, 0xc000
	ds_read_b128 v[186:189], v169
	ds_read_b128 v[190:193], v169 offset:1024
	ds_read_b128 v[194:197], v169 offset:2048
	ds_read_b128 v[198:201], v169 offset:3072
	ds_read_b128 v[202:205], v169 offset:4096
	ds_read_b128 v[206:209], v169 offset:5120
	ds_read_b128 v[210:213], v169 offset:6144
	ds_read_b128 v[214:217], v169 offset:7168
	global_load_lds_dwordx4 v[170:171], off
	v_lshl_add_u64 v[170:171], v[146:147], 0, s[26:27]
	s_add_i32 m0, s35, 0xe000
	s_nop 0
	global_load_lds_dwordx4 v[170:171], off
	s_waitcnt lgkmcnt(8)
	s_barrier
	s_waitcnt lgkmcnt(0)
	s_waitcnt lgkmcnt(0)
	v_mfma_i32_16x16x64_i8 v[128:131], v[148:151], v[186:189], v[128:131]
	v_mfma_i32_16x16x64_i8 v[120:123], v[176:179], v[186:189], v[120:123]
	v_mfma_i32_16x16x64_i8 v[112:115], v[148:151], v[194:197], v[112:115]
	v_mfma_i32_16x16x64_i8 v[108:111], v[176:179], v[194:197], v[108:111]
	v_mfma_i32_16x16x64_i8 v[94:97], v[148:151], v[202:205], v[94:97]
	v_mfma_i32_16x16x64_i8 v[90:93], v[176:179], v[202:205], v[90:93]
	v_mfma_i32_16x16x64_i8 v[78:81], v[148:151], v[210:213], v[78:81]
	v_mfma_i32_16x16x64_i8 v[74:77], v[176:179], v[210:213], v[74:77]
	v_mfma_i32_16x16x64_i8 v[128:131], v[154:157], v[190:193], v[128:131]
	v_mfma_i32_16x16x64_i8 v[120:123], v[182:185], v[190:193], v[120:123]
	v_mfma_i32_16x16x64_i8 v[112:115], v[154:157], v[198:201], v[112:115]
	v_mfma_i32_16x16x64_i8 v[108:111], v[182:185], v[198:201], v[108:111]
	v_mfma_i32_16x16x64_i8 v[94:97], v[154:157], v[206:209], v[94:97]
	v_mfma_i32_16x16x64_i8 v[90:93], v[182:185], v[206:209], v[90:93]
	v_mfma_i32_16x16x64_i8 v[78:81], v[154:157], v[214:217], v[78:81]
	v_mfma_i32_16x16x64_i8 v[74:77], v[182:185], v[214:217], v[74:77]
	s_barrier
	s_add_i32 s48, 0, 0x14000
	s_add_i32 s26, s45, s93
	v_add_u32_e32 v98, s48, v165
	v_lshl_add_u64 v[170:171], s[38:39], 0, v[132:133]
	s_mov_b32 m0, s26
	ds_read_b128 v[222:225], v98
	ds_read_b128 v[230:233], v98 offset:1024
	ds_read_b128 v[236:239], v98 offset:2048
	ds_read_b128 v[240:243], v98 offset:3072
	global_load_lds_dwordx4 v[170:171], off
	v_lshl_add_u64 v[218:219], s[38:39], 0, v[134:135]
	s_add_i32 m0, s26, 0x2000
	s_nop 0
	global_load_lds_dwordx4 v[218:219], off
	s_barrier
	s_waitcnt lgkmcnt(0)
	s_waitcnt lgkmcnt(0)
	v_mfma_i32_16x16x64_i8 v[124:127], v[222:225], v[186:189], v[124:127]
	v_mfma_i32_16x16x64_i8 v[116:119], v[236:239], v[186:189], v[116:119]
	v_mfma_i32_16x16x64_i8 v[104:107], v[222:225], v[194:197], v[104:107]
	v_mfma_i32_16x16x64_i8 v[100:103], v[236:239], v[194:197], v[100:103]
	v_mfma_i32_16x16x64_i8 v[86:89], v[222:225], v[202:205], v[86:89]
	v_mfma_i32_16x16x64_i8 v[82:85], v[236:239], v[202:205], v[82:85]
	v_mfma_i32_16x16x64_i8 v[70:73], v[222:225], v[210:213], v[70:73]
	v_mfma_i32_16x16x64_i8 v[66:69], v[236:239], v[210:213], v[66:69]
	v_mfma_i32_16x16x64_i8 v[124:127], v[230:233], v[190:193], v[124:127]
	v_mfma_i32_16x16x64_i8 v[116:119], v[240:243], v[190:193], v[116:119]
	v_mfma_i32_16x16x64_i8 v[104:107], v[230:233], v[198:201], v[104:107]
	v_mfma_i32_16x16x64_i8 v[100:103], v[240:243], v[198:201], v[100:103]
	v_mfma_i32_16x16x64_i8 v[86:89], v[230:233], v[206:209], v[86:89]
	v_mfma_i32_16x16x64_i8 v[82:85], v[240:243], v[206:209], v[82:85]
	v_mfma_i32_16x16x64_i8 v[70:73], v[230:233], v[214:217], v[70:73]
	v_mfma_i32_16x16x64_i8 v[66:69], v[240:243], v[214:217], v[66:69]
	s_mov_b32 m0, s35
	v_cndmask_b32_e32 v98, v136, v173, vcc
	s_barrier
	ds_read_b128 v[186:189], v169 offset:16384
	ds_read_b128 v[190:193], v169 offset:17408
	ds_read_b128 v[194:197], v169 offset:18432
	ds_read_b128 v[198:201], v169 offset:19456
	ds_read_b128 v[202:205], v169 offset:20480
	ds_read_b128 v[206:209], v169 offset:21504
	ds_read_b128 v[210:213], v169 offset:22528
	ds_read_b128 v[214:217], v169 offset:23552
	v_lshl_add_u64 v[244:245], s[40:41], 0, v[98:99]
	global_load_lds_dwordx4 v98, s[40:41]
	v_cndmask_b32_e32 v98, v138, v174, vcc
	s_mov_b32 m0, s18
	v_lshl_add_u64 v[246:247], s[40:41], 0, v[98:99]
	global_load_lds_dwordx4 v98, s[40:41]
	s_barrier
	s_waitcnt lgkmcnt(0)
	s_waitcnt lgkmcnt(0)
	v_mfma_i32_16x16x64_i8 v[62:65], v[148:151], v[186:189], v[62:65]
	v_mfma_i32_16x16x64_i8 v[58:61], v[176:179], v[186:189], v[58:61]
	v_mfma_i32_16x16x64_i8 v[46:49], v[148:151], v[194:197], v[46:49]
	v_mfma_i32_16x16x64_i8 v[42:45], v[176:179], v[194:197], v[42:45]
	v_mfma_i32_16x16x64_i8 v[30:33], v[148:151], v[202:205], v[30:33]
	v_mfma_i32_16x16x64_i8 v[26:29], v[176:179], v[202:205], v[26:29]
	v_mfma_i32_16x16x64_i8 v[14:17], v[148:151], v[210:213], v[14:17]
	v_mfma_i32_16x16x64_i8 v[10:13], v[176:179], v[210:213], v[10:13]
	v_mfma_i32_16x16x64_i8 v[62:65], v[154:157], v[190:193], v[62:65]
	v_mfma_i32_16x16x64_i8 v[58:61], v[182:185], v[190:193], v[58:61]
	v_mfma_i32_16x16x64_i8 v[46:49], v[154:157], v[198:201], v[46:49]
	v_mfma_i32_16x16x64_i8 v[42:45], v[182:185], v[198:201], v[42:45]
	v_mfma_i32_16x16x64_i8 v[30:33], v[154:157], v[206:209], v[30:33]
	v_mfma_i32_16x16x64_i8 v[26:29], v[182:185], v[206:209], v[26:29]
	v_mfma_i32_16x16x64_i8 v[14:17], v[154:157], v[214:217], v[14:17]
	v_mfma_i32_16x16x64_i8 v[10:13], v[182:185], v[214:217], v[10:13]
	s_barrier
	s_add_u32 s26, s38, 0x40000
	s_addc_u32 s27, s39, 0
	s_add_i32 s45, s48, s93
	v_lshl_add_u64 v[148:149], s[26:27], 0, v[132:133]
	s_mov_b32 m0, s45
	s_nop 0
	global_load_lds_dwordx4 v[148:149], off
	v_lshl_add_u64 v[148:149], s[26:27], 0, v[134:135]
	s_add_i32 m0, s45, 0x2000
	s_nop 0
	global_load_lds_dwordx4 v[148:149], off
	s_waitcnt vmcnt(6)
	s_barrier
	v_mfma_i32_16x16x64_i8 v[54:57], v[222:225], v[186:189], v[54:57]
	v_mfma_i32_16x16x64_i8 v[50:53], v[236:239], v[186:189], v[50:53]
	v_mfma_i32_16x16x64_i8 v[38:41], v[222:225], v[194:197], v[38:41]
	v_mfma_i32_16x16x64_i8 v[34:37], v[236:239], v[194:197], v[34:37]
	v_mfma_i32_16x16x64_i8 v[22:25], v[222:225], v[202:205], v[22:25]
	v_mfma_i32_16x16x64_i8 v[18:21], v[236:239], v[202:205], v[18:21]
	v_mfma_i32_16x16x64_i8 v[6:9], v[222:225], v[210:213], v[6:9]
	v_mfma_i32_16x16x64_i8 v[2:5], v[236:239], v[210:213], v[2:5]
	v_mfma_i32_16x16x64_i8 v[54:57], v[230:233], v[190:193], v[54:57]
	v_mfma_i32_16x16x64_i8 v[50:53], v[240:243], v[190:193], v[50:53]
	v_mfma_i32_16x16x64_i8 v[38:41], v[230:233], v[198:201], v[38:41]
	v_mfma_i32_16x16x64_i8 v[34:37], v[240:243], v[198:201], v[34:37]
	v_mfma_i32_16x16x64_i8 v[22:25], v[230:233], v[206:209], v[22:25]
	v_mfma_i32_16x16x64_i8 v[18:21], v[240:243], v[206:209], v[18:21]
	v_mfma_i32_16x16x64_i8 v[6:9], v[230:233], v[214:217], v[6:9]
	v_mfma_i32_16x16x64_i8 v[2:5], v[240:243], v[214:217], v[2:5]
	s_add_i32 s26, 0, 0x18000
	v_add_u32_e32 v98, s26, v165
	s_barrier
	ds_read_b128 v[148:151], v98
	ds_read_b128 v[154:157], v98 offset:1024
	ds_read_b128 v[176:179], v98 offset:2048
	ds_read_b128 v[182:185], v98 offset:3072
	s_mov_b32 m0, s19
	v_cndmask_b32_e32 v98, v140, v175, vcc
	ds_read_b128 v[186:189], v169 offset:32768
	ds_read_b128 v[190:193], v169 offset:33792
	ds_read_b128 v[194:197], v169 offset:34816
	ds_read_b128 v[198:201], v169 offset:35840
	ds_read_b128 v[202:205], v169 offset:36864
	ds_read_b128 v[206:209], v169 offset:37888
	ds_read_b128 v[210:213], v169 offset:38912
	ds_read_b128 v[214:217], v169 offset:39936
	global_load_lds_dwordx4 v98, s[40:41]
	v_cndmask_b32_e32 v98, v142, v180, vcc
	s_mov_b32 m0, s92
	s_nop 0
	global_load_lds_dwordx4 v98, s[40:41]
	s_waitcnt lgkmcnt(8)
	s_barrier
	s_waitcnt lgkmcnt(0)
	s_waitcnt lgkmcnt(0)
	v_mfma_i32_16x16x64_i8 v[128:131], v[148:151], v[186:189], v[128:131]
	v_mfma_i32_16x16x64_i8 v[120:123], v[176:179], v[186:189], v[120:123]
	v_mfma_i32_16x16x64_i8 v[112:115], v[148:151], v[194:197], v[112:115]
	v_mfma_i32_16x16x64_i8 v[108:111], v[176:179], v[194:197], v[108:111]
	v_mfma_i32_16x16x64_i8 v[94:97], v[148:151], v[202:205], v[94:97]
	v_mfma_i32_16x16x64_i8 v[90:93], v[176:179], v[202:205], v[90:93]
	v_mfma_i32_16x16x64_i8 v[78:81], v[148:151], v[210:213], v[78:81]
	v_mfma_i32_16x16x64_i8 v[74:77], v[176:179], v[210:213], v[74:77]
	v_mfma_i32_16x16x64_i8 v[128:131], v[154:157], v[190:193], v[128:131]
	v_mfma_i32_16x16x64_i8 v[120:123], v[182:185], v[190:193], v[120:123]
	v_mfma_i32_16x16x64_i8 v[112:115], v[154:157], v[198:201], v[112:115]
	v_mfma_i32_16x16x64_i8 v[108:111], v[182:185], v[198:201], v[108:111]
	v_mfma_i32_16x16x64_i8 v[94:97], v[154:157], v[206:209], v[94:97]
	v_mfma_i32_16x16x64_i8 v[90:93], v[182:185], v[206:209], v[90:93]
	v_mfma_i32_16x16x64_i8 v[78:81], v[154:157], v[214:217], v[78:81]
	v_mfma_i32_16x16x64_i8 v[74:77], v[182:185], v[214:217], v[74:77]
	s_barrier
	s_add_i32 s40, 0, 0x1c000
	s_add_i32 s26, s26, s93
	v_add_u32_e32 v98, s40, v165
	v_lshl_add_u64 v[170:171], v[170:171], 0, s[68:69]
	s_mov_b32 m0, s26
	ds_read_b128 v[222:225], v98
	ds_read_b128 v[230:233], v98 offset:1024
	ds_read_b128 v[236:239], v98 offset:2048
	ds_read_b128 v[240:243], v98 offset:3072
	global_load_lds_dwordx4 v[170:171], off
	v_lshl_add_u64 v[170:171], v[218:219], 0, s[68:69]
	s_add_i32 m0, s26, 0x2000
	s_nop 0
	global_load_lds_dwordx4 v[170:171], off
	s_barrier
	s_waitcnt lgkmcnt(0)
	s_waitcnt lgkmcnt(0)
	v_mfma_i32_16x16x64_i8 v[124:127], v[222:225], v[186:189], v[124:127]
	v_mfma_i32_16x16x64_i8 v[116:119], v[236:239], v[186:189], v[116:119]
	v_mfma_i32_16x16x64_i8 v[104:107], v[222:225], v[194:197], v[104:107]
	v_mfma_i32_16x16x64_i8 v[100:103], v[236:239], v[194:197], v[100:103]
	v_mfma_i32_16x16x64_i8 v[86:89], v[222:225], v[202:205], v[86:89]
	v_mfma_i32_16x16x64_i8 v[82:85], v[236:239], v[202:205], v[82:85]
	v_mfma_i32_16x16x64_i8 v[70:73], v[222:225], v[210:213], v[70:73]
	v_mfma_i32_16x16x64_i8 v[66:69], v[236:239], v[210:213], v[66:69]
	v_mfma_i32_16x16x64_i8 v[124:127], v[230:233], v[190:193], v[124:127]
	v_mfma_i32_16x16x64_i8 v[116:119], v[240:243], v[190:193], v[116:119]
	v_mfma_i32_16x16x64_i8 v[104:107], v[230:233], v[198:201], v[104:107]
	v_mfma_i32_16x16x64_i8 v[100:103], v[240:243], v[198:201], v[100:103]
	v_mfma_i32_16x16x64_i8 v[86:89], v[230:233], v[206:209], v[86:89]
	v_mfma_i32_16x16x64_i8 v[82:85], v[240:243], v[206:209], v[82:85]
	v_mfma_i32_16x16x64_i8 v[70:73], v[230:233], v[214:217], v[70:73]
	v_mfma_i32_16x16x64_i8 v[66:69], v[240:243], v[214:217], v[66:69]
	s_mov_b32 m0, s3
	v_lshl_add_u64 v[170:171], v[244:245], 0, s[68:69]
	s_barrier
	ds_read_b128 v[186:189], v169 offset:49152
	ds_read_b128 v[190:193], v169 offset:50176
	ds_read_b128 v[194:197], v169 offset:51200
	ds_read_b128 v[198:201], v169 offset:52224
	ds_read_b128 v[202:205], v169 offset:53248
	ds_read_b128 v[206:209], v169 offset:54272
	ds_read_b128 v[210:213], v169 offset:55296
	ds_read_b128 v[214:217], v169 offset:56320
	global_load_lds_dwordx4 v[170:171], off
	v_lshl_add_u64 v[170:171], v[246:247], 0, s[68:69]
	s_mov_b32 m0, s74
	s_nop 0
	global_load_lds_dwordx4 v[170:171], off
	s_barrier
	s_waitcnt lgkmcnt(0)
	s_waitcnt lgkmcnt(0)
	v_mfma_i32_16x16x64_i8 v[62:65], v[148:151], v[186:189], v[62:65]
	v_mfma_i32_16x16x64_i8 v[58:61], v[176:179], v[186:189], v[58:61]
	v_mfma_i32_16x16x64_i8 v[46:49], v[148:151], v[194:197], v[46:49]
	v_mfma_i32_16x16x64_i8 v[42:45], v[176:179], v[194:197], v[42:45]
	v_mfma_i32_16x16x64_i8 v[30:33], v[148:151], v[202:205], v[30:33]
	v_mfma_i32_16x16x64_i8 v[26:29], v[176:179], v[202:205], v[26:29]
	v_mfma_i32_16x16x64_i8 v[14:17], v[148:151], v[210:213], v[14:17]
	v_mfma_i32_16x16x64_i8 v[10:13], v[176:179], v[210:213], v[10:13]
	v_mfma_i32_16x16x64_i8 v[62:65], v[154:157], v[190:193], v[62:65]
	v_mfma_i32_16x16x64_i8 v[58:61], v[182:185], v[190:193], v[58:61]
	v_mfma_i32_16x16x64_i8 v[46:49], v[154:157], v[198:201], v[46:49]
	v_mfma_i32_16x16x64_i8 v[42:45], v[182:185], v[198:201], v[42:45]
	v_mfma_i32_16x16x64_i8 v[30:33], v[154:157], v[206:209], v[30:33]
	v_mfma_i32_16x16x64_i8 v[26:29], v[182:185], v[206:209], v[26:29]
	v_mfma_i32_16x16x64_i8 v[14:17], v[154:157], v[214:217], v[14:17]
	v_mfma_i32_16x16x64_i8 v[10:13], v[182:185], v[214:217], v[10:13]
	s_barrier
	s_add_u32 s26, s38, 0x40080
	s_addc_u32 s27, s39, 0
	s_add_i32 s38, s40, s93
	v_lshl_add_u64 v[148:149], s[26:27], 0, v[132:133]
	s_mov_b32 m0, s38
	s_nop 0
	global_load_lds_dwordx4 v[148:149], off
	v_lshl_add_u64 v[148:149], s[26:27], 0, v[134:135]
	s_add_i32 m0, s38, 0x2000
	s_nop 0
	global_load_lds_dwordx4 v[148:149], off
	s_waitcnt vmcnt(6)
	s_barrier
	v_mfma_i32_16x16x64_i8 v[54:57], v[222:225], v[186:189], v[54:57]
	v_mfma_i32_16x16x64_i8 v[50:53], v[236:239], v[186:189], v[50:53]
	v_mfma_i32_16x16x64_i8 v[38:41], v[222:225], v[194:197], v[38:41]
	v_mfma_i32_16x16x64_i8 v[34:37], v[236:239], v[194:197], v[34:37]
	v_mfma_i32_16x16x64_i8 v[22:25], v[222:225], v[202:205], v[22:25]
	v_mfma_i32_16x16x64_i8 v[18:21], v[236:239], v[202:205], v[18:21]
	v_mfma_i32_16x16x64_i8 v[6:9], v[222:225], v[210:213], v[6:9]
	v_mfma_i32_16x16x64_i8 v[2:5], v[236:239], v[210:213], v[2:5]
	v_mfma_i32_16x16x64_i8 v[54:57], v[230:233], v[190:193], v[54:57]
	v_mfma_i32_16x16x64_i8 v[50:53], v[240:243], v[190:193], v[50:53]
	v_mfma_i32_16x16x64_i8 v[38:41], v[230:233], v[198:201], v[38:41]
	v_mfma_i32_16x16x64_i8 v[34:37], v[240:243], v[198:201], v[34:37]
	v_mfma_i32_16x16x64_i8 v[22:25], v[230:233], v[206:209], v[22:25]
	v_mfma_i32_16x16x64_i8 v[18:21], v[240:243], v[206:209], v[18:21]
	v_mfma_i32_16x16x64_i8 v[6:9], v[230:233], v[214:217], v[6:9]
	v_mfma_i32_16x16x64_i8 v[2:5], v[240:243], v[214:217], v[2:5]
	s_add_i32 s42, s42, 2
	s_cmp_gt_u32 s42, 13
	s_mov_b64 s[26:27], s[36:37]
	s_barrier
	s_cbranch_scc0 .LBB0_1870
	v_lshl_add_u32 v136, s71, 8, v163
	v_readlane_b32 s26, v253, 52
	v_ashrrev_i32_e32 v137, 31, v136
	v_readlane_b32 s27, v253, 53
	s_mul_hi_i32 s20, s9, 0xb000
	s_mul_i32 s9, s9, 0xb000
	v_lshl_add_u64 v[138:139], v[136:137], 2, s[26:27]
	v_readlane_b32 s26, v254, 15
	s_add_u32 s9, s26, s9
	v_readlane_b32 s26, v254, 16
	s_addc_u32 s20, s26, s20
	s_lshl_b32 s26, s34, 8
	s_ashr_i32 s27, s26, 31
	s_lshl_b64 s[26:27], s[26:27], 2
	s_add_u32 s9, s9, s26
	s_addc_u32 s20, s20, s27
	s_add_u32 s26, s9, s85
	s_addc_u32 s27, s20, 0
	global_load_dword v168, v[138:139], off
	global_load_dword v166, v[138:139], off offset:64
	global_load_dword v164, v[138:139], off offset:128
	global_load_dword v162, v[138:139], off offset:192
	global_load_dword v160, v[138:139], off offset:512
	global_load_dword v158, v[138:139], off offset:576
	global_load_dword v152, v[138:139], off offset:640
	global_load_dword v98, v[138:139], off offset:704
	global_load_dwordx4 v[176:179], v172, s[26:27] offset:16
	global_load_dwordx4 v[140:143], v172, s[26:27]
	global_load_dwordx4 v[182:185], v172, s[26:27] offset:528
	global_load_dwordx4 v[144:147], v172, s[26:27] offset:512
	v_cvt_f32_i32_e32 v129, v129
	v_cvt_f32_i32_e32 v121, v121
	v_readlane_b32 s26, v254, 13
	v_readlane_b32 s27, v254, 14
	v_lshl_or_b32 v138, s34, 7, v167
	s_movk_i32 s9, 0x2c00
	v_mov_b64_e32 v[170:171], s[26:27]
	v_ashrrev_i32_e32 v139, 31, v138
	v_mad_i64_i32 v[170:171], s[26:27], v136, s9, v[170:171]
	s_waitcnt vmcnt(0)
	v_mov_b32_e32 v149, v140
	v_mov_b32_e32 v140, v145
	v_pk_mul_f32 v[154:155], v[140:141], s[58:59] op_sel_hi:[1,0]
	v_mov_b32_e32 v140, v146
	v_mov_b32_e32 v141, v142
	v_pk_mul_f32 v[150:151], v[140:141], s[58:59] op_sel_hi:[1,0]
	v_mov_b32_e32 v141, v176
	v_mov_b32_e32 v176, v183
	v_mov_b32_e32 v148, v144
	v_pk_mul_f32 v[144:145], v[176:177], s[58:59] op_sel_hi:[1,0]
	v_cvt_f32_i32_e32 v177, v128
	v_cvt_f32_i32_e32 v176, v124
	v_mov_b32_e32 v140, v182
	v_pk_mul_f32 v[156:157], v[148:149], s[58:59] op_sel_hi:[1,0]
	v_mov_b32_e32 v142, v147
	v_pk_mul_f32 v[146:147], v[140:141], s[58:59] op_sel_hi:[1,0]
	v_mov_b32_e32 v140, v184
	v_mov_b32_e32 v141, v178
	v_mov_b32_e32 v178, v185
	v_pk_mul_f32 v[148:149], v[142:143], s[58:59] op_sel_hi:[1,0]
	v_pk_mul_f32 v[142:143], v[140:141], s[58:59] op_sel_hi:[1,0]
	v_pk_mul_f32 v[140:141], v[178:179], s[58:59] op_sel_hi:[1,0]
	v_pk_mul_f32 v[178:179], v[168:169], v[156:157] op_sel_hi:[0,1]
	v_pk_mul_f32 v[176:177], v[178:179], v[176:177]
	v_cvt_f32_i32_e32 v128, v125
	v_mul_f32_e32 v124, 0xbfb8aa3b, v177
	v_exp_f32_e32 v124, v124
	s_nop 0
	v_add_f32_e32 v124, 1.0, v124
	v_rcp_f32_e32 v124, v124
	s_nop 0
	v_mul_f32_e32 v124, v177, v124
	v_mul_f32_e32 v124, v176, v124
	v_pk_mul_f32 v[176:177], v[168:169], v[154:155] op_sel_hi:[0,1]
	v_pk_mul_f32 v[128:129], v[176:177], v[128:129]
	v_pk_mul_f32 v[176:177], v[168:169], v[150:151] op_sel_hi:[0,1]
	v_mul_f32_e32 v125, 0xbfb8aa3b, v129
	v_exp_f32_e32 v125, v125
	s_nop 0
	v_add_f32_e32 v125, 1.0, v125
	v_rcp_f32_e32 v125, v125
	s_nop 0
	v_mul_f32_e32 v125, v129, v125
	v_mul_f32_e32 v125, v128, v125
	v_cvt_f32_i32_e32 v129, v130
	v_cvt_f32_i32_e32 v128, v126
	v_pk_mul_f32 v[128:129], v[176:177], v[128:129]
	s_nop 0
	v_mul_f32_e32 v126, 0xbfb8aa3b, v129
	v_exp_f32_e32 v126, v126
	s_nop 0
	v_add_f32_e32 v126, 1.0, v126
	v_rcp_f32_e32 v126, v126
	s_nop 0
	v_mul_f32_e32 v126, v129, v126
	v_mul_f32_e32 v126, v128, v126
	v_cvt_f32_i32_e32 v129, v131
	v_cvt_f32_i32_e32 v128, v127
	v_pk_mul_f32 v[130:131], v[168:169], v[148:149] op_sel_hi:[0,1]
	v_pk_mul_f32 v[128:129], v[130:131], v[128:129]
	s_nop 0
	v_mul_f32_e32 v127, 0xbfb8aa3b, v129
	v_exp_f32_e32 v127, v127
	v_pk_mul_f32 v[130:131], v[168:169], v[146:147] op_sel_hi:[0,1]
	v_add_f32_e32 v127, 1.0, v127
	v_rcp_f32_e32 v127, v127
	s_nop 0
	v_mul_f32_e32 v127, v129, v127
	v_mul_f32_e32 v127, v128, v127
	v_cvt_f32_i32_e32 v129, v120
	v_cvt_f32_i32_e32 v128, v116
	v_cvt_f32_i32_e32 v120, v117
	v_pk_mul_f32 v[128:129], v[130:131], v[128:129]
	s_nop 0
	v_mul_f32_e32 v116, 0xbfb8aa3b, v129
	v_exp_f32_e32 v116, v116
	s_nop 0
	v_add_f32_e32 v116, 1.0, v116
	v_rcp_f32_e32 v116, v116
	s_nop 0
	v_mul_f32_e32 v116, v129, v116
	v_mul_f32_e32 v128, v128, v116
	v_pk_mul_f32 v[116:117], v[168:169], v[144:145] op_sel_hi:[0,1]
	v_pk_mul_f32 v[116:117], v[116:117], v[120:121]
	s_nop 0
	v_mul_f32_e32 v120, 0xbfb8aa3b, v117
	v_exp_f32_e32 v120, v120
	s_nop 0
	v_add_f32_e32 v120, 1.0, v120
	v_rcp_f32_e32 v120, v120
	s_nop 0
	v_mul_f32_e32 v117, v117, v120
	v_mul_f32_e32 v129, v116, v117
	v_cvt_f32_i32_e32 v117, v122
	v_cvt_f32_i32_e32 v116, v118
	v_pk_mul_f32 v[120:121], v[168:169], v[142:143] op_sel_hi:[0,1]
	v_pk_mul_f32 v[116:117], v[120:121], v[116:117]
	s_nop 0
	v_mul_f32_e32 v118, 0xbfb8aa3b, v117
	v_exp_f32_e32 v118, v118
	v_lshl_add_u64 v[120:121], v[138:139], 1, v[170:171]
	v_add_f32_e32 v118, 1.0, v118
	v_rcp_f32_e32 v118, v118
	s_nop 0
	v_mul_f32_e32 v117, v117, v118
	v_mul_f32_e32 v122, v116, v117
	v_cvt_f32_i32_e32 v117, v123
	v_cvt_f32_i32_e32 v116, v119
	v_pk_mul_f32 v[118:119], v[168:169], v[140:141] op_sel_hi:[0,1]
	v_pk_mul_f32 v[116:117], v[118:119], v[116:117]
	s_nop 0
	v_mul_f32_e32 v118, 0xbfb8aa3b, v117
	v_exp_f32_e32 v118, v118
	s_nop 0
	v_add_f32_e32 v118, 1.0, v118
	v_rcp_f32_e32 v118, v118
	s_nop 0
	v_mul_f32_e32 v117, v117, v118
	v_mul_f32_e32 v123, v116, v117
	v_cvt_pk_bf16_f32 v116, v124, v125
	v_cvt_pk_bf16_f32 v117, v126, v127
	v_cvt_pk_bf16_f32 v118, v128, v129
	v_cvt_pk_bf16_f32 v119, v122, v123
	global_store_dwordx4 v[120:121], v[116:119], off
	s_nop 1
	v_max_f32_e64 v118, |v122|, |v123|
	v_max_f32_e64 v116, |v124|, |v125|
	v_max_f32_e64 v117, |v126|, |v127|
	v_max3_f32 v118, |v128|, |v129|, v118
	v_max3_f32 v116, v116, v117, v118
	v_mov_b32_e32 v117, v0
	s_nop 0
	v_lshlrev_b32_e32 v117, 2, v117
	v_bitop3_b32 v118, v117, 64, v220 bitop3:0x6c
	ds_bpermute_b32 v118, v118, v116
	v_bitop3_b32 v117, v117, s59, v220 bitop3:0x6c
	s_waitcnt lgkmcnt(0)
	v_max_f32_e32 v118, v118, v118
	v_max_f32_e32 v116, v116, v118
	ds_bpermute_b32 v117, v117, v116
	s_and_saveexec_b64 s[26:27], s[0:1]
	s_cbranch_execz .LBB0_1873
	v_readlane_b32 s36, v253, 57
	s_waitcnt lgkmcnt(0)
	v_max_f32_e32 v117, v117, v117
	v_max_f32_e32 v116, v116, v116
	v_readlane_b32 s37, v253, 58
	v_max_f32_e32 v118, v116, v117
	s_nop 0
	v_lshl_add_u64 v[116:117], v[136:137], 2, s[36:37]
	global_atomic_umax v[116:117], v118, off

.LBB0_2010:
	s_add_u32 s34, s30, 0x100
	s_addc_u32 s35, s31, 0
	s_add_i32 vcc_hi, 0, 0x10000
	v_add_u32_e32 v146, vcc_hi, v147
	ds_read_b128 v[132:135], v146
	ds_read_b128 v[150:153], v146 offset:1024
	ds_read_b128 v[154:157], v146 offset:2048
	ds_read_b128 v[158:161], v146 offset:3072
	s_cmp_eq_u32 vcc_lo, 40
	s_cselect_b32 s39, s23, s35
	s_cselect_b32 s38, s22, s34
	s_cselect_b32 s37, s25, s93
	s_cselect_b32 s36, s24, s71
	v_lshl_add_u64 v[196:197], s[30:31], 0, v[142:143]
	s_add_i32 m0, s8, 0xc000
	ds_read_b128 v[164:167], v163
	ds_read_b128 v[168:171], v163 offset:1024
	ds_read_b128 v[172:175], v163 offset:2048
	ds_read_b128 v[176:179], v163 offset:3072
	ds_read_b128 v[180:183], v163 offset:4096
	ds_read_b128 v[184:187], v163 offset:5120
	ds_read_b128 v[188:191], v163 offset:6144
	ds_read_b128 v[192:195], v163 offset:7168
	global_load_lds_dwordx4 v[196:197], off
	v_lshl_add_u64 v[196:197], s[30:31], 0, v[144:145]
	s_add_i32 m0, s8, 0xe000
	s_nop 0
	global_load_lds_dwordx4 v[196:197], off
	s_waitcnt lgkmcnt(8)
	s_barrier
	s_waitcnt lgkmcnt(0)
	s_waitcnt lgkmcnt(0)
	v_mfma_i32_16x16x64_i8 v[128:131], v[132:135], v[164:167], v[128:131]
	v_mfma_i32_16x16x64_i8 v[124:127], v[154:157], v[164:167], v[124:127]
	v_mfma_i32_16x16x64_i8 v[120:123], v[132:135], v[172:175], v[120:123]
	v_mfma_i32_16x16x64_i8 v[116:119], v[154:157], v[172:175], v[116:119]
	v_mfma_i32_16x16x64_i8 v[112:115], v[132:135], v[180:183], v[112:115]
	v_mfma_i32_16x16x64_i8 v[108:111], v[154:157], v[180:183], v[108:111]
	v_mfma_i32_16x16x64_i8 v[104:107], v[132:135], v[188:191], v[104:107]
	v_mfma_i32_16x16x64_i8 v[100:103], v[154:157], v[188:191], v[100:103]
	v_mfma_i32_16x16x64_i8 v[128:131], v[150:153], v[168:171], v[128:131]
	v_mfma_i32_16x16x64_i8 v[124:127], v[158:161], v[168:171], v[124:127]
	v_mfma_i32_16x16x64_i8 v[120:123], v[150:153], v[176:179], v[120:123]
	v_mfma_i32_16x16x64_i8 v[116:119], v[158:161], v[176:179], v[116:119]
	v_mfma_i32_16x16x64_i8 v[112:115], v[150:153], v[184:187], v[112:115]
	v_mfma_i32_16x16x64_i8 v[108:111], v[158:161], v[184:187], v[108:111]
	v_mfma_i32_16x16x64_i8 v[104:107], v[150:153], v[192:195], v[104:107]
	v_mfma_i32_16x16x64_i8 v[100:103], v[158:161], v[192:195], v[100:103]
	s_barrier
	s_add_i32 s3, 0, 0x14000
	s_add_i32 s30, vcc_hi, s62
	v_add_u32_e32 v146, s3, v147
	v_lshl_add_u64 v[212:213], s[36:37], 0, v[98:99]
	s_mov_b32 m0, s30
	ds_read_b128 v[196:199], v146
	ds_read_b128 v[200:203], v146 offset:1024
	ds_read_b128 v[204:207], v146 offset:2048
	ds_read_b128 v[208:211], v146 offset:3072
	global_load_lds_dwordx4 v[212:213], off
	v_lshl_add_u64 v[214:215], s[36:37], 0, v[136:137]
	s_add_i32 m0, s30, 0x2000
	s_nop 0
	global_load_lds_dwordx4 v[214:215], off
	s_barrier
	s_waitcnt lgkmcnt(0)
	s_waitcnt lgkmcnt(0)
	v_mfma_i32_16x16x64_i8 v[94:97], v[196:199], v[164:167], v[94:97]
	v_mfma_i32_16x16x64_i8 v[90:93], v[204:207], v[164:167], v[90:93]
	v_mfma_i32_16x16x64_i8 v[86:89], v[196:199], v[172:175], v[86:89]
	v_mfma_i32_16x16x64_i8 v[82:85], v[204:207], v[172:175], v[82:85]
	v_mfma_i32_16x16x64_i8 v[78:81], v[196:199], v[180:183], v[78:81]
	v_mfma_i32_16x16x64_i8 v[74:77], v[204:207], v[180:183], v[74:77]
	v_mfma_i32_16x16x64_i8 v[70:73], v[196:199], v[188:191], v[70:73]
	v_mfma_i32_16x16x64_i8 v[66:69], v[204:207], v[188:191], v[66:69]
	v_mfma_i32_16x16x64_i8 v[94:97], v[200:203], v[168:171], v[94:97]
	v_mfma_i32_16x16x64_i8 v[90:93], v[208:211], v[168:171], v[90:93]
	v_mfma_i32_16x16x64_i8 v[86:89], v[200:203], v[176:179], v[86:89]
	v_mfma_i32_16x16x64_i8 v[82:85], v[208:211], v[176:179], v[82:85]
	v_mfma_i32_16x16x64_i8 v[78:81], v[200:203], v[184:187], v[78:81]
	v_mfma_i32_16x16x64_i8 v[74:77], v[208:211], v[184:187], v[74:77]
	v_mfma_i32_16x16x64_i8 v[70:73], v[200:203], v[192:195], v[70:73]
	v_mfma_i32_16x16x64_i8 v[66:69], v[208:211], v[192:195], v[66:69]
	s_mov_b32 m0, s8
	v_lshl_add_u64 v[216:217], s[38:39], 0, v[140:141]
	s_barrier
	ds_read_b128 v[164:167], v163 offset:16384
	ds_read_b128 v[168:171], v163 offset:17408
	ds_read_b128 v[172:175], v163 offset:18432
	ds_read_b128 v[176:179], v163 offset:19456
	ds_read_b128 v[180:183], v163 offset:20480
	ds_read_b128 v[184:187], v163 offset:21504
	ds_read_b128 v[188:191], v163 offset:22528
	ds_read_b128 v[192:195], v163 offset:23552
	global_load_lds_dwordx4 v[216:217], off
	v_lshl_add_u64 v[218:219], s[38:39], 0, v[138:139]
	s_mov_b32 m0, s64
	s_nop 0
	global_load_lds_dwordx4 v[218:219], off
	s_barrier
	s_waitcnt lgkmcnt(0)
	s_waitcnt lgkmcnt(0)
	v_mfma_i32_16x16x64_i8 v[62:65], v[132:135], v[164:167], v[62:65]
	v_mfma_i32_16x16x64_i8 v[58:61], v[154:157], v[164:167], v[58:61]
	v_mfma_i32_16x16x64_i8 v[54:57], v[132:135], v[172:175], v[54:57]
	v_mfma_i32_16x16x64_i8 v[50:53], v[154:157], v[172:175], v[50:53]
	v_mfma_i32_16x16x64_i8 v[46:49], v[132:135], v[180:183], v[46:49]
	v_mfma_i32_16x16x64_i8 v[42:45], v[154:157], v[180:183], v[42:45]
	v_mfma_i32_16x16x64_i8 v[38:41], v[132:135], v[188:191], v[38:41]
	v_mfma_i32_16x16x64_i8 v[34:37], v[154:157], v[188:191], v[34:37]
	v_mfma_i32_16x16x64_i8 v[62:65], v[150:153], v[168:171], v[62:65]
	v_mfma_i32_16x16x64_i8 v[58:61], v[158:161], v[168:171], v[58:61]
	v_mfma_i32_16x16x64_i8 v[54:57], v[150:153], v[176:179], v[54:57]
	v_mfma_i32_16x16x64_i8 v[50:53], v[158:161], v[176:179], v[50:53]
	v_mfma_i32_16x16x64_i8 v[46:49], v[150:153], v[184:187], v[46:49]
	v_mfma_i32_16x16x64_i8 v[42:45], v[158:161], v[184:187], v[42:45]
	v_mfma_i32_16x16x64_i8 v[38:41], v[150:153], v[192:195], v[38:41]
	v_mfma_i32_16x16x64_i8 v[34:37], v[158:161], v[192:195], v[34:37]
	s_barrier
	s_add_u32 s30, s36, 0xb0000
	s_addc_u32 s31, s37, 0
	s_add_i32 s3, s3, s62
	v_lshl_add_u64 v[132:133], s[30:31], 0, v[98:99]
	s_mov_b32 m0, s3
	s_nop 0
	global_load_lds_dwordx4 v[132:133], off
	v_lshl_add_u64 v[132:133], s[30:31], 0, v[136:137]
	s_add_i32 m0, s3, 0x2000
	s_nop 0
	global_load_lds_dwordx4 v[132:133], off
	s_waitcnt vmcnt(6)
	s_barrier
	v_mfma_i32_16x16x64_i8 v[30:33], v[196:199], v[164:167], v[30:33]
	v_mfma_i32_16x16x64_i8 v[26:29], v[204:207], v[164:167], v[26:29]
	v_mfma_i32_16x16x64_i8 v[22:25], v[196:199], v[172:175], v[22:25]
	v_mfma_i32_16x16x64_i8 v[18:21], v[204:207], v[172:175], v[18:21]
	v_mfma_i32_16x16x64_i8 v[14:17], v[196:199], v[180:183], v[14:17]
	v_mfma_i32_16x16x64_i8 v[10:13], v[204:207], v[180:183], v[10:13]
	v_mfma_i32_16x16x64_i8 v[6:9], v[196:199], v[188:191], v[6:9]
	v_mfma_i32_16x16x64_i8 v[2:5], v[204:207], v[188:191], v[2:5]
	v_mfma_i32_16x16x64_i8 v[30:33], v[200:203], v[168:171], v[30:33]
	v_mfma_i32_16x16x64_i8 v[26:29], v[208:211], v[168:171], v[26:29]
	v_mfma_i32_16x16x64_i8 v[22:25], v[200:203], v[176:179], v[22:25]
	v_mfma_i32_16x16x64_i8 v[18:21], v[208:211], v[176:179], v[18:21]
	v_mfma_i32_16x16x64_i8 v[14:17], v[200:203], v[184:187], v[14:17]
	v_mfma_i32_16x16x64_i8 v[10:13], v[208:211], v[184:187], v[10:13]
	v_mfma_i32_16x16x64_i8 v[6:9], v[200:203], v[192:195], v[6:9]
	v_mfma_i32_16x16x64_i8 v[2:5], v[208:211], v[192:195], v[2:5]
	s_add_i32 s3, 0, 0x18000
	v_add_u32_e32 v146, s3, v147
	s_barrier
	ds_read_b128 v[132:135], v146
	ds_read_b128 v[150:153], v146 offset:1024
	ds_read_b128 v[154:157], v146 offset:2048
	ds_read_b128 v[158:161], v146 offset:3072
	s_add_u32 s30, s38, 0xb0000
	s_addc_u32 s31, s39, 0
	s_mov_b32 m0, s65
	v_lshl_add_u64 v[196:197], s[30:31], 0, v[140:141]
	ds_read_b128 v[164:167], v163 offset:32768
	ds_read_b128 v[168:171], v163 offset:33792
	ds_read_b128 v[172:175], v163 offset:34816
	ds_read_b128 v[176:179], v163 offset:35840
	ds_read_b128 v[180:183], v163 offset:36864
	ds_read_b128 v[184:187], v163 offset:37888
	ds_read_b128 v[188:191], v163 offset:38912
	ds_read_b128 v[192:195], v163 offset:39936
	global_load_lds_dwordx4 v[196:197], off
	v_lshl_add_u64 v[196:197], s[30:31], 0, v[138:139]
	s_mov_b32 m0, s66
	s_nop 0
	global_load_lds_dwordx4 v[196:197], off
	s_waitcnt lgkmcnt(8)
	s_barrier
	s_waitcnt lgkmcnt(0)
	s_waitcnt lgkmcnt(0)
	v_mfma_i32_16x16x64_i8 v[128:131], v[132:135], v[164:167], v[128:131]
	v_mfma_i32_16x16x64_i8 v[124:127], v[154:157], v[164:167], v[124:127]
	v_mfma_i32_16x16x64_i8 v[120:123], v[132:135], v[172:175], v[120:123]
	v_mfma_i32_16x16x64_i8 v[116:119], v[154:157], v[172:175], v[116:119]
	v_mfma_i32_16x16x64_i8 v[112:115], v[132:135], v[180:183], v[112:115]
	v_mfma_i32_16x16x64_i8 v[108:111], v[154:157], v[180:183], v[108:111]
	v_mfma_i32_16x16x64_i8 v[104:107], v[132:135], v[188:191], v[104:107]
	v_mfma_i32_16x16x64_i8 v[100:103], v[154:157], v[188:191], v[100:103]
	v_mfma_i32_16x16x64_i8 v[128:131], v[150:153], v[168:171], v[128:131]
	v_mfma_i32_16x16x64_i8 v[124:127], v[158:161], v[168:171], v[124:127]
	v_mfma_i32_16x16x64_i8 v[120:123], v[150:153], v[176:179], v[120:123]
	v_mfma_i32_16x16x64_i8 v[116:119], v[158:161], v[176:179], v[116:119]
	v_mfma_i32_16x16x64_i8 v[112:115], v[150:153], v[184:187], v[112:115]
	v_mfma_i32_16x16x64_i8 v[108:111], v[158:161], v[184:187], v[108:111]
	v_mfma_i32_16x16x64_i8 v[104:107], v[150:153], v[192:195], v[104:107]
	v_mfma_i32_16x16x64_i8 v[100:103], v[158:161], v[192:195], v[100:103]
	s_barrier
	s_add_i32 s38, 0, 0x1c000
	s_add_i32 s3, s3, s62
	v_add_u32_e32 v146, s38, v147
	v_lshl_add_u64 v[212:213], v[212:213], 0, s[68:69]
	s_mov_b32 m0, s3
	ds_read_b128 v[196:199], v146
	ds_read_b128 v[200:203], v146 offset:1024
	ds_read_b128 v[204:207], v146 offset:2048
	ds_read_b128 v[208:211], v146 offset:3072
	global_load_lds_dwordx4 v[212:213], off
	v_lshl_add_u64 v[212:213], v[214:215], 0, s[68:69]
	s_add_i32 m0, s3, 0x2000
	s_nop 0
	global_load_lds_dwordx4 v[212:213], off
	s_barrier
	s_waitcnt lgkmcnt(0)
	s_waitcnt lgkmcnt(0)
	v_mfma_i32_16x16x64_i8 v[94:97], v[196:199], v[164:167], v[94:97]
	v_mfma_i32_16x16x64_i8 v[90:93], v[204:207], v[164:167], v[90:93]
	v_mfma_i32_16x16x64_i8 v[86:89], v[196:199], v[172:175], v[86:89]
	v_mfma_i32_16x16x64_i8 v[82:85], v[204:207], v[172:175], v[82:85]
	v_mfma_i32_16x16x64_i8 v[78:81], v[196:199], v[180:183], v[78:81]
	v_mfma_i32_16x16x64_i8 v[74:77], v[204:207], v[180:183], v[74:77]
	v_mfma_i32_16x16x64_i8 v[70:73], v[196:199], v[188:191], v[70:73]
	v_mfma_i32_16x16x64_i8 v[66:69], v[204:207], v[188:191], v[66:69]
	v_mfma_i32_16x16x64_i8 v[94:97], v[200:203], v[168:171], v[94:97]
	v_mfma_i32_16x16x64_i8 v[90:93], v[208:211], v[168:171], v[90:93]
	v_mfma_i32_16x16x64_i8 v[86:89], v[200:203], v[176:179], v[86:89]
	v_mfma_i32_16x16x64_i8 v[82:85], v[208:211], v[176:179], v[82:85]
	v_mfma_i32_16x16x64_i8 v[78:81], v[200:203], v[184:187], v[78:81]
	v_mfma_i32_16x16x64_i8 v[74:77], v[208:211], v[184:187], v[74:77]
	v_mfma_i32_16x16x64_i8 v[70:73], v[200:203], v[192:195], v[70:73]
	v_mfma_i32_16x16x64_i8 v[66:69], v[208:211], v[192:195], v[66:69]
	s_mov_b32 m0, s67
	v_lshl_add_u64 v[212:213], v[216:217], 0, s[68:69]
	s_barrier
	ds_read_b128 v[164:167], v163 offset:49152
	ds_read_b128 v[168:171], v163 offset:50176
	ds_read_b128 v[172:175], v163 offset:51200
	ds_read_b128 v[176:179], v163 offset:52224
	ds_read_b128 v[180:183], v163 offset:53248
	ds_read_b128 v[184:187], v163 offset:54272
	ds_read_b128 v[188:191], v163 offset:55296
	ds_read_b128 v[192:195], v163 offset:56320
	global_load_lds_dwordx4 v[212:213], off
	v_lshl_add_u64 v[212:213], v[218:219], 0, s[68:69]
	s_mov_b32 m0, s74
	s_nop 0
	global_load_lds_dwordx4 v[212:213], off
	s_barrier
	s_waitcnt lgkmcnt(0)
	s_waitcnt lgkmcnt(0)
	v_mfma_i32_16x16x64_i8 v[62:65], v[132:135], v[164:167], v[62:65]
	v_mfma_i32_16x16x64_i8 v[58:61], v[154:157], v[164:167], v[58:61]
	v_mfma_i32_16x16x64_i8 v[54:57], v[132:135], v[172:175], v[54:57]
	v_mfma_i32_16x16x64_i8 v[50:53], v[154:157], v[172:175], v[50:53]
	v_mfma_i32_16x16x64_i8 v[46:49], v[132:135], v[180:183], v[46:49]
	v_mfma_i32_16x16x64_i8 v[42:45], v[154:157], v[180:183], v[42:45]
	v_mfma_i32_16x16x64_i8 v[38:41], v[132:135], v[188:191], v[38:41]
	v_mfma_i32_16x16x64_i8 v[34:37], v[154:157], v[188:191], v[34:37]
	v_mfma_i32_16x16x64_i8 v[62:65], v[150:153], v[168:171], v[62:65]
	v_mfma_i32_16x16x64_i8 v[58:61], v[158:161], v[168:171], v[58:61]
	v_mfma_i32_16x16x64_i8 v[54:57], v[150:153], v[176:179], v[54:57]
	v_mfma_i32_16x16x64_i8 v[50:53], v[158:161], v[176:179], v[50:53]
	v_mfma_i32_16x16x64_i8 v[46:49], v[150:153], v[184:187], v[46:49]
	v_mfma_i32_16x16x64_i8 v[42:45], v[158:161], v[184:187], v[42:45]
	v_mfma_i32_16x16x64_i8 v[38:41], v[150:153], v[192:195], v[38:41]
	v_mfma_i32_16x16x64_i8 v[34:37], v[158:161], v[192:195], v[34:37]
	s_barrier
	s_add_u32 s30, s36, 0xb0080
	s_addc_u32 s31, s37, 0
	s_add_i32 s3, s38, s62
	v_lshl_add_u64 v[132:133], s[30:31], 0, v[98:99]
	s_mov_b32 m0, s3
	s_nop 0
	global_load_lds_dwordx4 v[132:133], off
	v_lshl_add_u64 v[132:133], s[30:31], 0, v[136:137]
	s_add_i32 m0, s3, 0x2000
	s_nop 0
	global_load_lds_dwordx4 v[132:133], off
	s_waitcnt vmcnt(6)
	s_barrier
	v_mfma_i32_16x16x64_i8 v[30:33], v[196:199], v[164:167], v[30:33]
	v_mfma_i32_16x16x64_i8 v[26:29], v[204:207], v[164:167], v[26:29]
	v_mfma_i32_16x16x64_i8 v[22:25], v[196:199], v[172:175], v[22:25]
	v_mfma_i32_16x16x64_i8 v[18:21], v[204:207], v[172:175], v[18:21]
	v_mfma_i32_16x16x64_i8 v[14:17], v[196:199], v[180:183], v[14:17]
	v_mfma_i32_16x16x64_i8 v[10:13], v[204:207], v[180:183], v[10:13]
	v_mfma_i32_16x16x64_i8 v[6:9], v[196:199], v[188:191], v[6:9]
	v_mfma_i32_16x16x64_i8 v[2:5], v[204:207], v[188:191], v[2:5]
	v_mfma_i32_16x16x64_i8 v[30:33], v[200:203], v[168:171], v[30:33]
	v_mfma_i32_16x16x64_i8 v[26:29], v[208:211], v[168:171], v[26:29]
	v_mfma_i32_16x16x64_i8 v[22:25], v[200:203], v[176:179], v[22:25]
	v_mfma_i32_16x16x64_i8 v[18:21], v[208:211], v[176:179], v[18:21]
	v_mfma_i32_16x16x64_i8 v[14:17], v[200:203], v[184:187], v[14:17]
	v_mfma_i32_16x16x64_i8 v[10:13], v[208:211], v[184:187], v[10:13]
	v_mfma_i32_16x16x64_i8 v[6:9], v[200:203], v[192:195], v[6:9]
	v_mfma_i32_16x16x64_i8 v[2:5], v[208:211], v[192:195], v[2:5]
	s_add_i32 vcc_lo, vcc_lo, 2
	s_add_u32 s71, s71, 0x100
	s_addc_u32 s93, s93, 0
	s_cmp_gt_u32 vcc_lo, 41
	s_mov_b64 s[30:31], s[34:35]
	s_barrier
	s_cbranch_scc0 .LBB0_2010
	v_lshl_add_u32 v208, s70, 8, v1
	v_readlane_b32 s30, v253, 57
	v_or_b32_e32 v204, 16, v208
	v_lshl_or_b32 v210, s29, 8, v149
	s_ashr_i32 s29, s28, 31
	v_ashrrev_i32_e32 v209, 31, v208
	v_readlane_b32 s31, v253, 58
	v_ashrrev_i32_e32 v205, 31, v204
	v_or_b32_e32 v200, 32, v208
	s_lshl_b64 s[28:29], s[28:29], 13
	v_readlane_b32 s3, v254, 21
	v_lshl_add_u64 v[132:133], v[208:209], 2, s[30:31]
	v_lshl_add_u64 v[134:135], v[204:205], 2, s[30:31]
	v_ashrrev_i32_e32 v201, 31, v200
	v_or_b32_e32 v188, 48, v208
	s_add_u32 s28, s3, s28
	v_readlane_b32 s3, v254, 22
	global_load_dword v206, v[132:133], off
	global_load_dword v202, v[134:135], off
	v_lshl_add_u64 v[134:135], v[200:201], 2, s[30:31]
	v_ashrrev_i32_e32 v189, 31, v188
	v_ashrrev_i32_e32 v211, 31, v210
	s_addc_u32 s29, s3, s29
	global_load_dword v190, v[134:135], off
	v_lshl_add_u64 v[134:135], v[188:189], 2, s[30:31]
	v_lshl_add_u64 v[212:213], v[210:211], 2, s[28:29]
	global_load_dword v174, v[134:135], off
	global_load_dword v168, v[132:133], off offset:512
	global_load_dword v162, v[132:133], off offset:576
	global_load_dword v148, v[132:133], off offset:640
	global_load_dword v146, v[132:133], off offset:704
	s_nop 0
	global_load_dwordx4 v[132:135], v[212:213], off offset:16
	global_load_dwordx4 v[150:153], v[212:213], off
	v_cvt_f32_i32_e32 v155, v9
	v_cvt_f32_i32_e32 v154, v8
	v_cvt_f32_i32_e32 v161, v7
	v_cvt_f32_i32_e32 v160, v6
	v_cvt_f32_i32_e32 v195, v27
	v_cvt_f32_i32_e32 v194, v26
	v_cvt_f32_i32_e32 v197, v33
	v_cvt_f32_i32_e32 v196, v32
	v_cvt_f32_i32_e32 v27, v53
	v_cvt_f32_i32_e32 v26, v52
	v_cvt_f32_i32_e32 v33, v55
	v_cvt_f32_i32_e32 v32, v54
	v_cvt_f32_i32_e32 v53, v101
	v_cvt_f32_i32_e32 v52, v100
	v_cvt_f32_i32_e32 v55, v107
	v_cvt_f32_i32_e32 v54, v106
	v_cvt_f32_i32_e32 v101, v127
	v_cvt_f32_i32_e32 v100, v126
	v_cvt_f32_i32_e32 v107, v129
	v_cvt_f32_i32_e32 v106, v128
	v_cvt_f32_i32_e32 v167, v11
	v_cvt_f32_i32_e32 v166, v10
	v_cvt_f32_i32_e32 v171, v17
	v_cvt_f32_i32_e32 v170, v16
	v_cvt_f32_i32_e32 v193, v29
	v_cvt_f32_i32_e32 v192, v28
	v_cvt_f32_i32_e32 v11, v37
	v_cvt_f32_i32_e32 v10, v36
	v_cvt_f32_i32_e32 v17, v39
	v_cvt_f32_i32_e32 v16, v38
	v_cvt_f32_i32_e32 v29, v51
	v_cvt_f32_i32_e32 v28, v50
	v_cvt_f32_i32_e32 v37, v59
	v_cvt_f32_i32_e32 v36, v58
	v_cvt_f32_i32_e32 v39, v65
	v_cvt_f32_i32_e32 v38, v64
	v_cvt_f32_i32_e32 v65, v79
	v_cvt_f32_i32_e32 v64, v78
	v_cvt_f32_i32_e32 v79, v89
	v_cvt_f32_i32_e32 v78, v88
	v_cvt_f32_i32_e32 v89, v93
	v_cvt_f32_i32_e32 v88, v92
	v_cvt_f32_i32_e32 v95, v95
	v_cvt_f32_i32_e32 v94, v94
	v_cvt_f32_i32_e32 v51, v103
	v_cvt_f32_i32_e32 v50, v102
	v_cvt_f32_i32_e32 v59, v105
	v_cvt_f32_i32_e32 v58, v104
	v_cvt_f32_i32_e32 v103, v125
	v_cvt_f32_i32_e32 v102, v124
	v_cvt_f32_i32_e32 v105, v131
	v_cvt_f32_i32_e32 v104, v130
	v_cvt_f32_i32_e32 v93, v91
	v_cvt_f32_i32_e32 v92, v90
	v_cvt_f32_i32_e32 v97, v97
	v_cvt_f32_i32_e32 v96, v96
	v_cvt_f32_i32_e32 v199, v31
	v_cvt_f32_i32_e32 v198, v30
	v_cvt_f32_i32_e32 v31, v57
	v_cvt_f32_i32_e32 v30, v56
	v_cvt_f32_i32_e32 v57, v77
	v_cvt_f32_i32_e32 v56, v76
	v_cvt_f32_i32_e32 v77, v83
	v_cvt_f32_i32_e32 v76, v82
	v_cvt_f32_i32_e32 v83, v119
	v_cvt_f32_i32_e32 v82, v118
	v_cvt_f32_i32_e32 v91, v121
	v_cvt_f32_i32_e32 v90, v120
	v_readlane_b32 s28, v252, 15
	v_cvt_f32_i32_e32 v173, v15
	v_cvt_f32_i32_e32 v172, v14
	v_cvt_f32_i32_e32 v181, v21
	v_cvt_f32_i32_e32 v180, v20
	v_cvt_f32_i32_e32 v183, v19
	v_cvt_f32_i32_e32 v182, v18
	v_cvt_f32_i32_e32 v185, v25
	v_cvt_f32_i32_e32 v184, v24
	v_cvt_f32_i32_e32 v15, v41
	v_cvt_f32_i32_e32 v14, v40
	s_waitcnt vmcnt(0)
	v_pk_mul_f32 v[156:157], v[152:153], s[58:59] op_sel_hi:[1,0]
	v_pk_mul_f32 v[158:159], v[150:151], s[58:59] op_sel_hi:[1,0]
	v_cvt_f32_i32_e32 v151, v5
	v_cvt_f32_i32_e32 v150, v4
	v_cvt_f32_i32_e32 v153, v3
	v_cvt_f32_i32_e32 v152, v2
	global_load_dwordx4 v[2:5], v[212:213], off offset:512
	global_load_dwordx4 v[6:9], v[212:213], off offset:528
	v_cvt_f32_i32_e32 v19, v45
	v_cvt_f32_i32_e32 v18, v44
	v_cvt_f32_i32_e32 v21, v43
	v_cvt_f32_i32_e32 v20, v42
	v_cvt_f32_i32_e32 v25, v47
	v_cvt_f32_i32_e32 v24, v46
	v_cvt_f32_i32_e32 v41, v63
	v_cvt_f32_i32_e32 v40, v62
	v_cvt_f32_i32_e32 v43, v69
	v_cvt_f32_i32_e32 v42, v68
	v_cvt_f32_i32_e32 v45, v67
	v_cvt_f32_i32_e32 v44, v66
	v_cvt_f32_i32_e32 v47, v73
	v_cvt_f32_i32_e32 v46, v72
	v_cvt_f32_i32_e32 v63, v81
	v_cvt_f32_i32_e32 v62, v80
	v_cvt_f32_i32_e32 v73, v85
	v_cvt_f32_i32_e32 v72, v84
	v_cvt_f32_i32_e32 v81, v87
	v_cvt_f32_i32_e32 v80, v86
	v_cvt_f32_i32_e32 v67, v111
	v_cvt_f32_i32_e32 v66, v110
	v_cvt_f32_i32_e32 v69, v109
	v_cvt_f32_i32_e32 v68, v108
	v_cvt_f32_i32_e32 v85, v117
	v_cvt_f32_i32_e32 v84, v116
	v_cvt_f32_i32_e32 v87, v123
	v_cvt_f32_i32_e32 v86, v122
	v_pk_mul_f32 v[110:111], v[134:135], s[58:59] op_sel_hi:[1,0]
	v_lshlrev_b64 v[108:109], 12, v[208:209]
	v_readlane_b32 s29, v252, 16
	v_pk_mul_f32 v[106:107], v[206:207], v[106:107] op_sel_hi:[0,1]
	v_pk_mul_f32 v[100:101], v[206:207], v[100:101] op_sel_hi:[0,1]
	v_cvt_f32_i32_e32 v165, v13
	v_cvt_f32_i32_e32 v164, v12
	v_cvt_f32_i32_e32 v187, v23
	v_cvt_f32_i32_e32 v186, v22
	v_cvt_f32_i32_e32 v13, v35
	v_cvt_f32_i32_e32 v12, v34
	v_cvt_f32_i32_e32 v23, v49
	v_cvt_f32_i32_e32 v22, v48
	v_cvt_f32_i32_e32 v35, v61
	v_cvt_f32_i32_e32 v34, v60
	v_cvt_f32_i32_e32 v49, v71
	v_cvt_f32_i32_e32 v48, v70
	v_cvt_f32_i32_e32 v61, v75
	v_cvt_f32_i32_e32 v60, v74
	v_cvt_f32_i32_e32 v71, v115
	v_cvt_f32_i32_e32 v70, v114
	v_cvt_f32_i32_e32 v75, v113
	v_cvt_f32_i32_e32 v74, v112
	v_pk_mul_f32 v[112:113], v[132:133], s[58:59] op_sel_hi:[1,0]
	v_lshl_add_u64 v[108:109], s[28:29], 0, v[108:109]
	v_lshlrev_b64 v[114:115], 1, v[210:211]
	v_pk_mul_f32 v[104:105], v[206:207], v[104:105] op_sel_hi:[0,1]
	v_pk_mul_f32 v[102:103], v[206:207], v[102:103] op_sel_hi:[0,1]
	v_pk_mul_f32 v[116:117], v[110:111], v[100:101]
	v_pk_mul_f32 v[100:101], v[158:159], v[106:107]
	v_pk_mul_f32 v[94:95], v[206:207], v[94:95] op_sel_hi:[0,1]
	v_pk_mul_f32 v[88:89], v[206:207], v[88:89] op_sel_hi:[0,1]
	v_lshl_add_u64 v[108:109], v[108:109], 0, v[114:115]
	v_pk_mul_f32 v[102:103], v[112:113], v[102:103]
	v_pk_mul_f32 v[104:105], v[156:157], v[104:105]
	v_cvt_pk_bf16_f32 v100, v100, v101
	v_pk_mul_f32 v[96:97], v[206:207], v[96:97] op_sel_hi:[0,1]
	v_cvt_pk_bf16_f32 v101, v104, v105
	v_pk_mul_f32 v[92:93], v[206:207], v[92:93] op_sel_hi:[0,1]
	v_cvt_pk_bf16_f32 v102, v102, v103
	v_cvt_pk_bf16_f32 v103, v116, v117
	global_store_dwordx4 v[108:109], v[100:103], off
	v_pk_mul_f32 v[90:91], v[202:203], v[90:91] op_sel_hi:[0,1]
	v_pk_mul_f32 v[82:83], v[202:203], v[82:83] op_sel_hi:[0,1]
	v_pk_mul_f32 v[86:87], v[202:203], v[86:87] op_sel_hi:[0,1]
	v_pk_mul_f32 v[84:85], v[202:203], v[84:85] op_sel_hi:[0,1]
	v_pk_mul_f32 v[78:79], v[202:203], v[78:79] op_sel_hi:[0,1]
	v_pk_mul_f32 v[72:73], v[202:203], v[72:73] op_sel_hi:[0,1]
	v_pk_mul_f32 v[84:85], v[112:113], v[84:85]
	v_pk_mul_f32 v[86:87], v[156:157], v[86:87]
	s_waitcnt vmcnt(0)
	v_pk_mul_f32 v[2:3], v[2:3], s[58:59] op_sel_hi:[1,0]
	v_pk_mul_f32 v[8:9], v[8:9], s[58:59] op_sel_hi:[1,0]
	v_pk_mul_f32 v[6:7], v[6:7], s[58:59] op_sel_hi:[1,0]
	v_pk_mul_f32 v[4:5], v[4:5], s[58:59] op_sel_hi:[1,0]
	v_pk_mul_f32 v[94:95], v[2:3], v[94:95]
	v_pk_mul_f32 v[88:89], v[8:9], v[88:89]
	v_pk_mul_f32 v[96:97], v[4:5], v[96:97]
	v_pk_mul_f32 v[100:101], v[6:7], v[92:93]
	v_cvt_pk_bf16_f32 v92, v94, v95
	v_cvt_pk_bf16_f32 v93, v96, v97
	v_pk_mul_f32 v[80:81], v[202:203], v[80:81] op_sel_hi:[0,1]
	v_cvt_pk_bf16_f32 v94, v100, v101
	v_cvt_pk_bf16_f32 v95, v88, v89
	v_lshlrev_b64 v[88:89], 12, v[204:205]
	global_store_dwordx4 v[108:109], v[92:95], off offset:256
	v_lshl_add_u64 v[88:89], s[28:29], 0, v[88:89]
	v_lshl_add_u64 v[88:89], v[88:89], 0, v[114:115]
	v_pk_mul_f32 v[92:93], v[110:111], v[82:83]
	v_pk_mul_f32 v[82:83], v[158:159], v[90:91]
	v_pk_mul_f32 v[76:77], v[202:203], v[76:77] op_sel_hi:[0,1]
	v_cvt_pk_bf16_f32 v82, v82, v83
	v_cvt_pk_bf16_f32 v83, v86, v87
	v_pk_mul_f32 v[78:79], v[4:5], v[78:79]
	v_pk_mul_f32 v[72:73], v[8:9], v[72:73]
	v_cvt_pk_bf16_f32 v84, v84, v85
	v_cvt_pk_bf16_f32 v85, v92, v93
	global_store_dwordx4 v[88:89], v[82:85], off
	v_pk_mul_f32 v[80:81], v[2:3], v[80:81]
	v_pk_mul_f32 v[74:75], v[190:191], v[74:75] op_sel_hi:[0,1]
	v_pk_mul_f32 v[82:83], v[6:7], v[76:77]
	v_cvt_pk_bf16_f32 v76, v80, v81
	v_cvt_pk_bf16_f32 v77, v78, v79
	v_pk_mul_f32 v[66:67], v[190:191], v[66:67] op_sel_hi:[0,1]
	v_cvt_pk_bf16_f32 v78, v82, v83
	v_cvt_pk_bf16_f32 v79, v72, v73
	v_lshlrev_b64 v[72:73], 12, v[200:201]
	global_store_dwordx4 v[88:89], v[76:79], off offset:256
	v_lshl_add_u64 v[72:73], s[28:29], 0, v[72:73]
	v_pk_mul_f32 v[70:71], v[190:191], v[70:71] op_sel_hi:[0,1]
	v_pk_mul_f32 v[68:69], v[190:191], v[68:69] op_sel_hi:[0,1]
	v_pk_mul_f32 v[76:77], v[110:111], v[66:67]
	v_pk_mul_f32 v[66:67], v[158:159], v[74:75]
	v_pk_mul_f32 v[62:63], v[190:191], v[62:63] op_sel_hi:[0,1]
	v_pk_mul_f32 v[56:57], v[190:191], v[56:57] op_sel_hi:[0,1]
	v_lshl_add_u64 v[72:73], v[72:73], 0, v[114:115]
	v_pk_mul_f32 v[68:69], v[112:113], v[68:69]
	v_pk_mul_f32 v[70:71], v[156:157], v[70:71]
	v_cvt_pk_bf16_f32 v66, v66, v67
	v_pk_mul_f32 v[64:65], v[190:191], v[64:65] op_sel_hi:[0,1]
	v_cvt_pk_bf16_f32 v67, v70, v71
	v_pk_mul_f32 v[60:61], v[190:191], v[60:61] op_sel_hi:[0,1]
	v_pk_mul_f32 v[62:63], v[4:5], v[62:63]
	v_pk_mul_f32 v[56:57], v[8:9], v[56:57]
	v_cvt_pk_bf16_f32 v68, v68, v69
	v_cvt_pk_bf16_f32 v69, v76, v77
	global_store_dwordx4 v[72:73], v[66:69], off
	v_pk_mul_f32 v[64:65], v[2:3], v[64:65]
	v_pk_mul_f32 v[58:59], v[174:175], v[58:59] op_sel_hi:[0,1]
	v_pk_mul_f32 v[66:67], v[6:7], v[60:61]
	v_cvt_pk_bf16_f32 v60, v64, v65
	v_cvt_pk_bf16_f32 v61, v62, v63
	v_pk_mul_f32 v[50:51], v[174:175], v[50:51] op_sel_hi:[0,1]
	v_cvt_pk_bf16_f32 v62, v66, v67
	v_cvt_pk_bf16_f32 v63, v56, v57
	v_lshlrev_b64 v[56:57], 12, v[188:189]
	global_store_dwordx4 v[72:73], v[60:63], off offset:256
	v_lshl_add_u64 v[56:57], s[28:29], 0, v[56:57]
	v_pk_mul_f32 v[54:55], v[174:175], v[54:55] op_sel_hi:[0,1]
	v_pk_mul_f32 v[52:53], v[174:175], v[52:53] op_sel_hi:[0,1]
	v_pk_mul_f32 v[60:61], v[110:111], v[50:51]
	v_pk_mul_f32 v[50:51], v[158:159], v[58:59]
	v_pk_mul_f32 v[44:45], v[174:175], v[44:45] op_sel_hi:[0,1]
	v_lshl_add_u64 v[56:57], v[56:57], 0, v[114:115]
	v_pk_mul_f32 v[52:53], v[112:113], v[52:53]
	v_pk_mul_f32 v[54:55], v[156:157], v[54:55]
	v_cvt_pk_bf16_f32 v50, v50, v51
	v_pk_mul_f32 v[48:49], v[174:175], v[48:49] op_sel_hi:[0,1]
	v_cvt_pk_bf16_f32 v51, v54, v55
	v_pk_mul_f32 v[46:47], v[174:175], v[46:47] op_sel_hi:[0,1]
	v_pk_mul_f32 v[42:43], v[174:175], v[42:43] op_sel_hi:[0,1]
	v_pk_mul_f32 v[44:45], v[6:7], v[44:45]
	v_cvt_pk_bf16_f32 v52, v52, v53
	v_cvt_pk_bf16_f32 v53, v60, v61
	global_store_dwordx4 v[56:57], v[50:53], off
	v_pk_mul_f32 v[46:47], v[4:5], v[46:47]
	v_pk_mul_f32 v[48:49], v[2:3], v[48:49]
	v_pk_mul_f32 v[50:51], v[8:9], v[42:43]
	v_cvt_pk_bf16_f32 v42, v48, v49
	v_cvt_pk_bf16_f32 v43, v46, v47
	v_cvt_pk_bf16_f32 v44, v44, v45
	s_mov_b64 s[28:29], 0x80000
	v_cvt_pk_bf16_f32 v45, v50, v51
	v_pk_mul_f32 v[40:41], v[168:169], v[40:41] op_sel_hi:[0,1]
	v_pk_mul_f32 v[38:39], v[168:169], v[38:39] op_sel_hi:[0,1]
	v_pk_mul_f32 v[34:35], v[168:169], v[34:35] op_sel_hi:[0,1]
	global_store_dwordx4 v[56:57], v[42:45], off offset:256
	v_pk_mul_f32 v[36:37], v[168:169], v[36:37] op_sel_hi:[0,1]
	v_pk_mul_f32 v[38:39], v[156:157], v[38:39]
	v_lshl_add_u64 v[42:43], v[108:109], 0, s[28:29]
	v_pk_mul_f32 v[44:45], v[110:111], v[34:35]
	v_pk_mul_f32 v[34:35], v[158:159], v[40:41]
	s_mov_b32 s28, 0x80000
	v_pk_mul_f32 v[36:37], v[112:113], v[36:37]
	v_cvt_pk_bf16_f32 v34, v34, v35
	v_cvt_pk_bf16_f32 v35, v38, v39
	v_add_co_u32_e32 v38, vcc, s28, v108
	v_cvt_pk_bf16_f32 v36, v36, v37
	v_cvt_pk_bf16_f32 v37, v44, v45
	v_pk_mul_f32 v[40:41], v[168:169], v[192:193] op_sel_hi:[0,1]
	s_nop 0
	v_addc_co_u32_e32 v39, vcc, 0, v109, vcc
	global_store_dwordx4 v[38:39], v[34:37], off
	v_pk_mul_f32 v[38:39], v[168:169], v[194:195] op_sel_hi:[0,1]
	v_pk_mul_f32 v[40:41], v[8:9], v[40:41]
	v_pk_mul_f32 v[34:35], v[168:169], v[198:199] op_sel_hi:[0,1]
	v_pk_mul_f32 v[36:37], v[168:169], v[196:197] op_sel_hi:[0,1]
	v_pk_mul_f32 v[36:37], v[4:5], v[36:37]
	v_pk_mul_f32 v[34:35], v[2:3], v[34:35]
	v_pk_mul_f32 v[38:39], v[6:7], v[38:39]
	v_cvt_pk_bf16_f32 v34, v34, v35
	v_cvt_pk_bf16_f32 v35, v36, v37
	s_mov_b64 s[28:29], 0x90000
	v_cvt_pk_bf16_f32 v36, v38, v39
	v_cvt_pk_bf16_f32 v37, v40, v41
	v_pk_mul_f32 v[32:33], v[162:163], v[32:33] op_sel_hi:[0,1]
	v_pk_mul_f32 v[30:31], v[162:163], v[30:31] op_sel_hi:[0,1]
	v_pk_mul_f32 v[26:27], v[162:163], v[26:27] op_sel_hi:[0,1]
	global_store_dwordx4 v[42:43], v[34:37], off offset:256
	v_pk_mul_f32 v[28:29], v[162:163], v[28:29] op_sel_hi:[0,1]
	v_pk_mul_f32 v[30:31], v[156:157], v[30:31]
	v_lshl_add_u64 v[34:35], v[108:109], 0, s[28:29]
	v_pk_mul_f32 v[36:37], v[110:111], v[26:27]
	v_pk_mul_f32 v[26:27], v[158:159], v[32:33]
	s_mov_b32 s28, 0x90000
	v_pk_mul_f32 v[28:29], v[112:113], v[28:29]
	v_cvt_pk_bf16_f32 v26, v26, v27
	v_cvt_pk_bf16_f32 v27, v30, v31
	v_add_co_u32_e32 v30, vcc, s28, v108
	v_cvt_pk_bf16_f32 v28, v28, v29
	v_cvt_pk_bf16_f32 v29, v36, v37
	v_pk_mul_f32 v[32:33], v[162:163], v[180:181] op_sel_hi:[0,1]
	s_nop 0
	v_addc_co_u32_e32 v31, vcc, 0, v109, vcc
	global_store_dwordx4 v[30:31], v[26:29], off
	v_pk_mul_f32 v[30:31], v[162:163], v[182:183] op_sel_hi:[0,1]
	v_pk_mul_f32 v[32:33], v[8:9], v[32:33]
	v_pk_mul_f32 v[26:27], v[162:163], v[186:187] op_sel_hi:[0,1]
	v_pk_mul_f32 v[28:29], v[162:163], v[184:185] op_sel_hi:[0,1]
	v_pk_mul_f32 v[28:29], v[4:5], v[28:29]
	v_pk_mul_f32 v[26:27], v[2:3], v[26:27]
	v_pk_mul_f32 v[30:31], v[6:7], v[30:31]
	v_cvt_pk_bf16_f32 v26, v26, v27
	v_cvt_pk_bf16_f32 v27, v28, v29
	s_mov_b64 s[28:29], 0xa0000
	v_cvt_pk_bf16_f32 v28, v30, v31
	v_cvt_pk_bf16_f32 v29, v32, v33
	v_pk_mul_f32 v[24:25], v[148:149], v[24:25] op_sel_hi:[0,1]
	v_pk_mul_f32 v[22:23], v[148:149], v[22:23] op_sel_hi:[0,1]
	v_pk_mul_f32 v[18:19], v[148:149], v[18:19] op_sel_hi:[0,1]
	global_store_dwordx4 v[34:35], v[26:29], off offset:256
	v_pk_mul_f32 v[20:21], v[148:149], v[20:21] op_sel_hi:[0,1]
	v_pk_mul_f32 v[22:23], v[156:157], v[22:23]
	v_lshl_add_u64 v[26:27], v[108:109], 0, s[28:29]
	v_pk_mul_f32 v[28:29], v[110:111], v[18:19]
	v_pk_mul_f32 v[18:19], v[158:159], v[24:25]
	s_mov_b32 s28, 0xa0000
	v_pk_mul_f32 v[20:21], v[112:113], v[20:21]
	v_cvt_pk_bf16_f32 v18, v18, v19
	v_cvt_pk_bf16_f32 v19, v22, v23
	v_add_co_u32_e32 v22, vcc, s28, v108
	v_cvt_pk_bf16_f32 v20, v20, v21
	v_cvt_pk_bf16_f32 v21, v28, v29
	v_pk_mul_f32 v[24:25], v[148:149], v[164:165] op_sel_hi:[0,1]
	s_nop 0
	v_addc_co_u32_e32 v23, vcc, 0, v109, vcc
	global_store_dwordx4 v[22:23], v[18:21], off
	v_pk_mul_f32 v[22:23], v[148:149], v[166:167] op_sel_hi:[0,1]
	v_pk_mul_f32 v[24:25], v[8:9], v[24:25]
	v_pk_mul_f32 v[18:19], v[148:149], v[172:173] op_sel_hi:[0,1]
	v_pk_mul_f32 v[20:21], v[148:149], v[170:171] op_sel_hi:[0,1]
	v_pk_mul_f32 v[20:21], v[4:5], v[20:21]
	v_pk_mul_f32 v[18:19], v[2:3], v[18:19]
	v_pk_mul_f32 v[22:23], v[6:7], v[22:23]
	v_cvt_pk_bf16_f32 v18, v18, v19
	v_cvt_pk_bf16_f32 v19, v20, v21
	s_mov_b64 s[28:29], 0xb0000
	v_cvt_pk_bf16_f32 v20, v22, v23
	v_cvt_pk_bf16_f32 v21, v24, v25
	v_pk_mul_f32 v[16:17], v[146:147], v[16:17] op_sel_hi:[0,1]
	v_pk_mul_f32 v[14:15], v[146:147], v[14:15] op_sel_hi:[0,1]
	v_pk_mul_f32 v[10:11], v[146:147], v[10:11] op_sel_hi:[0,1]
	global_store_dwordx4 v[26:27], v[18:21], off offset:256
	v_pk_mul_f32 v[12:13], v[146:147], v[12:13] op_sel_hi:[0,1]
	v_pk_mul_f32 v[14:15], v[156:157], v[14:15]
	v_lshl_add_u64 v[18:19], v[108:109], 0, s[28:29]
	v_pk_mul_f32 v[20:21], v[110:111], v[10:11]
	v_pk_mul_f32 v[10:11], v[158:159], v[16:17]
	s_mov_b32 s28, 0xb0000
	v_pk_mul_f32 v[12:13], v[112:113], v[12:13]
	v_cvt_pk_bf16_f32 v10, v10, v11
	v_cvt_pk_bf16_f32 v11, v14, v15
	v_add_co_u32_e32 v14, vcc, s28, v108
	v_cvt_pk_bf16_f32 v12, v12, v13
	v_cvt_pk_bf16_f32 v13, v20, v21
	v_pk_mul_f32 v[16:17], v[146:147], v[150:151] op_sel_hi:[0,1]
	s_nop 0
	v_addc_co_u32_e32 v15, vcc, 0, v109, vcc
	global_store_dwordx4 v[14:15], v[10:13], off
	v_pk_mul_f32 v[14:15], v[146:147], v[152:153] op_sel_hi:[0,1]
	s_and_b64 vcc, exec, s[0:1]
	v_pk_mul_f32 v[10:11], v[146:147], v[160:161] op_sel_hi:[0,1]
	v_pk_mul_f32 v[12:13], v[146:147], v[154:155] op_sel_hi:[0,1]
	v_pk_mul_f32 v[4:5], v[4:5], v[12:13]
	v_pk_mul_f32 v[2:3], v[2:3], v[10:11]
	s_mov_b32 s28, s84
	s_mov_b32 s29, s85
	s_mov_b32 s70, s92
	s_mov_b64 s[34:35], s[24:25]
	s_mov_b64 s[30:31], s[22:23]
	v_pk_mul_f32 v[8:9], v[8:9], v[16:17]
	v_pk_mul_f32 v[6:7], v[6:7], v[14:15]
	v_cvt_pk_bf16_f32 v2, v2, v3
	v_cvt_pk_bf16_f32 v3, v4, v5
	s_nop 0
	v_cvt_pk_bf16_f32 v4, v6, v7
	v_cvt_pk_bf16_f32 v5, v8, v9
	global_store_dwordx4 v[18:19], v[2:5], off offset:256
	s_cbranch_vccz .LBB0_2003
	s_waitcnt vmcnt(0)
	v_readlane_b32 s0, v255, 48
	v_readlane_b32 s84, v252, 13
	v_readlane_b32 s70, v252, 21
	v_readlane_b32 s74, v255, 49
	s_cmpk_gt_u32 s0, 0xff
	v_readlane_b32 s85, v252, 14
	v_readlane_b32 s71, v252, 22
	v_readlane_b32 s75, v255, 50
	s_cbranch_scc1 .LBB0_2014
	s_barrier

.LBB0_2088:
	s_add_u32 s40, s38, 0xfffc0080
	s_addc_u32 s41, s39, -1
	s_add_i32 s46, 0, 0x10000
	v_add_u32_e32 v144, s46, v145
	ds_read_b128 v[146:149], v144
	ds_read_b128 v[150:153], v144 offset:1024
	ds_read_b128 v[154:157], v144 offset:2048
	ds_read_b128 v[158:161], v144 offset:3072
	s_cmp_eq_u32 s45, 12
	s_cselect_b32 s43, s8, s41
	s_cselect_b32 s42, s27, s40
	s_cselect_b32 s41, s25, s44
	s_cselect_b32 s40, s35, s37
	v_lshl_add_u64 v[198:199], s[38:39], 0, v[140:141]
	s_add_i32 m0, s5, 0xc000
	ds_read_b128 v[164:167], v169
	ds_read_b128 v[170:173], v169 offset:1024
	ds_read_b128 v[174:177], v169 offset:2048
	ds_read_b128 v[178:181], v169 offset:3072
	ds_read_b128 v[182:185], v169 offset:4096
	ds_read_b128 v[186:189], v169 offset:5120
	ds_read_b128 v[190:193], v169 offset:6144
	ds_read_b128 v[194:197], v169 offset:7168
	global_load_lds_dwordx4 v[198:199], off
	v_lshl_add_u64 v[198:199], s[38:39], 0, v[142:143]
	s_add_i32 m0, s5, 0xe000
	s_nop 0
	global_load_lds_dwordx4 v[198:199], off
	s_waitcnt lgkmcnt(8)
	s_barrier
	s_waitcnt lgkmcnt(0)
	s_waitcnt lgkmcnt(0)
	v_mfma_i32_16x16x64_i8 v[128:131], v[146:149], v[164:167], v[128:131]
	v_mfma_i32_16x16x64_i8 v[120:123], v[154:157], v[164:167], v[120:123]
	v_mfma_i32_16x16x64_i8 v[112:115], v[146:149], v[174:177], v[112:115]
	v_mfma_i32_16x16x64_i8 v[108:111], v[154:157], v[174:177], v[108:111]
	v_mfma_i32_16x16x64_i8 v[94:97], v[146:149], v[182:185], v[94:97]
	v_mfma_i32_16x16x64_i8 v[90:93], v[154:157], v[182:185], v[90:93]
	v_mfma_i32_16x16x64_i8 v[78:81], v[146:149], v[190:193], v[78:81]
	v_mfma_i32_16x16x64_i8 v[74:77], v[154:157], v[190:193], v[74:77]
	v_mfma_i32_16x16x64_i8 v[128:131], v[150:153], v[170:173], v[128:131]
	v_mfma_i32_16x16x64_i8 v[120:123], v[158:161], v[170:173], v[120:123]
	v_mfma_i32_16x16x64_i8 v[112:115], v[150:153], v[178:181], v[112:115]
	v_mfma_i32_16x16x64_i8 v[108:111], v[158:161], v[178:181], v[108:111]
	v_mfma_i32_16x16x64_i8 v[94:97], v[150:153], v[186:189], v[94:97]
	v_mfma_i32_16x16x64_i8 v[90:93], v[158:161], v[186:189], v[90:93]
	v_mfma_i32_16x16x64_i8 v[78:81], v[150:153], v[194:197], v[78:81]
	v_mfma_i32_16x16x64_i8 v[74:77], v[158:161], v[194:197], v[74:77]
	s_barrier
	s_add_i32 s48, 0, 0x14000
	s_add_i32 s46, s46, s3
	v_add_u32_e32 v144, s48, v145
	v_lshl_add_u64 v[214:215], s[40:41], 0, v[98:99]
	s_mov_b32 m0, s46
	ds_read_b128 v[198:201], v144
	ds_read_b128 v[202:205], v144 offset:1024
	ds_read_b128 v[206:209], v144 offset:2048
	ds_read_b128 v[210:213], v144 offset:3072
	global_load_lds_dwordx4 v[214:215], off
	v_lshl_add_u64 v[216:217], s[40:41], 0, v[136:137]
	s_add_i32 m0, s46, 0x2000
	s_nop 0
	global_load_lds_dwordx4 v[216:217], off
	s_barrier
	s_waitcnt lgkmcnt(0)
	s_waitcnt lgkmcnt(0)
	v_mfma_i32_16x16x64_i8 v[124:127], v[198:201], v[164:167], v[124:127]
	v_mfma_i32_16x16x64_i8 v[116:119], v[206:209], v[164:167], v[116:119]
	v_mfma_i32_16x16x64_i8 v[104:107], v[198:201], v[174:177], v[104:107]
	v_mfma_i32_16x16x64_i8 v[100:103], v[206:209], v[174:177], v[100:103]
	v_mfma_i32_16x16x64_i8 v[86:89], v[198:201], v[182:185], v[86:89]
	v_mfma_i32_16x16x64_i8 v[82:85], v[206:209], v[182:185], v[82:85]
	v_mfma_i32_16x16x64_i8 v[70:73], v[198:201], v[190:193], v[70:73]
	v_mfma_i32_16x16x64_i8 v[66:69], v[206:209], v[190:193], v[66:69]
	v_mfma_i32_16x16x64_i8 v[124:127], v[202:205], v[170:173], v[124:127]
	v_mfma_i32_16x16x64_i8 v[116:119], v[210:213], v[170:173], v[116:119]
	v_mfma_i32_16x16x64_i8 v[104:107], v[202:205], v[178:181], v[104:107]
	v_mfma_i32_16x16x64_i8 v[100:103], v[210:213], v[178:181], v[100:103]
	v_mfma_i32_16x16x64_i8 v[86:89], v[202:205], v[186:189], v[86:89]
	v_mfma_i32_16x16x64_i8 v[82:85], v[210:213], v[186:189], v[82:85]
	v_mfma_i32_16x16x64_i8 v[70:73], v[202:205], v[194:197], v[70:73]
	v_mfma_i32_16x16x64_i8 v[66:69], v[210:213], v[194:197], v[66:69]
	s_mov_b32 m0, s5
	v_lshl_add_u64 v[218:219], s[42:43], 0, v[132:133]
	s_barrier
	ds_read_b128 v[164:167], v169 offset:16384
	ds_read_b128 v[170:173], v169 offset:17408
	ds_read_b128 v[174:177], v169 offset:18432
	ds_read_b128 v[178:181], v169 offset:19456
	ds_read_b128 v[182:185], v169 offset:20480
	ds_read_b128 v[186:189], v169 offset:21504
	ds_read_b128 v[190:193], v169 offset:22528
	ds_read_b128 v[194:197], v169 offset:23552
	global_load_lds_dwordx4 v[218:219], off
	v_lshl_add_u64 v[222:223], s[42:43], 0, v[134:135]
	s_mov_b32 m0, s18
	s_nop 0
	global_load_lds_dwordx4 v[222:223], off
	s_barrier
	s_waitcnt lgkmcnt(0)
	s_waitcnt lgkmcnt(0)
	v_mfma_i32_16x16x64_i8 v[62:65], v[146:149], v[164:167], v[62:65]
	v_mfma_i32_16x16x64_i8 v[58:61], v[154:157], v[164:167], v[58:61]
	v_mfma_i32_16x16x64_i8 v[46:49], v[146:149], v[174:177], v[46:49]
	v_mfma_i32_16x16x64_i8 v[42:45], v[154:157], v[174:177], v[42:45]
	v_mfma_i32_16x16x64_i8 v[30:33], v[146:149], v[182:185], v[30:33]
	v_mfma_i32_16x16x64_i8 v[26:29], v[154:157], v[182:185], v[26:29]
	v_mfma_i32_16x16x64_i8 v[14:17], v[146:149], v[190:193], v[14:17]
	v_mfma_i32_16x16x64_i8 v[10:13], v[154:157], v[190:193], v[10:13]
	v_mfma_i32_16x16x64_i8 v[62:65], v[150:153], v[170:173], v[62:65]
	v_mfma_i32_16x16x64_i8 v[58:61], v[158:161], v[170:173], v[58:61]
	v_mfma_i32_16x16x64_i8 v[46:49], v[150:153], v[178:181], v[46:49]
	v_mfma_i32_16x16x64_i8 v[42:45], v[158:161], v[178:181], v[42:45]
	v_mfma_i32_16x16x64_i8 v[30:33], v[150:153], v[186:189], v[30:33]
	v_mfma_i32_16x16x64_i8 v[26:29], v[158:161], v[186:189], v[26:29]
	v_mfma_i32_16x16x64_i8 v[14:17], v[150:153], v[194:197], v[14:17]
	v_mfma_i32_16x16x64_i8 v[10:13], v[158:161], v[194:197], v[10:13]
	s_barrier
	s_add_u32 s46, s40, 0x40000
	s_addc_u32 s47, s41, 0
	s_add_i32 s48, s48, s3
	v_lshl_add_u64 v[146:147], s[46:47], 0, v[98:99]
	s_mov_b32 m0, s48
	s_nop 0
	global_load_lds_dwordx4 v[146:147], off
	v_lshl_add_u64 v[146:147], s[46:47], 0, v[136:137]
	s_add_i32 m0, s48, 0x2000
	s_nop 0
	global_load_lds_dwordx4 v[146:147], off
	s_waitcnt vmcnt(6)
	s_barrier
	v_mfma_i32_16x16x64_i8 v[54:57], v[198:201], v[164:167], v[54:57]
	v_mfma_i32_16x16x64_i8 v[50:53], v[206:209], v[164:167], v[50:53]
	v_mfma_i32_16x16x64_i8 v[38:41], v[198:201], v[174:177], v[38:41]
	v_mfma_i32_16x16x64_i8 v[34:37], v[206:209], v[174:177], v[34:37]
	v_mfma_i32_16x16x64_i8 v[22:25], v[198:201], v[182:185], v[22:25]
	v_mfma_i32_16x16x64_i8 v[18:21], v[206:209], v[182:185], v[18:21]
	v_mfma_i32_16x16x64_i8 v[6:9], v[198:201], v[190:193], v[6:9]
	v_mfma_i32_16x16x64_i8 v[2:5], v[206:209], v[190:193], v[2:5]
	v_mfma_i32_16x16x64_i8 v[54:57], v[202:205], v[170:173], v[54:57]
	v_mfma_i32_16x16x64_i8 v[50:53], v[210:213], v[170:173], v[50:53]
	v_mfma_i32_16x16x64_i8 v[38:41], v[202:205], v[178:181], v[38:41]
	v_mfma_i32_16x16x64_i8 v[34:37], v[210:213], v[178:181], v[34:37]
	v_mfma_i32_16x16x64_i8 v[22:25], v[202:205], v[186:189], v[22:25]
	v_mfma_i32_16x16x64_i8 v[18:21], v[210:213], v[186:189], v[18:21]
	v_mfma_i32_16x16x64_i8 v[6:9], v[202:205], v[194:197], v[6:9]
	v_mfma_i32_16x16x64_i8 v[2:5], v[210:213], v[194:197], v[2:5]
	s_add_i32 s46, 0, 0x18000
	v_add_u32_e32 v144, s46, v145
	s_barrier
	ds_read_b128 v[146:149], v144
	ds_read_b128 v[150:153], v144 offset:1024
	ds_read_b128 v[154:157], v144 offset:2048
	ds_read_b128 v[158:161], v144 offset:3072
	s_add_u32 s42, s42, 0x40000
	s_addc_u32 s43, s43, 0
	s_mov_b32 m0, s19
	v_lshl_add_u64 v[198:199], s[42:43], 0, v[132:133]
	ds_read_b128 v[164:167], v169 offset:32768
	ds_read_b128 v[170:173], v169 offset:33792
	ds_read_b128 v[174:177], v169 offset:34816
	ds_read_b128 v[178:181], v169 offset:35840
	ds_read_b128 v[182:185], v169 offset:36864
	ds_read_b128 v[186:189], v169 offset:37888
	ds_read_b128 v[190:193], v169 offset:38912
	ds_read_b128 v[194:197], v169 offset:39936
	global_load_lds_dwordx4 v[198:199], off
	v_lshl_add_u64 v[198:199], s[42:43], 0, v[134:135]
	s_mov_b32 m0, s20
	s_nop 0
	global_load_lds_dwordx4 v[198:199], off
	s_waitcnt lgkmcnt(8)
	s_barrier
	s_waitcnt lgkmcnt(0)
	s_waitcnt lgkmcnt(0)
	v_mfma_i32_16x16x64_i8 v[128:131], v[146:149], v[164:167], v[128:131]
	v_mfma_i32_16x16x64_i8 v[120:123], v[154:157], v[164:167], v[120:123]
	v_mfma_i32_16x16x64_i8 v[112:115], v[146:149], v[174:177], v[112:115]
	v_mfma_i32_16x16x64_i8 v[108:111], v[154:157], v[174:177], v[108:111]
	v_mfma_i32_16x16x64_i8 v[94:97], v[146:149], v[182:185], v[94:97]
	v_mfma_i32_16x16x64_i8 v[90:93], v[154:157], v[182:185], v[90:93]
	v_mfma_i32_16x16x64_i8 v[78:81], v[146:149], v[190:193], v[78:81]
	v_mfma_i32_16x16x64_i8 v[74:77], v[154:157], v[190:193], v[74:77]
	v_mfma_i32_16x16x64_i8 v[128:131], v[150:153], v[170:173], v[128:131]
	v_mfma_i32_16x16x64_i8 v[120:123], v[158:161], v[170:173], v[120:123]
	v_mfma_i32_16x16x64_i8 v[112:115], v[150:153], v[178:181], v[112:115]
	v_mfma_i32_16x16x64_i8 v[108:111], v[158:161], v[178:181], v[108:111]
	v_mfma_i32_16x16x64_i8 v[94:97], v[150:153], v[186:189], v[94:97]
	v_mfma_i32_16x16x64_i8 v[90:93], v[158:161], v[186:189], v[90:93]
	v_mfma_i32_16x16x64_i8 v[78:81], v[150:153], v[194:197], v[78:81]
	v_mfma_i32_16x16x64_i8 v[74:77], v[158:161], v[194:197], v[74:77]
	s_barrier
	s_add_i32 s42, 0, 0x1c000
	s_add_i32 s43, s46, s3
	v_add_u32_e32 v144, s42, v145
	v_lshl_add_u64 v[214:215], v[214:215], 0, s[68:69]
	s_mov_b32 m0, s43
	ds_read_b128 v[198:201], v144
	ds_read_b128 v[202:205], v144 offset:1024
	ds_read_b128 v[206:209], v144 offset:2048
	ds_read_b128 v[210:213], v144 offset:3072
	global_load_lds_dwordx4 v[214:215], off
	v_lshl_add_u64 v[214:215], v[216:217], 0, s[68:69]
	s_add_i32 m0, s43, 0x2000
	s_nop 0
	global_load_lds_dwordx4 v[214:215], off
	s_barrier
	s_waitcnt lgkmcnt(0)
	s_waitcnt lgkmcnt(0)
	v_mfma_i32_16x16x64_i8 v[124:127], v[198:201], v[164:167], v[124:127]
	v_mfma_i32_16x16x64_i8 v[116:119], v[206:209], v[164:167], v[116:119]
	v_mfma_i32_16x16x64_i8 v[104:107], v[198:201], v[174:177], v[104:107]
	v_mfma_i32_16x16x64_i8 v[100:103], v[206:209], v[174:177], v[100:103]
	v_mfma_i32_16x16x64_i8 v[86:89], v[198:201], v[182:185], v[86:89]
	v_mfma_i32_16x16x64_i8 v[82:85], v[206:209], v[182:185], v[82:85]
	v_mfma_i32_16x16x64_i8 v[70:73], v[198:201], v[190:193], v[70:73]
	v_mfma_i32_16x16x64_i8 v[66:69], v[206:209], v[190:193], v[66:69]
	v_mfma_i32_16x16x64_i8 v[124:127], v[202:205], v[170:173], v[124:127]
	v_mfma_i32_16x16x64_i8 v[116:119], v[210:213], v[170:173], v[116:119]
	v_mfma_i32_16x16x64_i8 v[104:107], v[202:205], v[178:181], v[104:107]
	v_mfma_i32_16x16x64_i8 v[100:103], v[210:213], v[178:181], v[100:103]
	v_mfma_i32_16x16x64_i8 v[86:89], v[202:205], v[186:189], v[86:89]
	v_mfma_i32_16x16x64_i8 v[82:85], v[210:213], v[186:189], v[82:85]
	v_mfma_i32_16x16x64_i8 v[70:73], v[202:205], v[194:197], v[70:73]
	v_mfma_i32_16x16x64_i8 v[66:69], v[210:213], v[194:197], v[66:69]
	s_mov_b32 m0, s9
	v_lshl_add_u64 v[214:215], v[218:219], 0, s[68:69]
	s_barrier
	ds_read_b128 v[164:167], v169 offset:49152
	ds_read_b128 v[170:173], v169 offset:50176
	ds_read_b128 v[174:177], v169 offset:51200
	ds_read_b128 v[178:181], v169 offset:52224
	ds_read_b128 v[182:185], v169 offset:53248
	ds_read_b128 v[186:189], v169 offset:54272
	ds_read_b128 v[190:193], v169 offset:55296
	ds_read_b128 v[194:197], v169 offset:56320
	global_load_lds_dwordx4 v[214:215], off
	v_lshl_add_u64 v[214:215], v[222:223], 0, s[68:69]
	s_mov_b32 m0, s21
	s_nop 0
	global_load_lds_dwordx4 v[214:215], off
	s_barrier
	s_waitcnt lgkmcnt(0)
	s_waitcnt lgkmcnt(0)
	v_mfma_i32_16x16x64_i8 v[62:65], v[146:149], v[164:167], v[62:65]
	v_mfma_i32_16x16x64_i8 v[58:61], v[154:157], v[164:167], v[58:61]
	v_mfma_i32_16x16x64_i8 v[46:49], v[146:149], v[174:177], v[46:49]
	v_mfma_i32_16x16x64_i8 v[42:45], v[154:157], v[174:177], v[42:45]
	v_mfma_i32_16x16x64_i8 v[30:33], v[146:149], v[182:185], v[30:33]
	v_mfma_i32_16x16x64_i8 v[26:29], v[154:157], v[182:185], v[26:29]
	v_mfma_i32_16x16x64_i8 v[14:17], v[146:149], v[190:193], v[14:17]
	v_mfma_i32_16x16x64_i8 v[10:13], v[154:157], v[190:193], v[10:13]
	v_mfma_i32_16x16x64_i8 v[62:65], v[150:153], v[170:173], v[62:65]
	v_mfma_i32_16x16x64_i8 v[58:61], v[158:161], v[170:173], v[58:61]
	v_mfma_i32_16x16x64_i8 v[46:49], v[150:153], v[178:181], v[46:49]
	v_mfma_i32_16x16x64_i8 v[42:45], v[158:161], v[178:181], v[42:45]
	v_mfma_i32_16x16x64_i8 v[30:33], v[150:153], v[186:189], v[30:33]
	v_mfma_i32_16x16x64_i8 v[26:29], v[158:161], v[186:189], v[26:29]
	v_mfma_i32_16x16x64_i8 v[14:17], v[150:153], v[194:197], v[14:17]
	v_mfma_i32_16x16x64_i8 v[10:13], v[158:161], v[194:197], v[10:13]
	s_barrier
	s_add_u32 s40, s40, 0x40080
	s_addc_u32 s41, s41, 0
	s_add_i32 s42, s42, s3
	v_lshl_add_u64 v[146:147], s[40:41], 0, v[98:99]
	s_mov_b32 m0, s42
	s_nop 0
	global_load_lds_dwordx4 v[146:147], off
	v_lshl_add_u64 v[146:147], s[40:41], 0, v[136:137]
	s_add_i32 m0, s42, 0x2000
	s_nop 0
	global_load_lds_dwordx4 v[146:147], off
	s_waitcnt vmcnt(6)
	s_barrier
	v_mfma_i32_16x16x64_i8 v[54:57], v[198:201], v[164:167], v[54:57]
	v_mfma_i32_16x16x64_i8 v[50:53], v[206:209], v[164:167], v[50:53]
	v_mfma_i32_16x16x64_i8 v[38:41], v[198:201], v[174:177], v[38:41]
	v_mfma_i32_16x16x64_i8 v[34:37], v[206:209], v[174:177], v[34:37]
	v_mfma_i32_16x16x64_i8 v[22:25], v[198:201], v[182:185], v[22:25]
	v_mfma_i32_16x16x64_i8 v[18:21], v[206:209], v[182:185], v[18:21]
	v_mfma_i32_16x16x64_i8 v[6:9], v[198:201], v[190:193], v[6:9]
	v_mfma_i32_16x16x64_i8 v[2:5], v[206:209], v[190:193], v[2:5]
	v_mfma_i32_16x16x64_i8 v[54:57], v[202:205], v[170:173], v[54:57]
	v_mfma_i32_16x16x64_i8 v[50:53], v[210:213], v[170:173], v[50:53]
	v_mfma_i32_16x16x64_i8 v[38:41], v[202:205], v[178:181], v[38:41]
	v_mfma_i32_16x16x64_i8 v[34:37], v[210:213], v[178:181], v[34:37]
	v_mfma_i32_16x16x64_i8 v[22:25], v[202:205], v[186:189], v[22:25]
	v_mfma_i32_16x16x64_i8 v[18:21], v[210:213], v[186:189], v[18:21]
	v_mfma_i32_16x16x64_i8 v[6:9], v[202:205], v[194:197], v[6:9]
	v_mfma_i32_16x16x64_i8 v[2:5], v[210:213], v[194:197], v[2:5]
	s_add_i32 s45, s45, 2
	s_add_u32 s38, s38, 0x100
	s_addc_u32 s39, s39, 0
	s_add_u32 s37, s37, 0x100
	s_addc_u32 s44, s44, 0
	s_cmp_gt_u32 s45, 13
	s_barrier
	s_cbranch_scc0 .LBB0_2088
	v_lshl_add_u32 v146, s36, 8, v1
	v_ashrrev_i32_e32 v147, 31, v146
	s_lshl_b32 s36, s34, 8
	v_lshl_add_u64 v[148:149], v[146:147], 2, s[54:55]
	s_ashr_i32 s37, s36, 31
	global_load_dword v182, v[148:149], off
	global_load_dword v180, v[148:149], off offset:64
	global_load_dword v174, v[148:149], off offset:128
	global_load_dword v172, v[148:149], off offset:192
	global_load_dword v170, v[148:149], off offset:512
	global_load_dword v168, v[148:149], off offset:576
	global_load_dword v162, v[148:149], off offset:640
	global_load_dword v144, v[148:149], off offset:704
	v_lshl_add_u64 v[148:149], s[36:37], 2, v[138:139]
	global_load_dwordx4 v[176:179], v[148:149], off offset:16
	global_load_dwordx4 v[150:153], v[148:149], off
	global_load_dwordx4 v[184:187], v[148:149], off offset:528
	global_load_dwordx4 v[154:157], v[148:149], off offset:512
	v_lshl_or_b32 v148, s34, 7, v163
	v_readlane_b32 s34, v252, 59
	v_readlane_b32 s35, v252, 60
	s_movk_i32 s8, 0x2c00
	v_cvt_f32_i32_e32 v129, v129
	v_cvt_f32_i32_e32 v121, v121
	v_ashrrev_i32_e32 v149, 31, v148
	s_waitcnt vmcnt(0)
	v_mov_b32_e32 v159, v150
	v_mov_b32_e32 v150, v155
	v_pk_mul_f32 v[164:165], v[150:151], s[58:59] op_sel_hi:[1,0]
	v_mov_b32_e32 v150, v156
	v_mov_b32_e32 v151, v152
	v_pk_mul_f32 v[160:161], v[150:151], s[58:59] op_sel_hi:[1,0]
	v_mov_b32_e32 v151, v176
	v_mov_b32_e32 v176, v185
	v_mov_b32_e32 v158, v154
	v_pk_mul_f32 v[154:155], v[176:177], s[58:59] op_sel_hi:[1,0]
	v_mov_b64_e32 v[176:177], s[34:35]
	v_mov_b32_e32 v150, v184
	v_mad_i64_i32 v[184:185], s[34:35], v146, s8, v[176:177]
	v_cvt_f32_i32_e32 v177, v128
	v_cvt_f32_i32_e32 v176, v124
	v_pk_mul_f32 v[166:167], v[158:159], s[58:59] op_sel_hi:[1,0]
	v_mov_b32_e32 v152, v157
	v_pk_mul_f32 v[156:157], v[150:151], s[58:59] op_sel_hi:[1,0]
	v_mov_b32_e32 v150, v186
	v_mov_b32_e32 v151, v178
	v_mov_b32_e32 v178, v187
	v_pk_mul_f32 v[158:159], v[152:153], s[58:59] op_sel_hi:[1,0]
	v_pk_mul_f32 v[152:153], v[150:151], s[58:59] op_sel_hi:[1,0]
	v_pk_mul_f32 v[150:151], v[178:179], s[58:59] op_sel_hi:[1,0]
	v_pk_mul_f32 v[178:179], v[182:183], v[166:167] op_sel_hi:[0,1]
	v_pk_mul_f32 v[176:177], v[178:179], v[176:177]
	v_cvt_f32_i32_e32 v128, v125
	v_mul_f32_e32 v124, 0xbfb8aa3b, v177
	v_exp_f32_e32 v124, v124
	s_nop 0
	v_add_f32_e32 v124, 1.0, v124
	v_rcp_f32_e32 v124, v124
	s_nop 0
	v_mul_f32_e32 v124, v177, v124
	v_mul_f32_e32 v124, v176, v124
	v_pk_mul_f32 v[176:177], v[182:183], v[164:165] op_sel_hi:[0,1]
	v_pk_mul_f32 v[128:129], v[176:177], v[128:129]
	v_pk_mul_f32 v[176:177], v[182:183], v[160:161] op_sel_hi:[0,1]
	v_mul_f32_e32 v125, 0xbfb8aa3b, v129
	v_exp_f32_e32 v125, v125
	s_nop 0
	v_add_f32_e32 v125, 1.0, v125
	v_rcp_f32_e32 v125, v125
	s_nop 0
	v_mul_f32_e32 v125, v129, v125
	v_mul_f32_e32 v125, v128, v125
	v_cvt_f32_i32_e32 v129, v130
	v_cvt_f32_i32_e32 v128, v126
	v_pk_mul_f32 v[128:129], v[176:177], v[128:129]
	s_nop 0
	v_mul_f32_e32 v126, 0xbfb8aa3b, v129
	v_exp_f32_e32 v126, v126
	s_nop 0
	v_add_f32_e32 v126, 1.0, v126
	v_rcp_f32_e32 v126, v126
	s_nop 0
	v_mul_f32_e32 v126, v129, v126
	v_mul_f32_e32 v126, v128, v126
	v_cvt_f32_i32_e32 v129, v131
	v_cvt_f32_i32_e32 v128, v127
	v_pk_mul_f32 v[130:131], v[182:183], v[158:159] op_sel_hi:[0,1]
	v_pk_mul_f32 v[128:129], v[130:131], v[128:129]
	s_nop 0
	v_mul_f32_e32 v127, 0xbfb8aa3b, v129
	v_exp_f32_e32 v127, v127
	v_pk_mul_f32 v[130:131], v[182:183], v[156:157] op_sel_hi:[0,1]
	v_add_f32_e32 v127, 1.0, v127
	v_rcp_f32_e32 v127, v127
	s_nop 0
	v_mul_f32_e32 v127, v129, v127
	v_mul_f32_e32 v127, v128, v127
	v_cvt_f32_i32_e32 v129, v120
	v_cvt_f32_i32_e32 v128, v116
	v_cvt_f32_i32_e32 v120, v117
	v_pk_mul_f32 v[128:129], v[130:131], v[128:129]
	s_nop 0
	v_mul_f32_e32 v116, 0xbfb8aa3b, v129
	v_exp_f32_e32 v116, v116
	s_nop 0
	v_add_f32_e32 v116, 1.0, v116
	v_rcp_f32_e32 v116, v116
	s_nop 0
	v_mul_f32_e32 v116, v129, v116
	v_mul_f32_e32 v128, v128, v116
	v_pk_mul_f32 v[116:117], v[182:183], v[154:155] op_sel_hi:[0,1]
	v_pk_mul_f32 v[116:117], v[116:117], v[120:121]
	s_nop 0
	v_mul_f32_e32 v120, 0xbfb8aa3b, v117
	v_exp_f32_e32 v120, v120
	s_nop 0
	v_add_f32_e32 v120, 1.0, v120
	v_rcp_f32_e32 v120, v120
	s_nop 0
	v_mul_f32_e32 v117, v117, v120
	v_mul_f32_e32 v129, v116, v117
	v_cvt_f32_i32_e32 v117, v122
	v_cvt_f32_i32_e32 v116, v118
	v_pk_mul_f32 v[120:121], v[182:183], v[152:153] op_sel_hi:[0,1]
	v_pk_mul_f32 v[116:117], v[120:121], v[116:117]
	s_nop 0
	v_mul_f32_e32 v118, 0xbfb8aa3b, v117
	v_exp_f32_e32 v118, v118
	v_lshl_add_u64 v[120:121], v[148:149], 1, v[184:185]
	v_add_f32_e32 v118, 1.0, v118
	v_rcp_f32_e32 v118, v118
	s_nop 0
	v_mul_f32_e32 v117, v117, v118
	v_mul_f32_e32 v122, v116, v117
	v_cvt_f32_i32_e32 v117, v123
	v_cvt_f32_i32_e32 v116, v119
	v_pk_mul_f32 v[118:119], v[182:183], v[150:151] op_sel_hi:[0,1]
	v_pk_mul_f32 v[116:117], v[118:119], v[116:117]
	s_nop 0
	v_mul_f32_e32 v118, 0xbfb8aa3b, v117
	v_exp_f32_e32 v118, v118
	s_nop 0
	v_add_f32_e32 v118, 1.0, v118
	v_rcp_f32_e32 v118, v118
	s_nop 0
	v_mul_f32_e32 v117, v117, v118
	v_mul_f32_e32 v123, v116, v117
	v_cvt_pk_bf16_f32 v116, v124, v125
	v_cvt_pk_bf16_f32 v117, v126, v127
	v_cvt_pk_bf16_f32 v118, v128, v129
	v_cvt_pk_bf16_f32 v119, v122, v123
	global_store_dwordx4 v[120:121], v[116:119], off
	s_nop 1
	v_max_f32_e64 v118, |v122|, |v123|
	v_max_f32_e64 v116, |v124|, |v125|
	v_max_f32_e64 v117, |v126|, |v127|
	v_max3_f32 v118, |v128|, |v129|, v118
	v_max3_f32 v116, v116, v117, v118
	v_mov_b32_e32 v117, v0
	s_nop 0
	v_lshlrev_b32_e32 v117, 2, v117
	v_bitop3_b32 v118, v117, 64, v220 bitop3:0x6c
	ds_bpermute_b32 v118, v118, v116
	v_bitop3_b32 v117, v117, s59, v220 bitop3:0x6c
	s_waitcnt lgkmcnt(0)
	v_max_f32_e32 v118, v118, v118
	v_max_f32_e32 v116, v116, v118
	ds_bpermute_b32 v117, v117, v116
	s_and_saveexec_b64 s[34:35], s[0:1]
	s_cbranch_execz .LBB0_2091
	v_readlane_b32 s36, v253, 57
	s_waitcnt lgkmcnt(0)
	v_max_f32_e32 v117, v117, v117
	v_max_f32_e32 v116, v116, v116
	v_readlane_b32 s37, v253, 58
	v_max_f32_e32 v118, v116, v117
	s_nop 0
	v_lshl_add_u64 v[116:117], v[146:147], 2, s[36:37]
	global_atomic_umax v[116:117], v118, off

.LBB0_2238:
	s_add_i32 s46, s30, 2
	s_add_u32 s28, s26, 0x100
	s_addc_u32 s29, s27, 0
	s_add_i32 s47, 0, 0x10000
	v_add_u32_e32 v142, s47, v1
	ds_read_b128 v[144:147], v142
	ds_read_b128 v[148:151], v142 offset:1024
	ds_read_b128 v[152:155], v142 offset:2048
	ds_read_b128 v[156:159], v142 offset:3072
	s_cmp_eq_u32 s19, s30
	s_cselect_b32 s30, s0, s33
	s_cselect_b32 s35, s25, s29
	s_cselect_b32 s34, s24, s28
	s_cselect_b32 s31, s1, s45
	v_lshl_add_u64 v[192:193], s[26:27], 0, v[138:139]
	s_add_i32 m0, s20, 0xc000
	ds_read_b128 v[160:163], v143
	ds_read_b128 v[164:167], v143 offset:1024
	ds_read_b128 v[168:171], v143 offset:2048
	ds_read_b128 v[172:175], v143 offset:3072
	ds_read_b128 v[176:179], v143 offset:4096
	ds_read_b128 v[180:183], v143 offset:5120
	ds_read_b128 v[184:187], v143 offset:6144
	ds_read_b128 v[188:191], v143 offset:7168
	global_load_lds_dwordx4 v[192:193], off
	v_lshl_add_u64 v[192:193], s[26:27], 0, v[140:141]
	s_add_i32 m0, s20, 0xe000
	s_nop 0
	global_load_lds_dwordx4 v[192:193], off
	s_waitcnt lgkmcnt(8)
	s_barrier
	s_waitcnt lgkmcnt(0)
	s_waitcnt lgkmcnt(0)
	v_mfma_i32_16x16x64_i8 v[128:131], v[144:147], v[160:163], v[128:131]
	v_mfma_i32_16x16x64_i8 v[124:127], v[152:155], v[160:163], v[124:127]
	v_mfma_i32_16x16x64_i8 v[120:123], v[144:147], v[168:171], v[120:123]
	v_mfma_i32_16x16x64_i8 v[116:119], v[152:155], v[168:171], v[116:119]
	v_mfma_i32_16x16x64_i8 v[112:115], v[144:147], v[176:179], v[112:115]
	v_mfma_i32_16x16x64_i8 v[108:111], v[152:155], v[176:179], v[108:111]
	v_mfma_i32_16x16x64_i8 v[104:107], v[144:147], v[184:187], v[104:107]
	v_mfma_i32_16x16x64_i8 v[100:103], v[152:155], v[184:187], v[100:103]
	v_mfma_i32_16x16x64_i8 v[128:131], v[148:151], v[164:167], v[128:131]
	v_mfma_i32_16x16x64_i8 v[124:127], v[156:159], v[164:167], v[124:127]
	v_mfma_i32_16x16x64_i8 v[120:123], v[148:151], v[172:175], v[120:123]
	v_mfma_i32_16x16x64_i8 v[116:119], v[156:159], v[172:175], v[116:119]
	v_mfma_i32_16x16x64_i8 v[112:115], v[148:151], v[180:183], v[112:115]
	v_mfma_i32_16x16x64_i8 v[108:111], v[156:159], v[180:183], v[108:111]
	v_mfma_i32_16x16x64_i8 v[104:107], v[148:151], v[188:191], v[104:107]
	v_mfma_i32_16x16x64_i8 v[100:103], v[156:159], v[188:191], v[100:103]
	s_barrier
	s_add_i32 s48, 0, 0x14000
	s_add_i32 s26, s47, s5
	v_add_u32_e32 v142, s48, v1
	v_lshl_add_u64 v[208:209], s[30:31], 0, v[98:99]
	s_mov_b32 m0, s26
	ds_read_b128 v[192:195], v142
	ds_read_b128 v[196:199], v142 offset:1024
	ds_read_b128 v[200:203], v142 offset:2048
	ds_read_b128 v[204:207], v142 offset:3072
	global_load_lds_dwordx4 v[208:209], off
	v_lshl_add_u64 v[210:211], s[30:31], 0, v[132:133]
	s_add_i32 m0, s26, 0x2000
	s_nop 0
	global_load_lds_dwordx4 v[210:211], off
	s_barrier
	s_waitcnt lgkmcnt(0)
	s_waitcnt lgkmcnt(0)
	v_mfma_i32_16x16x64_i8 v[94:97], v[192:195], v[160:163], v[94:97]
	v_mfma_i32_16x16x64_i8 v[90:93], v[200:203], v[160:163], v[90:93]
	v_mfma_i32_16x16x64_i8 v[86:89], v[192:195], v[168:171], v[86:89]
	v_mfma_i32_16x16x64_i8 v[82:85], v[200:203], v[168:171], v[82:85]
	v_mfma_i32_16x16x64_i8 v[78:81], v[192:195], v[176:179], v[78:81]
	v_mfma_i32_16x16x64_i8 v[74:77], v[200:203], v[176:179], v[74:77]
	v_mfma_i32_16x16x64_i8 v[70:73], v[192:195], v[184:187], v[70:73]
	v_mfma_i32_16x16x64_i8 v[66:69], v[200:203], v[184:187], v[66:69]
	v_mfma_i32_16x16x64_i8 v[94:97], v[196:199], v[164:167], v[94:97]
	v_mfma_i32_16x16x64_i8 v[90:93], v[204:207], v[164:167], v[90:93]
	v_mfma_i32_16x16x64_i8 v[86:89], v[196:199], v[172:175], v[86:89]
	v_mfma_i32_16x16x64_i8 v[82:85], v[204:207], v[172:175], v[82:85]
	v_mfma_i32_16x16x64_i8 v[78:81], v[196:199], v[180:183], v[78:81]
	v_mfma_i32_16x16x64_i8 v[74:77], v[204:207], v[180:183], v[74:77]
	v_mfma_i32_16x16x64_i8 v[70:73], v[196:199], v[188:191], v[70:73]
	v_mfma_i32_16x16x64_i8 v[66:69], v[204:207], v[188:191], v[66:69]
	s_mov_b32 m0, s20
	v_lshl_add_u64 v[212:213], s[34:35], 0, v[98:99]
	s_barrier
	ds_read_b128 v[160:163], v143 offset:16384
	ds_read_b128 v[164:167], v143 offset:17408
	ds_read_b128 v[168:171], v143 offset:18432
	ds_read_b128 v[172:175], v143 offset:19456
	ds_read_b128 v[176:179], v143 offset:20480
	ds_read_b128 v[180:183], v143 offset:21504
	ds_read_b128 v[184:187], v143 offset:22528
	ds_read_b128 v[188:191], v143 offset:23552
	global_load_lds_dwordx4 v[212:213], off
	v_lshl_add_u64 v[214:215], s[34:35], 0, v[132:133]
	s_mov_b32 m0, s21
	s_nop 0
	global_load_lds_dwordx4 v[214:215], off
	s_barrier
	s_waitcnt lgkmcnt(0)
	s_waitcnt lgkmcnt(0)
	v_mfma_i32_16x16x64_i8 v[62:65], v[144:147], v[160:163], v[62:65]
	v_mfma_i32_16x16x64_i8 v[58:61], v[152:155], v[160:163], v[58:61]
	v_mfma_i32_16x16x64_i8 v[54:57], v[144:147], v[168:171], v[54:57]
	v_mfma_i32_16x16x64_i8 v[50:53], v[152:155], v[168:171], v[50:53]
	v_mfma_i32_16x16x64_i8 v[46:49], v[144:147], v[176:179], v[46:49]
	v_mfma_i32_16x16x64_i8 v[42:45], v[152:155], v[176:179], v[42:45]
	v_mfma_i32_16x16x64_i8 v[38:41], v[144:147], v[184:187], v[38:41]
	v_mfma_i32_16x16x64_i8 v[34:37], v[152:155], v[184:187], v[34:37]
	v_mfma_i32_16x16x64_i8 v[62:65], v[148:151], v[164:167], v[62:65]
	v_mfma_i32_16x16x64_i8 v[58:61], v[156:159], v[164:167], v[58:61]
	v_mfma_i32_16x16x64_i8 v[54:57], v[148:151], v[172:175], v[54:57]
	v_mfma_i32_16x16x64_i8 v[50:53], v[156:159], v[172:175], v[50:53]
	v_mfma_i32_16x16x64_i8 v[46:49], v[148:151], v[180:183], v[46:49]
	v_mfma_i32_16x16x64_i8 v[42:45], v[156:159], v[180:183], v[42:45]
	v_mfma_i32_16x16x64_i8 v[38:41], v[148:151], v[188:191], v[38:41]
	v_mfma_i32_16x16x64_i8 v[34:37], v[156:159], v[188:191], v[34:37]
	s_barrier
	s_add_u32 s26, s30, 0xb0000
	s_addc_u32 s27, s31, 0
	s_add_i32 s47, s48, s5
	v_lshl_add_u64 v[144:145], s[26:27], 0, v[98:99]
	s_mov_b32 m0, s47
	s_nop 0
	global_load_lds_dwordx4 v[144:145], off
	v_lshl_add_u64 v[144:145], s[26:27], 0, v[132:133]
	s_add_i32 m0, s47, 0x2000
	s_nop 0
	global_load_lds_dwordx4 v[144:145], off
	s_waitcnt vmcnt(6)
	s_barrier
	v_mfma_i32_16x16x64_i8 v[30:33], v[192:195], v[160:163], v[30:33]
	v_mfma_i32_16x16x64_i8 v[26:29], v[200:203], v[160:163], v[26:29]
	v_mfma_i32_16x16x64_i8 v[22:25], v[192:195], v[168:171], v[22:25]
	v_mfma_i32_16x16x64_i8 v[18:21], v[200:203], v[168:171], v[18:21]
	v_mfma_i32_16x16x64_i8 v[14:17], v[192:195], v[176:179], v[14:17]
	v_mfma_i32_16x16x64_i8 v[10:13], v[200:203], v[176:179], v[10:13]
	v_mfma_i32_16x16x64_i8 v[6:9], v[192:195], v[184:187], v[6:9]
	v_mfma_i32_16x16x64_i8 v[2:5], v[200:203], v[184:187], v[2:5]
	v_mfma_i32_16x16x64_i8 v[30:33], v[196:199], v[164:167], v[30:33]
	v_mfma_i32_16x16x64_i8 v[26:29], v[204:207], v[164:167], v[26:29]
	v_mfma_i32_16x16x64_i8 v[22:25], v[196:199], v[172:175], v[22:25]
	v_mfma_i32_16x16x64_i8 v[18:21], v[204:207], v[172:175], v[18:21]
	v_mfma_i32_16x16x64_i8 v[14:17], v[196:199], v[180:183], v[14:17]
	v_mfma_i32_16x16x64_i8 v[10:13], v[204:207], v[180:183], v[10:13]
	v_mfma_i32_16x16x64_i8 v[6:9], v[196:199], v[188:191], v[6:9]
	v_mfma_i32_16x16x64_i8 v[2:5], v[204:207], v[188:191], v[2:5]
	s_add_i32 s47, 0, 0x18000
	v_add_u32_e32 v142, s47, v1
	s_barrier
	ds_read_b128 v[144:147], v142
	ds_read_b128 v[148:151], v142 offset:1024
	ds_read_b128 v[152:155], v142 offset:2048
	ds_read_b128 v[156:159], v142 offset:3072
	s_add_u32 s26, s34, 0xb0000
	s_addc_u32 s27, s35, 0
	s_mov_b32 m0, s36
	v_lshl_add_u64 v[192:193], s[26:27], 0, v[98:99]
	ds_read_b128 v[160:163], v143 offset:32768
	ds_read_b128 v[164:167], v143 offset:33792
	ds_read_b128 v[168:171], v143 offset:34816
	ds_read_b128 v[172:175], v143 offset:35840
	ds_read_b128 v[176:179], v143 offset:36864
	ds_read_b128 v[180:183], v143 offset:37888
	ds_read_b128 v[184:187], v143 offset:38912
	ds_read_b128 v[188:191], v143 offset:39936
	global_load_lds_dwordx4 v[192:193], off
	v_lshl_add_u64 v[192:193], s[26:27], 0, v[132:133]
	s_mov_b32 m0, s37
	s_nop 0
	global_load_lds_dwordx4 v[192:193], off
	s_waitcnt lgkmcnt(8)
	s_barrier
	s_waitcnt lgkmcnt(0)
	s_waitcnt lgkmcnt(0)
	v_mfma_i32_16x16x64_i8 v[128:131], v[144:147], v[160:163], v[128:131]
	v_mfma_i32_16x16x64_i8 v[124:127], v[152:155], v[160:163], v[124:127]
	v_mfma_i32_16x16x64_i8 v[120:123], v[144:147], v[168:171], v[120:123]
	v_mfma_i32_16x16x64_i8 v[116:119], v[152:155], v[168:171], v[116:119]
	v_mfma_i32_16x16x64_i8 v[112:115], v[144:147], v[176:179], v[112:115]
	v_mfma_i32_16x16x64_i8 v[108:111], v[152:155], v[176:179], v[108:111]
	v_mfma_i32_16x16x64_i8 v[104:107], v[144:147], v[184:187], v[104:107]
	v_mfma_i32_16x16x64_i8 v[100:103], v[152:155], v[184:187], v[100:103]
	v_mfma_i32_16x16x64_i8 v[128:131], v[148:151], v[164:167], v[128:131]
	v_mfma_i32_16x16x64_i8 v[124:127], v[156:159], v[164:167], v[124:127]
	v_mfma_i32_16x16x64_i8 v[120:123], v[148:151], v[172:175], v[120:123]
	v_mfma_i32_16x16x64_i8 v[116:119], v[156:159], v[172:175], v[116:119]
	v_mfma_i32_16x16x64_i8 v[112:115], v[148:151], v[180:183], v[112:115]
	v_mfma_i32_16x16x64_i8 v[108:111], v[156:159], v[180:183], v[108:111]
	v_mfma_i32_16x16x64_i8 v[104:107], v[148:151], v[188:191], v[104:107]
	v_mfma_i32_16x16x64_i8 v[100:103], v[156:159], v[188:191], v[100:103]
	s_barrier
	s_add_i32 s34, 0, 0x1c000
	s_add_i32 s26, s47, s5
	v_add_u32_e32 v142, s34, v1
	v_lshl_add_u64 v[208:209], v[208:209], 0, s[68:69]
	s_mov_b32 m0, s26
	ds_read_b128 v[192:195], v142
	ds_read_b128 v[196:199], v142 offset:1024
	ds_read_b128 v[200:203], v142 offset:2048
	ds_read_b128 v[204:207], v142 offset:3072
	global_load_lds_dwordx4 v[208:209], off
	v_lshl_add_u64 v[208:209], v[210:211], 0, s[68:69]
	s_add_i32 m0, s26, 0x2000
	s_nop 0
	global_load_lds_dwordx4 v[208:209], off
	s_barrier
	s_waitcnt lgkmcnt(0)
	s_waitcnt lgkmcnt(0)
	v_mfma_i32_16x16x64_i8 v[94:97], v[192:195], v[160:163], v[94:97]
	v_mfma_i32_16x16x64_i8 v[90:93], v[200:203], v[160:163], v[90:93]
	v_mfma_i32_16x16x64_i8 v[86:89], v[192:195], v[168:171], v[86:89]
	v_mfma_i32_16x16x64_i8 v[82:85], v[200:203], v[168:171], v[82:85]
	v_mfma_i32_16x16x64_i8 v[78:81], v[192:195], v[176:179], v[78:81]
	v_mfma_i32_16x16x64_i8 v[74:77], v[200:203], v[176:179], v[74:77]
	v_mfma_i32_16x16x64_i8 v[70:73], v[192:195], v[184:187], v[70:73]
	v_mfma_i32_16x16x64_i8 v[66:69], v[200:203], v[184:187], v[66:69]
	v_mfma_i32_16x16x64_i8 v[94:97], v[196:199], v[164:167], v[94:97]
	v_mfma_i32_16x16x64_i8 v[90:93], v[204:207], v[164:167], v[90:93]
	v_mfma_i32_16x16x64_i8 v[86:89], v[196:199], v[172:175], v[86:89]
	v_mfma_i32_16x16x64_i8 v[82:85], v[204:207], v[172:175], v[82:85]
	v_mfma_i32_16x16x64_i8 v[78:81], v[196:199], v[180:183], v[78:81]
	v_mfma_i32_16x16x64_i8 v[74:77], v[204:207], v[180:183], v[74:77]
	v_mfma_i32_16x16x64_i8 v[70:73], v[196:199], v[188:191], v[70:73]
	v_mfma_i32_16x16x64_i8 v[66:69], v[204:207], v[188:191], v[66:69]
	s_mov_b32 m0, s38
	v_lshl_add_u64 v[208:209], v[212:213], 0, s[68:69]
	s_barrier
	ds_read_b128 v[160:163], v143 offset:49152
	ds_read_b128 v[164:167], v143 offset:50176
	ds_read_b128 v[168:171], v143 offset:51200
	ds_read_b128 v[172:175], v143 offset:52224
	ds_read_b128 v[176:179], v143 offset:53248
	ds_read_b128 v[180:183], v143 offset:54272
	ds_read_b128 v[184:187], v143 offset:55296
	ds_read_b128 v[188:191], v143 offset:56320
	global_load_lds_dwordx4 v[208:209], off
	v_lshl_add_u64 v[208:209], v[214:215], 0, s[68:69]
	s_mov_b32 m0, s39
	s_nop 0
	global_load_lds_dwordx4 v[208:209], off
	s_barrier
	s_waitcnt lgkmcnt(0)
	s_waitcnt lgkmcnt(0)
	v_mfma_i32_16x16x64_i8 v[62:65], v[144:147], v[160:163], v[62:65]
	v_mfma_i32_16x16x64_i8 v[58:61], v[152:155], v[160:163], v[58:61]
	v_mfma_i32_16x16x64_i8 v[54:57], v[144:147], v[168:171], v[54:57]
	v_mfma_i32_16x16x64_i8 v[50:53], v[152:155], v[168:171], v[50:53]
	v_mfma_i32_16x16x64_i8 v[46:49], v[144:147], v[176:179], v[46:49]
	v_mfma_i32_16x16x64_i8 v[42:45], v[152:155], v[176:179], v[42:45]
	v_mfma_i32_16x16x64_i8 v[38:41], v[144:147], v[184:187], v[38:41]
	v_mfma_i32_16x16x64_i8 v[34:37], v[152:155], v[184:187], v[34:37]
	v_mfma_i32_16x16x64_i8 v[62:65], v[148:151], v[164:167], v[62:65]
	v_mfma_i32_16x16x64_i8 v[58:61], v[156:159], v[164:167], v[58:61]
	v_mfma_i32_16x16x64_i8 v[54:57], v[148:151], v[172:175], v[54:57]
	v_mfma_i32_16x16x64_i8 v[50:53], v[156:159], v[172:175], v[50:53]
	v_mfma_i32_16x16x64_i8 v[46:49], v[148:151], v[180:183], v[46:49]
	v_mfma_i32_16x16x64_i8 v[42:45], v[156:159], v[180:183], v[42:45]
	v_mfma_i32_16x16x64_i8 v[38:41], v[148:151], v[188:191], v[38:41]
	v_mfma_i32_16x16x64_i8 v[34:37], v[156:159], v[188:191], v[34:37]
	s_barrier
	s_add_u32 s26, s30, 0xb0080
	s_addc_u32 s27, s31, 0
	s_add_i32 s30, s34, s5
	v_lshl_add_u64 v[144:145], s[26:27], 0, v[98:99]
	s_mov_b32 m0, s30
	s_nop 0
	global_load_lds_dwordx4 v[144:145], off
	v_lshl_add_u64 v[144:145], s[26:27], 0, v[132:133]
	s_add_i32 m0, s30, 0x2000
	s_nop 0
	global_load_lds_dwordx4 v[144:145], off
	s_waitcnt vmcnt(6)
	s_barrier
	v_mfma_i32_16x16x64_i8 v[30:33], v[192:195], v[160:163], v[30:33]
	v_mfma_i32_16x16x64_i8 v[26:29], v[200:203], v[160:163], v[26:29]
	v_mfma_i32_16x16x64_i8 v[22:25], v[192:195], v[168:171], v[22:25]
	v_mfma_i32_16x16x64_i8 v[18:21], v[200:203], v[168:171], v[18:21]
	v_mfma_i32_16x16x64_i8 v[14:17], v[192:195], v[176:179], v[14:17]
	v_mfma_i32_16x16x64_i8 v[10:13], v[200:203], v[176:179], v[10:13]
	v_mfma_i32_16x16x64_i8 v[6:9], v[192:195], v[184:187], v[6:9]
	v_mfma_i32_16x16x64_i8 v[2:5], v[200:203], v[184:187], v[2:5]
	v_mfma_i32_16x16x64_i8 v[30:33], v[196:199], v[164:167], v[30:33]
	v_mfma_i32_16x16x64_i8 v[26:29], v[204:207], v[164:167], v[26:29]
	v_mfma_i32_16x16x64_i8 v[22:25], v[196:199], v[172:175], v[22:25]
	v_mfma_i32_16x16x64_i8 v[18:21], v[204:207], v[172:175], v[18:21]
	v_mfma_i32_16x16x64_i8 v[14:17], v[196:199], v[180:183], v[14:17]
	v_mfma_i32_16x16x64_i8 v[10:13], v[204:207], v[180:183], v[10:13]
	v_mfma_i32_16x16x64_i8 v[6:9], v[196:199], v[188:191], v[6:9]
	v_mfma_i32_16x16x64_i8 v[2:5], v[204:207], v[188:191], v[2:5]
	s_add_u32 s33, s33, 0x100
	s_addc_u32 s45, s45, 0
	s_cmp_ge_i32 s46, s8
	s_mov_b64 s[26:27], s[28:29]
	s_mov_b32 s30, s46
	s_barrier
	s_cbranch_scc0 .LBB0_2238
	v_lshl_add_u32 v190, s9, 8, v134
	v_readlane_b32 s8, v253, 57
	v_ashrrev_i32_e32 v191, 31, v190
	v_readlane_b32 s9, v253, 58
	v_lshl_or_b32 v192, s3, 8, v135
	v_ashrrev_i32_e32 v193, 31, v192
	v_lshl_add_u64 v[158:159], v[190:191], 2, s[8:9]
	v_readlane_b32 s8, v254, 30
	v_readlane_b32 s9, v254, 31
	v_cvt_f32_i32_e32 v161, v129
	v_cvt_f32_i32_e32 v160, v128
	v_cvt_f32_i32_e32 v129, v127
	v_cvt_f32_i32_e32 v128, v126
	v_cvt_f32_i32_e32 v127, v87
	v_cvt_f32_i32_e32 v126, v86
	v_cvt_f32_i32_e32 v87, v77
	v_cvt_f32_i32_e32 v86, v76
	v_cvt_f32_i32_e32 v77, v31
	v_cvt_f32_i32_e32 v76, v30
	v_cvt_f32_i32_e32 v31, v21
	v_cvt_f32_i32_e32 v30, v20
	v_cvt_f32_i32_e32 v21, v7
	v_cvt_f32_i32_e32 v20, v6
	v_lshl_add_u64 v[6:7], v[192:193], 2, s[8:9]
	global_load_dword v156, v[158:159], off
	global_load_dword v154, v[158:159], off offset:64
	global_load_dword v152, v[158:159], off offset:128
	global_load_dword v150, v[158:159], off offset:192
	global_load_dword v148, v[158:159], off offset:512
	global_load_dword v146, v[158:159], off offset:576
	global_load_dword v144, v[158:159], off offset:640
	global_load_dword v142, v[158:159], off offset:704
	v_cvt_f32_i32_e32 v163, v93
	v_cvt_f32_i32_e32 v162, v92
	v_cvt_f32_i32_e32 v165, v91
	v_cvt_f32_i32_e32 v164, v90
	v_cvt_f32_i32_e32 v91, v81
	v_cvt_f32_i32_e32 v90, v80
	v_cvt_f32_i32_e32 v93, v79
	v_cvt_f32_i32_e32 v92, v78
	v_cvt_f32_i32_e32 v79, v69
	v_cvt_f32_i32_e32 v78, v68
	v_cvt_f32_i32_e32 v81, v67
	v_cvt_f32_i32_e32 v80, v66
	v_cvt_f32_i32_e32 v67, v29
	v_cvt_f32_i32_e32 v66, v28
	v_cvt_f32_i32_e32 v69, v27
	v_cvt_f32_i32_e32 v68, v26
	v_cvt_f32_i32_e32 v27, v17
	v_cvt_f32_i32_e32 v26, v16
	v_cvt_f32_i32_e32 v29, v15
	v_cvt_f32_i32_e32 v28, v14
	v_cvt_f32_i32_e32 v15, v5
	v_cvt_f32_i32_e32 v14, v4
	v_cvt_f32_i32_e32 v17, v3
	v_cvt_f32_i32_e32 v16, v2
	global_load_dwordx4 v[2:5], v[6:7], off
	v_cvt_f32_i32_e32 v159, v131
	v_cvt_f32_i32_e32 v158, v130
	v_cvt_f32_i32_e32 v131, v125
	v_cvt_f32_i32_e32 v130, v124
	v_cvt_f32_i32_e32 v123, v123
	v_cvt_f32_i32_e32 v122, v122
	v_cvt_f32_i32_e32 v121, v121
	v_cvt_f32_i32_e32 v120, v120
	v_cvt_f32_i32_e32 v119, v119
	v_cvt_f32_i32_e32 v118, v118
	v_cvt_f32_i32_e32 v117, v117
	v_cvt_f32_i32_e32 v116, v116
	v_cvt_f32_i32_e32 v115, v115
	v_cvt_f32_i32_e32 v114, v114
	v_cvt_f32_i32_e32 v113, v113
	v_cvt_f32_i32_e32 v112, v112
	v_cvt_f32_i32_e32 v111, v111
	v_cvt_f32_i32_e32 v110, v110
	v_cvt_f32_i32_e32 v109, v109
	v_cvt_f32_i32_e32 v108, v108
	v_cvt_f32_i32_e32 v107, v107
	v_cvt_f32_i32_e32 v106, v106
	v_cvt_f32_i32_e32 v105, v105
	v_cvt_f32_i32_e32 v104, v104
	v_cvt_f32_i32_e32 v103, v103
	v_cvt_f32_i32_e32 v102, v102
	v_cvt_f32_i32_e32 v101, v101
	v_cvt_f32_i32_e32 v100, v100
	v_cvt_f32_i32_e32 v167, v97
	v_cvt_f32_i32_e32 v166, v96
	v_cvt_f32_i32_e32 v169, v95
	v_cvt_f32_i32_e32 v168, v94
	v_cvt_f32_i32_e32 v125, v89
	v_cvt_f32_i32_e32 v124, v88
	v_cvt_f32_i32_e32 v95, v85
	v_cvt_f32_i32_e32 v94, v84
	v_cvt_f32_i32_e32 v97, v83
	v_cvt_f32_i32_e32 v96, v82
	v_cvt_f32_i32_e32 v89, v75
	v_cvt_f32_i32_e32 v88, v74
	v_cvt_f32_i32_e32 v83, v73
	v_cvt_f32_i32_e32 v82, v72
	v_cvt_f32_i32_e32 v85, v71
	v_cvt_f32_i32_e32 v84, v70
	v_cvt_f32_i32_e32 v71, v65
	v_cvt_f32_i32_e32 v70, v64
	v_cvt_f32_i32_e32 v73, v63
	v_cvt_f32_i32_e32 v72, v62
	v_cvt_f32_i32_e32 v63, v61
	v_cvt_f32_i32_e32 v62, v60
	v_cvt_f32_i32_e32 v65, v59
	v_cvt_f32_i32_e32 v64, v58
	v_cvt_f32_i32_e32 v57, v57
	v_cvt_f32_i32_e32 v56, v56
	v_cvt_f32_i32_e32 v55, v55
	v_cvt_f32_i32_e32 v54, v54
	v_cvt_f32_i32_e32 v53, v53
	v_cvt_f32_i32_e32 v52, v52
	v_cvt_f32_i32_e32 v51, v51
	v_cvt_f32_i32_e32 v50, v50
	v_cvt_f32_i32_e32 v49, v49
	v_cvt_f32_i32_e32 v48, v48
	v_cvt_f32_i32_e32 v47, v47
	v_cvt_f32_i32_e32 v46, v46
	v_cvt_f32_i32_e32 v45, v45
	v_cvt_f32_i32_e32 v44, v44
	v_cvt_f32_i32_e32 v43, v43
	v_cvt_f32_i32_e32 v42, v42
	v_cvt_f32_i32_e32 v41, v41
	v_cvt_f32_i32_e32 v40, v40
	v_cvt_f32_i32_e32 v39, v39
	v_cvt_f32_i32_e32 v38, v38
	v_cvt_f32_i32_e32 v37, v37
	v_cvt_f32_i32_e32 v36, v36
	v_cvt_f32_i32_e32 v35, v35
	v_cvt_f32_i32_e32 v34, v34
	v_cvt_f32_i32_e32 v75, v33
	v_cvt_f32_i32_e32 v74, v32
	v_cvt_f32_i32_e32 v59, v25
	s_waitcnt vmcnt(0)
	v_pk_mul_f32 v[170:171], v[4:5], s[58:59] op_sel_hi:[1,0]
	v_pk_mul_f32 v[172:173], v[2:3], s[58:59] op_sel_hi:[1,0]
	global_load_dwordx4 v[2:5], v[6:7], off offset:64
	v_cvt_f32_i32_e32 v58, v24
	v_cvt_f32_i32_e32 v61, v23
	v_cvt_f32_i32_e32 v60, v22
	v_cvt_f32_i32_e32 v33, v19
	v_cvt_f32_i32_e32 v32, v18
	v_cvt_f32_i32_e32 v23, v13
	v_cvt_f32_i32_e32 v22, v12
	v_cvt_f32_i32_e32 v25, v11
	v_cvt_f32_i32_e32 v24, v10
	v_cvt_f32_i32_e32 v19, v9
	v_cvt_f32_i32_e32 v18, v8
	s_mov_b64 s[26:27], -1
	s_cmp_lt_i32 s62, 0
	s_waitcnt vmcnt(0)
	v_pk_mul_f32 v[174:175], v[4:5], s[58:59] op_sel_hi:[1,0]
	v_pk_mul_f32 v[180:181], v[2:3], s[58:59] op_sel_hi:[1,0]
	global_load_dwordx4 v[2:5], v[6:7], off offset:512
	s_waitcnt vmcnt(0)
	v_pk_mul_f32 v[182:183], v[4:5], s[58:59] op_sel_hi:[1,0]
	v_pk_mul_f32 v[184:185], v[2:3], s[58:59] op_sel_hi:[1,0]
	global_load_dwordx4 v[2:5], v[6:7], off offset:576
	s_waitcnt vmcnt(0)
	v_pk_mul_f32 v[186:187], v[4:5], s[58:59] op_sel_hi:[1,0]
	v_pk_mul_f32 v[188:189], v[2:3], s[58:59] op_sel_hi:[1,0]
	s_cbranch_scc0 .LBB0_2241
	v_readlane_b32 s8, v254, 28
	v_lshlrev_b64 v[2:3], 2, v[192:193]
	v_readlane_b32 s9, v254, 29
	v_pk_mul_f32 v[218:219], v[156:157], v[160:161] op_sel_hi:[0,1]
	v_pk_mul_f32 v[244:245], v[152:153], v[112:113] op_sel_hi:[0,1]
	v_lshl_add_u64 v[8:9], s[8:9], 0, v[2:3]
	global_load_dwordx4 v[4:7], v[8:9], off
	v_readlane_b32 s8, v253, 28
	v_readlane_b32 s9, v253, 29
	s_mov_b32 s3, 0x100000
	s_mov_b64 s[26:27], 0
	v_lshl_add_u64 v[212:213], s[8:9], 0, v[2:3]
	s_mov_b64 s[8:9], 0x100000
	s_waitcnt vmcnt(0)
	v_pk_mul_f32 v[206:207], v[170:171], v[6:7]
	v_pk_mul_f32 v[208:209], v[172:173], v[4:5]
	global_load_dwordx4 v[4:7], v[8:9], off offset:64
	s_waitcnt vmcnt(0)
	v_pk_mul_f32 v[202:203], v[174:175], v[6:7]
	v_pk_mul_f32 v[204:205], v[180:181], v[4:5]
	global_load_dwordx4 v[4:7], v[8:9], off offset:512
	s_waitcnt vmcnt(0)
	v_pk_mul_f32 v[198:199], v[182:183], v[6:7]
	v_pk_mul_f32 v[200:201], v[184:185], v[4:5]
	global_load_dwordx4 v[4:7], v[8:9], off offset:576
	s_waitcnt vmcnt(0)
	v_pk_mul_f32 v[196:197], v[188:189], v[4:5]
	v_add_u32_e32 v4, 0xffffff00, v190
	v_ashrrev_i32_e32 v5, 31, v4
	v_lshlrev_b64 v[4:5], 13, v[4:5]
	v_lshl_add_u64 v[12:13], v[212:213], 0, v[4:5]
	v_pk_mul_f32 v[194:195], v[186:187], v[6:7]
	global_load_dwordx4 v[4:7], v[12:13], off
	global_load_dwordx4 v[8:11], v[12:13], off offset:64
	global_load_dwordx4 v[176:179], v[12:13], off offset:512
	global_load_dwordx4 v[214:217], v[12:13], off offset:576
	v_add_u32_e32 v12, 0xffffff10, v190
	v_ashrrev_i32_e32 v13, 31, v12
	v_lshlrev_b64 v[12:13], 13, v[12:13]
	v_lshl_add_u64 v[12:13], v[212:213], 0, v[12:13]
	global_load_dwordx4 v[222:225], v[12:13], off
	global_load_dwordx4 v[230:233], v[12:13], off offset:64
	global_load_dwordx4 v[236:239], v[12:13], off offset:512
	global_load_dwordx4 v[240:243], v[12:13], off offset:576
	v_lshlrev_b64 v[12:13], 13, v[190:191]
	v_lshl_add_u64 v[12:13], s[76:77], 0, v[12:13]
	v_lshl_add_u64 v[210:211], v[12:13], 0, v[2:3]
	v_pk_mul_f32 v[12:13], v[156:157], v[158:159] op_sel_hi:[0,1]
	s_waitcnt vmcnt(0)
	v_pk_fma_f32 v[6:7], v[12:13], v[206:207], v[6:7]
	v_pk_fma_f32 v[4:5], v[218:219], v[208:209], v[4:5]
	global_store_dwordx4 v[210:211], v[4:7], off
	v_pk_mul_f32 v[12:13], v[156:157], v[130:131] op_sel_hi:[0,1]
	v_pk_mul_f32 v[218:219], v[152:153], v[114:115] op_sel_hi:[0,1]
	v_pk_mul_f32 v[4:5], v[156:157], v[128:129] op_sel_hi:[0,1]
	v_pk_fma_f32 v[6:7], v[4:5], v[202:203], v[10:11]
	v_pk_fma_f32 v[4:5], v[12:13], v[204:205], v[8:9]
	global_store_dwordx4 v[210:211], v[4:7], off offset:64
	v_pk_mul_f32 v[8:9], v[156:157], v[168:169] op_sel_hi:[0,1]
	v_pk_mul_f32 v[10:11], v[154:155], v[120:121] op_sel_hi:[0,1]
	v_pk_mul_f32 v[4:5], v[156:157], v[166:167] op_sel_hi:[0,1]
	v_pk_fma_f32 v[6:7], v[4:5], v[198:199], v[178:179]
	v_pk_fma_f32 v[4:5], v[8:9], v[200:201], v[176:177]
	global_store_dwordx4 v[210:211], v[4:7], off offset:512
	v_pk_mul_f32 v[8:9], v[156:157], v[164:165] op_sel_hi:[0,1]
	s_nop 0
	v_pk_mul_f32 v[4:5], v[156:157], v[162:163] op_sel_hi:[0,1]
	v_pk_fma_f32 v[6:7], v[4:5], v[194:195], v[216:217]
	v_pk_fma_f32 v[4:5], v[8:9], v[196:197], v[214:215]
	global_store_dwordx4 v[210:211], v[4:7], off offset:576
	s_nop 1
	v_or_b32_e32 v4, 16, v190
	v_ashrrev_i32_e32 v5, 31, v4
	v_lshlrev_b64 v[4:5], 13, v[4:5]
	v_lshl_add_u64 v[4:5], s[76:77], 0, v[4:5]
	v_lshl_add_u64 v[8:9], v[4:5], 0, v[2:3]
	v_pk_mul_f32 v[4:5], v[154:155], v[122:123] op_sel_hi:[0,1]
	v_pk_fma_f32 v[6:7], v[4:5], v[206:207], v[224:225]
	v_pk_fma_f32 v[4:5], v[10:11], v[208:209], v[222:223]
	global_store_dwordx4 v[8:9], v[4:7], off
	v_pk_mul_f32 v[10:11], v[154:155], v[116:117] op_sel_hi:[0,1]
	s_nop 0
	v_pk_mul_f32 v[4:5], v[154:155], v[118:119] op_sel_hi:[0,1]
	v_pk_fma_f32 v[6:7], v[4:5], v[202:203], v[232:233]
	v_pk_fma_f32 v[4:5], v[10:11], v[204:205], v[230:231]
	global_store_dwordx4 v[8:9], v[4:7], off offset:64
	v_pk_mul_f32 v[10:11], v[154:155], v[126:127] op_sel_hi:[0,1]
	s_nop 0
	v_pk_mul_f32 v[4:5], v[154:155], v[124:125] op_sel_hi:[0,1]
	v_pk_fma_f32 v[6:7], v[4:5], v[198:199], v[238:239]
	v_pk_fma_f32 v[4:5], v[10:11], v[200:201], v[236:237]
	global_store_dwordx4 v[8:9], v[4:7], off offset:512
	v_pk_mul_f32 v[10:11], v[154:155], v[96:97] op_sel_hi:[0,1]
	s_nop 0
	v_pk_mul_f32 v[4:5], v[154:155], v[94:95] op_sel_hi:[0,1]
	v_pk_fma_f32 v[6:7], v[4:5], v[194:195], v[242:243]
	v_pk_fma_f32 v[4:5], v[10:11], v[196:197], v[240:241]
	global_store_dwordx4 v[8:9], v[4:7], off offset:576
	s_nop 1
	v_add_u32_e32 v4, 0xffffff20, v190
	v_ashrrev_i32_e32 v5, 31, v4
	v_lshlrev_b64 v[4:5], 13, v[4:5]
	v_lshl_add_u64 v[12:13], v[212:213], 0, v[4:5]
	global_load_dwordx4 v[4:7], v[12:13], off
	global_load_dwordx4 v[8:11], v[12:13], off offset:64
	global_load_dwordx4 v[176:179], v[12:13], off offset:512
	global_load_dwordx4 v[214:217], v[12:13], off offset:576
	v_add_u32_e32 v12, 0xffffff30, v190
	v_ashrrev_i32_e32 v13, 31, v12
	v_lshlrev_b64 v[12:13], 13, v[12:13]
	v_lshl_add_u64 v[12:13], v[212:213], 0, v[12:13]
	global_load_dwordx4 v[222:225], v[12:13], off
	global_load_dwordx4 v[230:233], v[12:13], off offset:64
	global_load_dwordx4 v[236:239], v[12:13], off offset:512
	global_load_dwordx4 v[240:243], v[12:13], off offset:576
	v_or_b32_e32 v12, 32, v190
	v_ashrrev_i32_e32 v13, 31, v12
	v_lshlrev_b64 v[12:13], 13, v[12:13]
	v_lshl_add_u64 v[12:13], s[76:77], 0, v[12:13]
	v_lshl_add_u64 v[12:13], v[12:13], 0, v[2:3]
	s_waitcnt vmcnt(0)
	v_pk_fma_f32 v[6:7], v[218:219], v[206:207], v[6:7]
	v_pk_fma_f32 v[4:5], v[244:245], v[208:209], v[4:5]
	global_store_dwordx4 v[12:13], v[4:7], off
	v_pk_mul_f32 v[218:219], v[152:153], v[108:109] op_sel_hi:[0,1]
	s_nop 0
	v_pk_mul_f32 v[4:5], v[152:153], v[110:111] op_sel_hi:[0,1]
	v_pk_fma_f32 v[6:7], v[4:5], v[202:203], v[10:11]
	v_pk_fma_f32 v[4:5], v[218:219], v[204:205], v[8:9]
	global_store_dwordx4 v[12:13], v[4:7], off offset:64
	v_pk_mul_f32 v[8:9], v[152:153], v[92:93] op_sel_hi:[0,1]
	s_nop 0
	v_pk_mul_f32 v[4:5], v[152:153], v[90:91] op_sel_hi:[0,1]
	v_pk_fma_f32 v[6:7], v[4:5], v[198:199], v[178:179]
	v_pk_fma_f32 v[4:5], v[8:9], v[200:201], v[176:177]
	global_store_dwordx4 v[12:13], v[4:7], off offset:512
	v_pk_mul_f32 v[8:9], v[152:153], v[88:89] op_sel_hi:[0,1]
	s_nop 0
	v_pk_mul_f32 v[4:5], v[152:153], v[86:87] op_sel_hi:[0,1]
	v_pk_fma_f32 v[6:7], v[4:5], v[194:195], v[216:217]
	v_pk_fma_f32 v[4:5], v[8:9], v[196:197], v[214:215]
	global_store_dwordx4 v[12:13], v[4:7], off offset:576
	v_pk_mul_f32 v[8:9], v[150:151], v[104:105] op_sel_hi:[0,1]
	v_add_u32_e32 v214, 0xffffff90, v190
	v_or_b32_e32 v4, 48, v190
	v_ashrrev_i32_e32 v5, 31, v4
	v_lshlrev_b64 v[4:5], 13, v[4:5]
	v_lshl_add_u64 v[4:5], s[76:77], 0, v[4:5]
	v_lshl_add_u64 v[6:7], v[4:5], 0, v[2:3]
	v_pk_mul_f32 v[2:3], v[150:151], v[106:107] op_sel_hi:[0,1]
	v_pk_fma_f32 v[4:5], v[2:3], v[206:207], v[224:225]
	v_pk_fma_f32 v[2:3], v[8:9], v[208:209], v[222:223]
	global_store_dwordx4 v[6:7], v[2:5], off
	v_pk_mul_f32 v[8:9], v[150:151], v[100:101] op_sel_hi:[0,1]
	v_ashrrev_i32_e32 v215, 31, v214
	v_pk_mul_f32 v[2:3], v[150:151], v[102:103] op_sel_hi:[0,1]
	v_pk_fma_f32 v[4:5], v[2:3], v[202:203], v[232:233]
	v_pk_fma_f32 v[2:3], v[8:9], v[204:205], v[230:231]
	global_store_dwordx4 v[6:7], v[2:5], off offset:64
	v_pk_mul_f32 v[8:9], v[150:151], v[84:85] op_sel_hi:[0,1]
	v_lshlrev_b64 v[214:215], 13, v[214:215]
	v_pk_mul_f32 v[2:3], v[150:151], v[82:83] op_sel_hi:[0,1]
	v_pk_fma_f32 v[4:5], v[2:3], v[198:199], v[238:239]
	v_pk_fma_f32 v[2:3], v[8:9], v[200:201], v[236:237]
	global_store_dwordx4 v[6:7], v[2:5], off offset:512
	v_pk_mul_f32 v[8:9], v[150:151], v[80:81] op_sel_hi:[0,1]
	v_lshl_add_u64 v[218:219], v[212:213], 0, v[214:215]
	v_pk_mul_f32 v[2:3], v[150:151], v[78:79] op_sel_hi:[0,1]
	v_pk_fma_f32 v[4:5], v[2:3], v[194:195], v[242:243]
	v_pk_fma_f32 v[2:3], v[8:9], v[196:197], v[240:241]
	global_store_dwordx4 v[6:7], v[2:5], off offset:576
	v_pk_mul_f32 v[240:241], v[148:149], v[70:71] op_sel_hi:[0,1]
	v_pk_mul_f32 v[242:243], v[148:149], v[72:73] op_sel_hi:[0,1]
	v_add_u32_e32 v2, 0xffffff80, v190
	v_ashrrev_i32_e32 v3, 31, v2
	v_lshlrev_b64 v[2:3], 13, v[2:3]
	v_lshl_add_u64 v[2:3], v[212:213], 0, v[2:3]
	global_load_dwordx4 v[10:13], v[2:3], off
	global_load_dwordx4 v[176:179], v[2:3], off offset:64
	global_load_dwordx4 v[6:9], v[2:3], off offset:512
	s_nop 0
	global_load_dwordx4 v[2:5], v[2:3], off offset:576
	s_nop 0
	global_load_dwordx4 v[214:217], v[218:219], off
	global_load_dwordx4 v[222:225], v[218:219], off offset:64
	global_load_dwordx4 v[230:233], v[218:219], off offset:512
	global_load_dwordx4 v[236:239], v[218:219], off offset:576
	v_lshl_add_u64 v[218:219], v[210:211], 0, s[8:9]
	s_mov_b64 s[8:9], 0x120000
	s_waitcnt vmcnt(0)
	v_pk_fma_f32 v[12:13], v[240:241], v[206:207], v[12:13]
	v_add_co_u32_e32 v240, vcc, s3, v210
	v_pk_fma_f32 v[10:11], v[242:243], v[208:209], v[10:11]
	s_nop 0
	v_addc_co_u32_e32 v241, vcc, 0, v211, vcc
	global_store_dwordx4 v[240:241], v[10:13], off
	v_pk_mul_f32 v[240:241], v[148:149], v[64:65] op_sel_hi:[0,1]
	s_mov_b32 s3, 0x120000
	v_pk_mul_f32 v[10:11], v[148:149], v[62:63] op_sel_hi:[0,1]
	v_pk_fma_f32 v[12:13], v[10:11], v[202:203], v[178:179]
	v_pk_fma_f32 v[10:11], v[240:241], v[204:205], v[176:177]
	global_store_dwordx4 v[218:219], v[10:13], off offset:64
	s_nop 1
	v_pk_mul_f32 v[10:11], v[148:149], v[74:75] op_sel_hi:[0,1]
	v_pk_mul_f32 v[12:13], v[148:149], v[76:77] op_sel_hi:[0,1]
	v_pk_fma_f32 v[8:9], v[10:11], v[198:199], v[8:9]
	v_pk_fma_f32 v[6:7], v[12:13], v[200:201], v[6:7]
	global_store_dwordx4 v[218:219], v[6:9], off offset:512
	s_nop 1
	v_pk_mul_f32 v[6:7], v[148:149], v[66:67] op_sel_hi:[0,1]
	v_pk_mul_f32 v[8:9], v[148:149], v[68:69] op_sel_hi:[0,1]
	v_pk_fma_f32 v[4:5], v[6:7], v[194:195], v[4:5]
	v_pk_fma_f32 v[2:3], v[8:9], v[196:197], v[2:3]
	global_store_dwordx4 v[218:219], v[2:5], off offset:576
	v_pk_mul_f32 v[8:9], v[146:147], v[54:55] op_sel_hi:[0,1]
	v_lshl_add_u64 v[6:7], v[210:211], 0, s[8:9]
	v_pk_mul_f32 v[2:3], v[146:147], v[56:57] op_sel_hi:[0,1]
	v_pk_fma_f32 v[4:5], v[2:3], v[206:207], v[216:217]
	v_pk_fma_f32 v[2:3], v[8:9], v[208:209], v[214:215]
	v_add_co_u32_e32 v8, vcc, s3, v210
	s_mov_b32 s3, 0x140000
	s_nop 0
	v_addc_co_u32_e32 v9, vcc, 0, v211, vcc
	global_store_dwordx4 v[8:9], v[2:5], off
	v_pk_mul_f32 v[8:9], v[146:147], v[50:51] op_sel_hi:[0,1]
	v_pk_mul_f32 v[218:219], v[144:145], v[46:47] op_sel_hi:[0,1]
	v_pk_mul_f32 v[2:3], v[146:147], v[52:53] op_sel_hi:[0,1]
	v_pk_fma_f32 v[4:5], v[2:3], v[202:203], v[224:225]
	v_pk_fma_f32 v[2:3], v[8:9], v[204:205], v[222:223]
	global_store_dwordx4 v[6:7], v[2:5], off offset:64
	v_pk_mul_f32 v[8:9], v[146:147], v[60:61] op_sel_hi:[0,1]
	s_mov_b64 s[8:9], 0x140000
	v_pk_mul_f32 v[2:3], v[146:147], v[58:59] op_sel_hi:[0,1]
	v_pk_fma_f32 v[4:5], v[2:3], v[198:199], v[232:233]
	v_pk_fma_f32 v[2:3], v[8:9], v[200:201], v[230:231]
	global_store_dwordx4 v[6:7], v[2:5], off offset:512
	v_pk_mul_f32 v[8:9], v[146:147], v[32:33] op_sel_hi:[0,1]
	s_nop 0
	v_pk_mul_f32 v[2:3], v[146:147], v[30:31] op_sel_hi:[0,1]
	v_pk_fma_f32 v[4:5], v[2:3], v[194:195], v[238:239]
	v_pk_fma_f32 v[2:3], v[8:9], v[196:197], v[236:237]
	global_store_dwordx4 v[6:7], v[2:5], off offset:576
	s_nop 1
	v_add_u32_e32 v2, 0xffffffa0, v190
	v_ashrrev_i32_e32 v3, 31, v2
	v_lshlrev_b64 v[2:3], 13, v[2:3]
	v_lshl_add_u64 v[2:3], v[212:213], 0, v[2:3]
	global_load_dwordx4 v[176:179], v[2:3], off
	global_load_dwordx4 v[214:217], v[2:3], off offset:64
	global_load_dwordx4 v[10:13], v[2:3], off offset:512
	global_load_dwordx4 v[6:9], v[2:3], off offset:576
	v_add_u32_e32 v2, 0xffffffb0, v190
	v_ashrrev_i32_e32 v3, 31, v2
	v_lshlrev_b64 v[2:3], 13, v[2:3]
	v_lshl_add_u64 v[2:3], v[212:213], 0, v[2:3]
	global_load_dwordx4 v[222:225], v[2:3], off
	global_load_dwordx4 v[230:233], v[2:3], off offset:64
	global_load_dwordx4 v[236:239], v[2:3], off offset:512
	s_nop 0
	global_load_dwordx4 v[2:5], v[2:3], off offset:576
	v_pk_mul_f32 v[212:213], v[144:145], v[48:49] op_sel_hi:[0,1]
	v_lshl_add_u64 v[190:191], v[210:211], 0, s[8:9]
	s_mov_b64 s[8:9], 0x160000
	s_waitcnt vmcnt(0)
	v_pk_fma_f32 v[178:179], v[212:213], v[206:207], v[178:179]
	v_add_co_u32_e32 v212, vcc, s3, v210
	v_pk_fma_f32 v[176:177], v[218:219], v[208:209], v[176:177]
	s_nop 0
	v_addc_co_u32_e32 v213, vcc, 0, v211, vcc
	global_store_dwordx4 v[212:213], v[176:179], off
	v_pk_mul_f32 v[212:213], v[144:145], v[42:43] op_sel_hi:[0,1]
	s_mov_b32 s3, 0x160000
	v_pk_mul_f32 v[176:177], v[144:145], v[44:45] op_sel_hi:[0,1]
	v_pk_fma_f32 v[178:179], v[176:177], v[202:203], v[216:217]
	v_pk_fma_f32 v[176:177], v[212:213], v[204:205], v[214:215]
	global_store_dwordx4 v[190:191], v[176:179], off offset:64
	s_nop 1
	v_pk_mul_f32 v[176:177], v[144:145], v[26:27] op_sel_hi:[0,1]
	v_pk_mul_f32 v[178:179], v[144:145], v[28:29] op_sel_hi:[0,1]
	v_pk_fma_f32 v[12:13], v[176:177], v[198:199], v[12:13]
	v_pk_fma_f32 v[10:11], v[178:179], v[200:201], v[10:11]
	global_store_dwordx4 v[190:191], v[10:13], off offset:512
	s_nop 1
	v_pk_mul_f32 v[10:11], v[144:145], v[22:23] op_sel_hi:[0,1]
	v_pk_mul_f32 v[12:13], v[144:145], v[24:25] op_sel_hi:[0,1]
	v_pk_fma_f32 v[8:9], v[10:11], v[194:195], v[8:9]
	v_pk_fma_f32 v[6:7], v[12:13], v[196:197], v[6:7]
	global_store_dwordx4 v[190:191], v[6:9], off offset:576
	v_pk_mul_f32 v[12:13], v[142:143], v[38:39] op_sel_hi:[0,1]
	v_lshl_add_u64 v[10:11], v[210:211], 0, s[8:9]
	v_pk_mul_f32 v[6:7], v[142:143], v[40:41] op_sel_hi:[0,1]
	v_pk_fma_f32 v[8:9], v[6:7], v[206:207], v[224:225]
	v_pk_fma_f32 v[6:7], v[12:13], v[208:209], v[222:223]
	v_add_co_u32_e32 v12, vcc, s3, v210
	s_nop 1
	v_addc_co_u32_e32 v13, vcc, 0, v211, vcc
	global_store_dwordx4 v[12:13], v[6:9], off
	v_pk_mul_f32 v[12:13], v[142:143], v[34:35] op_sel_hi:[0,1]
	s_nop 0
	v_pk_mul_f32 v[6:7], v[142:143], v[36:37] op_sel_hi:[0,1]
	v_pk_fma_f32 v[8:9], v[6:7], v[202:203], v[232:233]
	v_pk_fma_f32 v[6:7], v[12:13], v[204:205], v[230:231]
	global_store_dwordx4 v[10:11], v[6:9], off offset:64
	v_pk_mul_f32 v[12:13], v[142:143], v[20:21] op_sel_hi:[0,1]
	s_nop 0
	v_pk_mul_f32 v[6:7], v[142:143], v[18:19] op_sel_hi:[0,1]
	v_pk_fma_f32 v[8:9], v[6:7], v[198:199], v[238:239]
	v_pk_fma_f32 v[6:7], v[12:13], v[200:201], v[236:237]
	global_store_dwordx4 v[10:11], v[6:9], off offset:512
	s_nop 1
	v_pk_mul_f32 v[6:7], v[142:143], v[14:15] op_sel_hi:[0,1]
	v_pk_mul_f32 v[8:9], v[142:143], v[16:17] op_sel_hi:[0,1]
	v_pk_fma_f32 v[4:5], v[6:7], v[194:195], v[4:5]
	v_pk_fma_f32 v[2:3], v[8:9], v[196:197], v[2:3]
	global_store_dwordx4 v[10:11], v[2:5], off offset:576
